# baseline (speedup 1.0000x reference)
.LBB7_27:
	s_add_u32 s30, s28, 0xfffd0080
	s_addc_u32 s31, s29, -1
	s_cmp_eq_u32 s73, 8
	s_cselect_b32 s35, s9, s31
	s_cselect_b32 s34, s8, s30
	s_cselect_b32 s31, s1, s72
	s_cselect_b32 s30, s0, s71
	s_add_i32 m0, s43, 0xc000
	ds_read_b128 v[158:161], v171
	ds_read_b128 v[176:179], v171 offset:1024
	ds_read_b128 v[180:183], v171 offset:2048
	ds_read_b128 v[184:187], v171 offset:3072
	ds_read_b128 v[188:191], v171 offset:4096
	ds_read_b128 v[192:195], v171 offset:5120
	ds_read_b128 v[196:199], v171 offset:6144
	ds_read_b128 v[200:203], v171 offset:7168
	global_load_lds_dwordx4 v152, s[28:29]
	s_add_i32 m0, s43, 0xe000
	s_nop 0
	global_load_lds_dwordx4 v154, s[28:29]
	s_waitcnt lgkmcnt(8)
	s_barrier
	s_waitcnt lgkmcnt(0)
	v_mfma_f32_16x16x32_f16 v[124:127], v[128:131], v[158:161], v[124:127]
	v_mfma_f32_16x16x32_f16 v[120:123], v[136:139], v[158:161], v[120:123]
	v_mfma_f32_16x16x32_f16 v[108:111], v[128:131], v[180:183], v[108:111]
	v_mfma_f32_16x16x32_f16 v[104:107], v[136:139], v[180:183], v[104:107]
	v_mfma_f32_16x16x32_f16 v[96:99], v[128:131], v[188:191], v[96:99]
	v_mfma_f32_16x16x32_f16 v[88:91], v[136:139], v[188:191], v[88:91]
	v_mfma_f32_16x16x32_f16 v[80:83], v[128:131], v[196:199], v[80:83]
	v_mfma_f32_16x16x32_f16 v[72:75], v[136:139], v[196:199], v[72:75]
	v_mfma_f32_16x16x32_f16 v[124:127], v[132:135], v[176:179], v[124:127]
	v_mfma_f32_16x16x32_f16 v[120:123], v[140:143], v[176:179], v[120:123]
	v_mfma_f32_16x16x32_f16 v[108:111], v[132:135], v[184:187], v[108:111]
	v_mfma_f32_16x16x32_f16 v[104:107], v[140:143], v[184:187], v[104:107]
	v_mfma_f32_16x16x32_f16 v[96:99], v[132:135], v[192:195], v[96:99]
	v_mfma_f32_16x16x32_f16 v[88:91], v[140:143], v[192:195], v[88:91]
	v_mfma_f32_16x16x32_f16 v[80:83], v[132:135], v[200:203], v[80:83]
	v_mfma_f32_16x16x32_f16 v[72:75], v[140:143], v[200:203], v[72:75]
	s_barrier
	s_add_i32 s74, s65, s42
	s_add_u32 s78, s30, 0x80
	s_addc_u32 s79, s31, 0
	s_mov_b32 m0, s74
	ds_read_b128 v[204:207], v172
	ds_read_b128 v[208:211], v172 offset:1024
	ds_read_b128 v[212:215], v172 offset:2048
	ds_read_b128 v[216:219], v172 offset:3072
	global_load_lds_dwordx4 v146, s[30:31]
	s_add_i32 m0, s74, 0x2000
	s_nop 0
	global_load_lds_dwordx4 v150, s[30:31]
	s_barrier
	s_waitcnt lgkmcnt(0)
	v_mfma_f32_16x16x32_f16 v[116:119], v[204:207], v[158:161], v[116:119]
	v_mfma_f32_16x16x32_f16 v[112:115], v[212:215], v[158:161], v[112:115]
	v_mfma_f32_16x16x32_f16 v[100:103], v[204:207], v[180:183], v[100:103]
	v_mfma_f32_16x16x32_f16 v[92:95], v[212:215], v[180:183], v[92:95]
	v_mfma_f32_16x16x32_f16 v[84:87], v[204:207], v[188:191], v[84:87]
	v_mfma_f32_16x16x32_f16 v[76:79], v[212:215], v[188:191], v[76:79]
	v_mfma_f32_16x16x32_f16 v[68:71], v[204:207], v[196:199], v[68:71]
	v_mfma_f32_16x16x32_f16 v[64:67], v[212:215], v[196:199], v[64:67]
	v_mfma_f32_16x16x32_f16 v[116:119], v[208:211], v[176:179], v[116:119]
	v_mfma_f32_16x16x32_f16 v[112:115], v[216:219], v[176:179], v[112:115]
	v_mfma_f32_16x16x32_f16 v[100:103], v[208:211], v[184:187], v[100:103]
	v_mfma_f32_16x16x32_f16 v[92:95], v[216:219], v[184:187], v[92:95]
	v_mfma_f32_16x16x32_f16 v[84:87], v[208:211], v[192:195], v[84:87]
	v_mfma_f32_16x16x32_f16 v[76:79], v[216:219], v[192:195], v[76:79]
	v_mfma_f32_16x16x32_f16 v[68:71], v[208:211], v[200:203], v[68:71]
	v_mfma_f32_16x16x32_f16 v[64:67], v[216:219], v[200:203], v[64:67]
	s_barrier
	s_mov_b32 m0, s43
	s_add_u32 s80, s34, 0x80
	s_addc_u32 s81, s35, 0
	ds_read_b128 v[158:161], v171 offset:16384
	ds_read_b128 v[176:179], v171 offset:17408
	ds_read_b128 v[180:183], v171 offset:18432
	ds_read_b128 v[184:187], v171 offset:19456
	ds_read_b128 v[188:191], v171 offset:20480
	ds_read_b128 v[192:195], v171 offset:21504
	ds_read_b128 v[196:199], v171 offset:22528
	ds_read_b128 v[200:203], v171 offset:23552
	global_load_lds_dwordx4 v144, s[34:35]
	s_mov_b32 m0, s44
	s_nop 0
	global_load_lds_dwordx4 v148, s[34:35]
	s_waitcnt vmcnt(10)
	s_barrier
	s_waitcnt lgkmcnt(0)
	v_mfma_f32_16x16x32_f16 v[60:63], v[128:131], v[158:161], v[60:63]
	v_mfma_f32_16x16x32_f16 v[56:59], v[136:139], v[158:161], v[56:59]
	v_mfma_f32_16x16x32_f16 v[48:51], v[128:131], v[180:183], v[48:51]
	v_mfma_f32_16x16x32_f16 v[40:43], v[136:139], v[180:183], v[40:43]
	v_mfma_f32_16x16x32_f16 v[32:35], v[128:131], v[188:191], v[32:35]
	v_mfma_f32_16x16x32_f16 v[24:27], v[136:139], v[188:191], v[24:27]
	v_mfma_f32_16x16x32_f16 v[16:19], v[128:131], v[196:199], v[16:19]
	v_mfma_f32_16x16x32_f16 v[8:11], v[136:139], v[196:199], v[8:11]
	v_mfma_f32_16x16x32_f16 v[60:63], v[132:135], v[176:179], v[60:63]
	v_mfma_f32_16x16x32_f16 v[56:59], v[140:143], v[176:179], v[56:59]
	v_mfma_f32_16x16x32_f16 v[48:51], v[132:135], v[184:187], v[48:51]
	v_mfma_f32_16x16x32_f16 v[40:43], v[140:143], v[184:187], v[40:43]
	v_mfma_f32_16x16x32_f16 v[32:35], v[132:135], v[192:195], v[32:35]
	v_mfma_f32_16x16x32_f16 v[24:27], v[140:143], v[192:195], v[24:27]
	v_mfma_f32_16x16x32_f16 v[16:19], v[132:135], v[200:203], v[16:19]
	v_mfma_f32_16x16x32_f16 v[8:11], v[140:143], v[200:203], v[8:11]
	s_barrier
	s_add_u32 s74, s30, 0xc000
	s_addc_u32 s75, s31, 0
	s_add_i32 s76, s66, s42
	s_mov_b32 m0, s76
	s_nop 0
	global_load_lds_dwordx4 v146, s[74:75]
	s_add_i32 m0, s76, 0x2000
	s_nop 0
	global_load_lds_dwordx4 v150, s[74:75]
	s_add_i32 s74, 0, 0x18000
	v_add_u32_e32 v140, s74, v166
	ds_read_b128 v[128:131], v140
	ds_read_b128 v[132:135], v140 offset:1024
	ds_read_b128 v[136:139], v140 offset:2048
	ds_read_b128 v[140:143], v140 offset:3072
	s_waitcnt vmcnt(6)
	s_barrier
	v_mfma_f32_16x16x32_f16 v[52:55], v[204:207], v[158:161], v[52:55]
	v_mfma_f32_16x16x32_f16 v[44:47], v[212:215], v[158:161], v[44:47]
	v_mfma_f32_16x16x32_f16 v[36:39], v[204:207], v[180:183], v[36:39]
	v_mfma_f32_16x16x32_f16 v[28:31], v[212:215], v[180:183], v[28:31]
	v_mfma_f32_16x16x32_f16 v[20:23], v[204:207], v[188:191], v[20:23]
	v_mfma_f32_16x16x32_f16 v[12:15], v[212:215], v[188:191], v[12:15]
	v_mfma_f32_16x16x32_f16 v[4:7], v[204:207], v[196:199], v[4:7]
	v_mfma_f32_16x16x32_f16 v[0:3], v[212:215], v[196:199], v[0:3]
	v_mfma_f32_16x16x32_f16 v[52:55], v[208:211], v[176:179], v[52:55]
	v_mfma_f32_16x16x32_f16 v[44:47], v[216:219], v[176:179], v[44:47]
	v_mfma_f32_16x16x32_f16 v[36:39], v[208:211], v[184:187], v[36:39]
	v_mfma_f32_16x16x32_f16 v[28:31], v[216:219], v[184:187], v[28:31]
	v_mfma_f32_16x16x32_f16 v[20:23], v[208:211], v[192:195], v[20:23]
	v_mfma_f32_16x16x32_f16 v[12:15], v[216:219], v[192:195], v[12:15]
	v_mfma_f32_16x16x32_f16 v[4:7], v[208:211], v[200:203], v[4:7]
	v_mfma_f32_16x16x32_f16 v[0:3], v[216:219], v[200:203], v[0:3]
	s_barrier
	s_add_u32 s34, s34, 0x30000
	s_addc_u32 s35, s35, 0
	s_mov_b32 m0, s45
	ds_read_b128 v[158:161], v171 offset:32768
	ds_read_b128 v[176:179], v171 offset:33792
	ds_read_b128 v[180:183], v171 offset:34816
	ds_read_b128 v[184:187], v171 offset:35840
	ds_read_b128 v[188:191], v171 offset:36864
	ds_read_b128 v[192:195], v171 offset:37888
	ds_read_b128 v[196:199], v171 offset:38912
	ds_read_b128 v[200:203], v171 offset:39936
	global_load_lds_dwordx4 v144, s[34:35]
	s_mov_b32 m0, s46
	s_nop 0
	global_load_lds_dwordx4 v148, s[34:35]
	s_waitcnt lgkmcnt(8)
	s_barrier
	s_waitcnt lgkmcnt(0)
	v_mfma_f32_16x16x32_f16 v[124:127], v[128:131], v[158:161], v[124:127]
	v_mfma_f32_16x16x32_f16 v[120:123], v[136:139], v[158:161], v[120:123]
	v_mfma_f32_16x16x32_f16 v[108:111], v[128:131], v[180:183], v[108:111]
	v_mfma_f32_16x16x32_f16 v[104:107], v[136:139], v[180:183], v[104:107]
	v_mfma_f32_16x16x32_f16 v[96:99], v[128:131], v[188:191], v[96:99]
	v_mfma_f32_16x16x32_f16 v[88:91], v[136:139], v[188:191], v[88:91]
	v_mfma_f32_16x16x32_f16 v[80:83], v[128:131], v[196:199], v[80:83]
	v_mfma_f32_16x16x32_f16 v[72:75], v[136:139], v[196:199], v[72:75]
	v_mfma_f32_16x16x32_f16 v[124:127], v[132:135], v[176:179], v[124:127]
	v_mfma_f32_16x16x32_f16 v[120:123], v[140:143], v[176:179], v[120:123]
	v_mfma_f32_16x16x32_f16 v[108:111], v[132:135], v[184:187], v[108:111]
	v_mfma_f32_16x16x32_f16 v[104:107], v[140:143], v[184:187], v[104:107]
	v_mfma_f32_16x16x32_f16 v[96:99], v[132:135], v[192:195], v[96:99]
	v_mfma_f32_16x16x32_f16 v[88:91], v[140:143], v[192:195], v[88:91]
	v_mfma_f32_16x16x32_f16 v[80:83], v[132:135], v[200:203], v[80:83]
	v_mfma_f32_16x16x32_f16 v[72:75], v[140:143], v[200:203], v[72:75]
	s_barrier
	s_add_i32 s34, 0, 0x1c000
	s_add_i32 s35, s74, s42
	v_add_u32_e32 v175, s34, v166
	s_mov_b32 m0, s35
	ds_read_b128 v[204:207], v175
	ds_read_b128 v[208:211], v175 offset:1024
	ds_read_b128 v[212:215], v175 offset:2048
	ds_read_b128 v[216:219], v175 offset:3072
	global_load_lds_dwordx4 v146, s[78:79]
	s_add_i32 m0, s35, 0x2000
	s_nop 0
	global_load_lds_dwordx4 v150, s[78:79]
	s_barrier
	s_waitcnt lgkmcnt(0)
	v_mfma_f32_16x16x32_f16 v[116:119], v[204:207], v[158:161], v[116:119]
	v_mfma_f32_16x16x32_f16 v[112:115], v[212:215], v[158:161], v[112:115]
	v_mfma_f32_16x16x32_f16 v[100:103], v[204:207], v[180:183], v[100:103]
	v_mfma_f32_16x16x32_f16 v[92:95], v[212:215], v[180:183], v[92:95]
	v_mfma_f32_16x16x32_f16 v[84:87], v[204:207], v[188:191], v[84:87]
	v_mfma_f32_16x16x32_f16 v[76:79], v[212:215], v[188:191], v[76:79]
	v_mfma_f32_16x16x32_f16 v[68:71], v[204:207], v[196:199], v[68:71]
	v_mfma_f32_16x16x32_f16 v[64:67], v[212:215], v[196:199], v[64:67]
	v_mfma_f32_16x16x32_f16 v[116:119], v[208:211], v[176:179], v[116:119]
	v_mfma_f32_16x16x32_f16 v[112:115], v[216:219], v[176:179], v[112:115]
	v_mfma_f32_16x16x32_f16 v[100:103], v[208:211], v[184:187], v[100:103]
	v_mfma_f32_16x16x32_f16 v[92:95], v[216:219], v[184:187], v[92:95]
	v_mfma_f32_16x16x32_f16 v[84:87], v[208:211], v[192:195], v[84:87]
	v_mfma_f32_16x16x32_f16 v[76:79], v[216:219], v[192:195], v[76:79]
	v_mfma_f32_16x16x32_f16 v[68:71], v[208:211], v[200:203], v[68:71]
	v_mfma_f32_16x16x32_f16 v[64:67], v[216:219], v[200:203], v[64:67]
	s_barrier
	s_mov_b32 m0, s49
	ds_read_b128 v[158:161], v171 offset:49152
	ds_read_b128 v[176:179], v171 offset:50176
	ds_read_b128 v[180:183], v171 offset:51200
	ds_read_b128 v[184:187], v171 offset:52224
	ds_read_b128 v[188:191], v171 offset:53248
	ds_read_b128 v[192:195], v171 offset:54272
	ds_read_b128 v[196:199], v171 offset:55296
	ds_read_b128 v[200:203], v171 offset:56320
	global_load_lds_dwordx4 v144, s[80:81]
	s_mov_b32 m0, s50
	s_nop 0
	global_load_lds_dwordx4 v148, s[80:81]
	s_waitcnt vmcnt(10)
	s_barrier
	s_waitcnt lgkmcnt(0)
	v_mfma_f32_16x16x32_f16 v[60:63], v[128:131], v[158:161], v[60:63]
	v_mfma_f32_16x16x32_f16 v[56:59], v[136:139], v[158:161], v[56:59]
	v_mfma_f32_16x16x32_f16 v[48:51], v[128:131], v[180:183], v[48:51]
	v_mfma_f32_16x16x32_f16 v[40:43], v[136:139], v[180:183], v[40:43]
	v_mfma_f32_16x16x32_f16 v[32:35], v[128:131], v[188:191], v[32:35]
	v_mfma_f32_16x16x32_f16 v[24:27], v[136:139], v[188:191], v[24:27]
	v_mfma_f32_16x16x32_f16 v[16:19], v[128:131], v[196:199], v[16:19]
	v_mfma_f32_16x16x32_f16 v[8:11], v[136:139], v[196:199], v[8:11]
	v_mfma_f32_16x16x32_f16 v[60:63], v[132:135], v[176:179], v[60:63]
	v_mfma_f32_16x16x32_f16 v[56:59], v[140:143], v[176:179], v[56:59]
	v_mfma_f32_16x16x32_f16 v[48:51], v[132:135], v[184:187], v[48:51]
	v_mfma_f32_16x16x32_f16 v[40:43], v[140:143], v[184:187], v[40:43]
	v_mfma_f32_16x16x32_f16 v[32:35], v[132:135], v[192:195], v[32:35]
	v_mfma_f32_16x16x32_f16 v[24:27], v[140:143], v[192:195], v[24:27]
	v_mfma_f32_16x16x32_f16 v[16:19], v[132:135], v[200:203], v[16:19]
	v_mfma_f32_16x16x32_f16 v[8:11], v[140:143], v[200:203], v[8:11]
	s_barrier
	s_add_u32 s30, s30, 0xc080
	s_addc_u32 s31, s31, 0
	s_add_i32 s34, s34, s42
	s_mov_b32 m0, s34
	s_nop 0
	global_load_lds_dwordx4 v146, s[30:31]
	s_add_i32 m0, s34, 0x2000
	s_nop 0
	global_load_lds_dwordx4 v150, s[30:31]
	ds_read_b128 v[128:131], v170
	ds_read_b128 v[132:135], v170 offset:1024
	ds_read_b128 v[136:139], v170 offset:2048
	ds_read_b128 v[140:143], v170 offset:3072
	s_waitcnt vmcnt(6)
	s_barrier
	v_mfma_f32_16x16x32_f16 v[52:55], v[204:207], v[158:161], v[52:55]
	v_mfma_f32_16x16x32_f16 v[44:47], v[212:215], v[158:161], v[44:47]
	v_mfma_f32_16x16x32_f16 v[36:39], v[204:207], v[180:183], v[36:39]
	v_mfma_f32_16x16x32_f16 v[28:31], v[212:215], v[180:183], v[28:31]
	v_mfma_f32_16x16x32_f16 v[20:23], v[204:207], v[188:191], v[20:23]
	v_mfma_f32_16x16x32_f16 v[12:15], v[212:215], v[188:191], v[12:15]
	v_mfma_f32_16x16x32_f16 v[4:7], v[204:207], v[196:199], v[4:7]
	v_mfma_f32_16x16x32_f16 v[0:3], v[212:215], v[196:199], v[0:3]
	v_mfma_f32_16x16x32_f16 v[52:55], v[208:211], v[176:179], v[52:55]
	v_mfma_f32_16x16x32_f16 v[44:47], v[216:219], v[176:179], v[44:47]
	v_mfma_f32_16x16x32_f16 v[36:39], v[208:211], v[184:187], v[36:39]
	v_mfma_f32_16x16x32_f16 v[28:31], v[216:219], v[184:187], v[28:31]
	v_mfma_f32_16x16x32_f16 v[20:23], v[208:211], v[192:195], v[20:23]
	v_mfma_f32_16x16x32_f16 v[12:15], v[216:219], v[192:195], v[12:15]
	v_mfma_f32_16x16x32_f16 v[4:7], v[208:211], v[200:203], v[4:7]
	v_mfma_f32_16x16x32_f16 v[0:3], v[216:219], v[200:203], v[0:3]
	s_barrier
	s_add_i32 s73, s73, 2
	s_add_u32 s28, s28, 0x100
	s_addc_u32 s29, s29, 0
	s_add_u32 s71, s71, 0x100
	s_addc_u32 s72, s72, 0
	s_cmp_gt_u32 s73, 9
	s_cbranch_scc0 .LBB7_27
	s_lshl_b32 s28, s70, 8
	s_add_i32 s28, s28, s48
	s_lshl_b32 s29, s67, 8
	s_or_b32 s29, s29, s51
	s_waitcnt vmcnt(6)
	v_pk_fma_f32 v[126:127], v[126:127], v[226:227], v[236:237] op_sel_hi:[1,0,1]
	v_pk_fma_f32 v[124:125], v[124:125], v[226:227], v[234:235] op_sel_hi:[1,0,1]
	v_pk_fma_f32 v[186:187], v[122:123], v[226:227], v[240:241] op_sel_hi:[1,0,1]
	v_pk_fma_f32 v[122:123], v[120:121], v[226:227], v[238:239] op_sel_hi:[1,0,1]
	v_cvt_pk_f16_f32 v120, v124, v125
	v_cvt_pk_f16_f32 v121, v126, v127
	v_cvt_pk_f16_f32 v122, v122, v123
	v_cvt_pk_f16_f32 v123, v186, v187
	ds_write_b128 v173, v[120:123]
	v_pk_fma_f32 v[118:119], v[118:119], v[226:227], v[244:245] op_sel_hi:[1,0,1]
	v_pk_fma_f32 v[116:117], v[116:117], v[226:227], v[242:243] op_sel_hi:[1,0,1]
	v_pk_fma_f32 v[120:121], v[114:115], v[226:227], v[248:249] op_sel_hi:[1,0,1]
	v_pk_fma_f32 v[114:115], v[112:113], v[226:227], v[246:247] op_sel_hi:[1,0,1]
	v_cvt_pk_f16_f32 v112, v116, v117
	v_cvt_pk_f16_f32 v113, v118, v119
	v_cvt_pk_f16_f32 v114, v114, v115
	v_cvt_pk_f16_f32 v115, v120, v121
	ds_write_b128 v173, v[112:115] offset:64
	v_or_b32_e32 v116, s28, v167
	ds_read_b128 v[112:115], v174
	v_mul_lo_u32 v116, v116, s10
	v_add_u32_e32 v120, s29, v116
	v_lshlrev_b32_e32 v121, 1, v120
	v_add_u32_e32 v122, v121, v168
	ds_read_b128 v[116:119], v174 offset:1152
	s_waitcnt lgkmcnt(0)
	buffer_store_dwordx4 v[112:115], v122, s[20:23], 0 offen sc1
	v_pk_fma_f32 v[110:111], v[110:111], v[226:227], v[236:237] op_sel:[0,1,0]
	v_pk_fma_f32 v[108:109], v[108:109], v[226:227], v[234:235] op_sel:[0,1,0]
	v_pk_fma_f32 v[112:113], v[106:107], v[226:227], v[240:241] op_sel:[0,1,0]
	v_pk_fma_f32 v[106:107], v[104:105], v[226:227], v[238:239] op_sel:[0,1,0]
	v_cvt_pk_f16_f32 v104, v108, v109
	v_cvt_pk_f16_f32 v105, v110, v111
	v_cvt_pk_f16_f32 v106, v106, v107
	v_cvt_pk_f16_f32 v107, v112, v113
	ds_write_b128 v173, v[104:107]
	v_pk_fma_f32 v[102:103], v[102:103], v[226:227], v[244:245] op_sel:[0,1,0]
	v_pk_fma_f32 v[100:101], v[100:101], v[226:227], v[242:243] op_sel:[0,1,0]
	v_pk_fma_f32 v[104:105], v[94:95], v[226:227], v[248:249] op_sel:[0,1,0]
	v_pk_fma_f32 v[94:95], v[92:93], v[226:227], v[246:247] op_sel:[0,1,0]
	v_cvt_pk_f16_f32 v92, v100, v101
	v_cvt_pk_f16_f32 v93, v102, v103
	v_cvt_pk_f16_f32 v94, v94, v95
	v_cvt_pk_f16_f32 v95, v104, v105
	ds_write_b128 v173, v[92:95] offset:64
	ds_read_b128 v[92:95], v174
	ds_read_b128 v[100:103], v174 offset:1152
	v_add_u32_e32 v104, s55, v121
	v_add_u32_e32 v114, v121, v169
	v_add_u32_e32 v105, v104, v168
	buffer_store_dwordx4 v[116:119], v114, s[20:23], 0 offen sc1
	s_waitcnt lgkmcnt(1)
	buffer_store_dwordx4 v[92:95], v105, s[20:23], 0 offen sc1
	v_pk_fma_f32 v[86:87], v[86:87], v[228:229], v[244:245] op_sel_hi:[1,0,1]
	v_pk_fma_f32 v[84:85], v[84:85], v[228:229], v[242:243] op_sel_hi:[1,0,1]
	v_pk_fma_f32 v[92:93], v[98:99], v[228:229], v[236:237] op_sel_hi:[1,0,1]
	v_pk_fma_f32 v[94:95], v[96:97], v[228:229], v[234:235] op_sel_hi:[1,0,1]
	v_pk_fma_f32 v[96:97], v[90:91], v[228:229], v[240:241] op_sel_hi:[1,0,1]
	v_pk_fma_f32 v[90:91], v[88:89], v[228:229], v[238:239] op_sel_hi:[1,0,1]
	v_cvt_pk_f16_f32 v88, v94, v95
	v_cvt_pk_f16_f32 v89, v92, v93
	v_cvt_pk_f16_f32 v90, v90, v91
	v_cvt_pk_f16_f32 v91, v96, v97
	ds_write_b128 v173, v[88:91]
	v_pk_fma_f32 v[88:89], v[78:79], v[228:229], v[248:249] op_sel_hi:[1,0,1]
	v_pk_fma_f32 v[78:79], v[76:77], v[228:229], v[246:247] op_sel_hi:[1,0,1]
	v_cvt_pk_f16_f32 v76, v84, v85
	v_cvt_pk_f16_f32 v77, v86, v87
	v_cvt_pk_f16_f32 v78, v78, v79
	v_cvt_pk_f16_f32 v79, v88, v89
	ds_write_b128 v173, v[76:79] offset:64
	ds_read_b128 v[76:79], v174
	ds_read_b128 v[84:87], v174 offset:1152
	v_add_u32_e32 v88, s55, v104
	v_add_u32_e32 v105, v104, v169
	v_add_u32_e32 v89, v88, v168
	s_waitcnt lgkmcnt(4)
	buffer_store_dwordx4 v[100:103], v105, s[20:23], 0 offen sc1
	s_waitcnt lgkmcnt(1)
	buffer_store_dwordx4 v[76:79], v89, s[20:23], 0 offen sc1
	v_pk_fma_f32 v[70:71], v[70:71], v[228:229], v[244:245] op_sel:[0,1,0]
	v_pk_fma_f32 v[68:69], v[68:69], v[228:229], v[242:243] op_sel:[0,1,0]
	v_add_u32_e32 v76, v88, v169
	s_waitcnt lgkmcnt(0)
	buffer_store_dwordx4 v[84:87], v76, s[20:23], 0 offen sc1
	v_pk_fma_f32 v[76:77], v[82:83], v[228:229], v[236:237] op_sel:[0,1,0]
	v_pk_fma_f32 v[78:79], v[80:81], v[228:229], v[234:235] op_sel:[0,1,0]
	v_pk_fma_f32 v[80:81], v[74:75], v[228:229], v[240:241] op_sel:[0,1,0]
	v_pk_fma_f32 v[74:75], v[72:73], v[228:229], v[238:239] op_sel:[0,1,0]
	v_cvt_pk_f16_f32 v72, v78, v79
	v_cvt_pk_f16_f32 v73, v76, v77
	v_cvt_pk_f16_f32 v74, v74, v75
	v_cvt_pk_f16_f32 v75, v80, v81
	ds_write_b128 v173, v[72:75]
	v_pk_fma_f32 v[72:73], v[66:67], v[228:229], v[248:249] op_sel:[0,1,0]
	v_pk_fma_f32 v[66:67], v[64:65], v[228:229], v[246:247] op_sel:[0,1,0]
	v_cvt_pk_f16_f32 v64, v68, v69
	v_cvt_pk_f16_f32 v65, v70, v71
	v_cvt_pk_f16_f32 v66, v66, v67
	v_cvt_pk_f16_f32 v67, v72, v73
	ds_write_b128 v173, v[64:67] offset:64
	ds_read_b128 v[64:67], v174
	ds_read_b128 v[68:71], v174 offset:1152
	v_add_u32_e32 v72, s56, v120
	v_lshlrev_b32_e32 v73, 1, v72
	v_add_u32_e32 v74, v73, v168
	s_waitcnt lgkmcnt(1)
	buffer_store_dwordx4 v[64:67], v74, s[20:23], 0 offen sc1
	v_pk_fma_f32 v[62:63], v[62:63], v[230:231], v[236:237] op_sel_hi:[1,0,1]
	v_pk_fma_f32 v[60:61], v[60:61], v[230:231], v[234:235] op_sel_hi:[1,0,1]
	v_pk_fma_f32 v[64:65], v[58:59], v[230:231], v[240:241] op_sel_hi:[1,0,1]
	v_pk_fma_f32 v[58:59], v[56:57], v[230:231], v[238:239] op_sel_hi:[1,0,1]
	v_cvt_pk_f16_f32 v56, v60, v61
	v_cvt_pk_f16_f32 v57, v62, v63
	v_cvt_pk_f16_f32 v58, v58, v59
	v_cvt_pk_f16_f32 v59, v64, v65
	ds_write_b128 v173, v[56:59]
	v_pk_fma_f32 v[54:55], v[54:55], v[230:231], v[244:245] op_sel_hi:[1,0,1]
	v_pk_fma_f32 v[52:53], v[52:53], v[230:231], v[242:243] op_sel_hi:[1,0,1]
	v_pk_fma_f32 v[56:57], v[46:47], v[230:231], v[248:249] op_sel_hi:[1,0,1]
	v_pk_fma_f32 v[46:47], v[44:45], v[230:231], v[246:247] op_sel_hi:[1,0,1]
	v_cvt_pk_f16_f32 v44, v52, v53
	v_cvt_pk_f16_f32 v45, v54, v55
	v_cvt_pk_f16_f32 v46, v46, v47
	v_cvt_pk_f16_f32 v47, v56, v57
	ds_write_b128 v173, v[44:47] offset:64
	ds_read_b128 v[44:47], v174
	ds_read_b128 v[52:55], v174 offset:1152
	v_add_u32_e32 v56, s62, v88
	v_add_u32_e32 v66, v73, v169
	v_add_u32_e32 v57, v56, v168
	s_waitcnt lgkmcnt(4)
	buffer_store_dwordx4 v[68:71], v66, s[20:23], 0 offen sc1
	s_waitcnt lgkmcnt(1)
	buffer_store_dwordx4 v[44:47], v57, s[20:23], 0 offen sc1
	v_pk_fma_f32 v[38:39], v[38:39], v[230:231], v[244:245] op_sel:[0,1,0]
	v_pk_fma_f32 v[36:37], v[36:37], v[230:231], v[242:243] op_sel:[0,1,0]
	v_add_u32_e32 v44, v56, v169
	s_waitcnt lgkmcnt(0)
	buffer_store_dwordx4 v[52:55], v44, s[20:23], 0 offen sc1
	v_pk_fma_f32 v[44:45], v[50:51], v[230:231], v[236:237] op_sel:[0,1,0]
	v_pk_fma_f32 v[46:47], v[48:49], v[230:231], v[234:235] op_sel:[0,1,0]
	v_pk_fma_f32 v[48:49], v[42:43], v[230:231], v[240:241] op_sel:[0,1,0]
	v_pk_fma_f32 v[42:43], v[40:41], v[230:231], v[238:239] op_sel:[0,1,0]
	v_cvt_pk_f16_f32 v40, v46, v47
	v_cvt_pk_f16_f32 v41, v44, v45
	v_cvt_pk_f16_f32 v42, v42, v43
	v_cvt_pk_f16_f32 v43, v48, v49
	ds_write_b128 v173, v[40:43]
	v_pk_fma_f32 v[40:41], v[30:31], v[230:231], v[248:249] op_sel:[0,1,0]
	v_pk_fma_f32 v[30:31], v[28:29], v[230:231], v[246:247] op_sel:[0,1,0]
	v_cvt_pk_f16_f32 v28, v36, v37
	v_cvt_pk_f16_f32 v29, v38, v39
	v_cvt_pk_f16_f32 v30, v30, v31
	v_cvt_pk_f16_f32 v31, v40, v41
	ds_write_b128 v173, v[28:31] offset:64
	ds_read_b128 v[28:31], v174
	ds_read_b128 v[36:39], v174 offset:1152
	v_add_u32_e32 v40, s63, v72
	v_lshlrev_b32_e32 v41, 1, v40
	v_add_u32_e32 v42, v41, v168
	s_waitcnt lgkmcnt(1)
	buffer_store_dwordx4 v[28:31], v42, s[20:23], 0 offen sc1
	v_pk_fma_f32 v[22:23], v[22:23], v[232:233], v[244:245] op_sel_hi:[1,0,1]
	v_pk_fma_f32 v[20:21], v[20:21], v[232:233], v[242:243] op_sel_hi:[1,0,1]
	v_add_u32_e32 v28, v41, v169
	s_waitcnt lgkmcnt(0)
	buffer_store_dwordx4 v[36:39], v28, s[20:23], 0 offen sc1
	v_pk_fma_f32 v[28:29], v[34:35], v[232:233], v[236:237] op_sel_hi:[1,0,1]
	v_pk_fma_f32 v[30:31], v[32:33], v[232:233], v[234:235] op_sel_hi:[1,0,1]
	v_pk_fma_f32 v[32:33], v[26:27], v[232:233], v[240:241] op_sel_hi:[1,0,1]
	v_pk_fma_f32 v[26:27], v[24:25], v[232:233], v[238:239] op_sel_hi:[1,0,1]
	v_cvt_pk_f16_f32 v24, v30, v31
	v_cvt_pk_f16_f32 v25, v28, v29
	v_cvt_pk_f16_f32 v26, v26, v27
	v_cvt_pk_f16_f32 v27, v32, v33
	ds_write_b128 v173, v[24:27]
	v_pk_fma_f32 v[24:25], v[14:15], v[232:233], v[248:249] op_sel_hi:[1,0,1]
	v_pk_fma_f32 v[14:15], v[12:13], v[232:233], v[246:247] op_sel_hi:[1,0,1]
	v_cvt_pk_f16_f32 v12, v20, v21
	v_cvt_pk_f16_f32 v13, v22, v23
	v_cvt_pk_f16_f32 v14, v14, v15
	v_cvt_pk_f16_f32 v15, v24, v25
	ds_write_b128 v173, v[12:15] offset:64
	ds_read_b128 v[12:15], v174
	ds_read_b128 v[20:23], v174 offset:1152
	v_add_u32_e32 v24, s64, v40
	v_lshlrev_b32_e32 v25, 1, v24
	v_add_u32_e32 v26, v25, v168
	s_waitcnt lgkmcnt(1)
	buffer_store_dwordx4 v[12:15], v26, s[20:23], 0 offen sc1
	v_pk_fma_f32 v[6:7], v[6:7], v[232:233], v[244:245] op_sel:[0,1,0]
	v_pk_fma_f32 v[4:5], v[4:5], v[232:233], v[242:243] op_sel:[0,1,0]
	v_pk_fma_f32 v[12:13], v[18:19], v[232:233], v[236:237] op_sel:[0,1,0]
	v_pk_fma_f32 v[14:15], v[16:17], v[232:233], v[234:235] op_sel:[0,1,0]
	v_pk_fma_f32 v[16:17], v[10:11], v[232:233], v[240:241] op_sel:[0,1,0]
	v_pk_fma_f32 v[10:11], v[8:9], v[232:233], v[238:239] op_sel:[0,1,0]
	v_cvt_pk_f16_f32 v8, v14, v15
	v_cvt_pk_f16_f32 v9, v12, v13
	v_cvt_pk_f16_f32 v10, v10, v11
	v_cvt_pk_f16_f32 v11, v16, v17
	ds_write_b128 v173, v[8:11]
	v_pk_fma_f32 v[8:9], v[2:3], v[232:233], v[248:249] op_sel:[0,1,0]
	v_pk_fma_f32 v[2:3], v[0:1], v[232:233], v[246:247] op_sel:[0,1,0]
	v_cvt_pk_f16_f32 v0, v4, v5
	v_cvt_pk_f16_f32 v1, v6, v7
	v_cvt_pk_f16_f32 v2, v2, v3
	v_cvt_pk_f16_f32 v3, v8, v9
	ds_write_b128 v173, v[0:3] offset:64
	ds_read_b128 v[0:3], v174
	ds_read_b128 v[4:7], v174 offset:1152
	v_add_lshl_u32 v8, v24, s64, 1
	v_add_u32_e32 v25, v25, v169
	v_add_u32_e32 v9, v8, v168
	s_waitcnt lgkmcnt(4)
	buffer_store_dwordx4 v[20:23], v25, s[20:23], 0 offen sc1
	s_waitcnt lgkmcnt(1)
	buffer_store_dwordx4 v[0:3], v9, s[20:23], 0 offen sc1
	s_mov_b32 s67, s68
	s_mov_b32 s70, s69
	v_add_u32_e32 v0, v8, v169
	s_mov_b64 s[30:31], s[0:1]
	s_mov_b64 s[28:29], s[8:9]
	s_mov_b64 vcc, s[6:7]
	s_waitcnt lgkmcnt(0)
	buffer_store_dwordx4 v[4:7], v0, s[20:23], 0 offen sc1
	s_cbranch_vccz .LBB7_12
	s_waitcnt vmcnt(0)
	s_cmpk_gt_u32 s36, 0xff
	s_cbranch_scc1 .LBB7_31
	s_barrier

.LBB8_27:
	s_add_u32 s40, s38, 0xfffd0080
	s_addc_u32 s41, s39, -1
	s_cmp_eq_u32 s87, 8
	s_cselect_b32 s43, s9, s41
	s_cselect_b32 s42, s8, s40
	s_cselect_b32 s41, s1, s86
	s_cselect_b32 s40, s0, s85
	s_add_i32 m0, s51, 0xc000
	ds_read_b128 v[136:139], v232
	ds_read_b128 v[148:151], v232 offset:1024
	ds_read_b128 v[152:155], v232 offset:2048
	ds_read_b128 v[156:159], v232 offset:3072
	ds_read_b128 v[160:163], v232 offset:4096
	ds_read_b128 v[164:167], v232 offset:5120
	ds_read_b128 v[168:171], v232 offset:6144
	ds_read_b128 v[172:175], v232 offset:7168
	global_load_lds_dwordx4 v184, s[38:39]
	s_add_i32 m0, s51, 0xe000
	s_nop 0
	global_load_lds_dwordx4 v186, s[38:39]
	s_waitcnt lgkmcnt(8)
	s_barrier
	s_waitcnt lgkmcnt(0)
	v_mfma_f32_16x16x32_f16 v[144:147], v[72:75], v[136:139], v[144:147]
	v_mfma_f32_16x16x32_f16 v[140:143], v[88:91], v[136:139], v[140:143]
	v_mfma_f32_16x16x32_f16 v[124:127], v[72:75], v[152:155], v[124:127]
	v_mfma_f32_16x16x32_f16 v[120:123], v[88:91], v[152:155], v[120:123]
	v_mfma_f32_16x16x32_f16 v[108:111], v[72:75], v[160:163], v[108:111]
	v_mfma_f32_16x16x32_f16 v[104:107], v[88:91], v[160:163], v[104:107]
	v_mfma_f32_16x16x32_f16 v[84:87], v[72:75], v[168:171], v[84:87]
	v_mfma_f32_16x16x32_f16 v[76:79], v[88:91], v[168:171], v[76:79]
	v_mfma_f32_16x16x32_f16 v[144:147], v[80:83], v[148:151], v[144:147]
	v_mfma_f32_16x16x32_f16 v[140:143], v[92:95], v[148:151], v[140:143]
	v_mfma_f32_16x16x32_f16 v[124:127], v[80:83], v[156:159], v[124:127]
	v_mfma_f32_16x16x32_f16 v[120:123], v[92:95], v[156:159], v[120:123]
	v_mfma_f32_16x16x32_f16 v[108:111], v[80:83], v[164:167], v[108:111]
	v_mfma_f32_16x16x32_f16 v[104:107], v[92:95], v[164:167], v[104:107]
	v_mfma_f32_16x16x32_f16 v[84:87], v[80:83], v[172:175], v[84:87]
	v_mfma_f32_16x16x32_f16 v[76:79], v[92:95], v[172:175], v[76:79]
	s_barrier
	s_add_i32 s88, s70, s50
	s_add_u32 s92, s40, 0x80
	s_addc_u32 s93, s41, 0
	s_mov_b32 m0, s88
	ds_read_b128 v[190:193], v233
	ds_read_b128 v[194:197], v233 offset:1024
	ds_read_b128 v[198:201], v233 offset:2048
	ds_read_b128 v[202:205], v233 offset:3072
	global_load_lds_dwordx4 v178, s[40:41]
	s_add_i32 m0, s88, 0x2000
	s_nop 0
	global_load_lds_dwordx4 v182, s[40:41]
	s_barrier
	s_waitcnt lgkmcnt(0)
	v_mfma_f32_16x16x32_f16 v[132:135], v[190:193], v[136:139], v[132:135]
	v_mfma_f32_16x16x32_f16 v[128:131], v[198:201], v[136:139], v[128:131]
	v_mfma_f32_16x16x32_f16 v[116:119], v[190:193], v[152:155], v[116:119]
	v_mfma_f32_16x16x32_f16 v[112:115], v[198:201], v[152:155], v[112:115]
	v_mfma_f32_16x16x32_f16 v[100:103], v[190:193], v[160:163], v[100:103]
	v_mfma_f32_16x16x32_f16 v[96:99], v[198:201], v[160:163], v[96:99]
	v_mfma_f32_16x16x32_f16 v[68:71], v[190:193], v[168:171], v[68:71]
	v_mfma_f32_16x16x32_f16 v[64:67], v[198:201], v[168:171], v[64:67]
	v_mfma_f32_16x16x32_f16 v[132:135], v[194:197], v[148:151], v[132:135]
	v_mfma_f32_16x16x32_f16 v[128:131], v[202:205], v[148:151], v[128:131]
	v_mfma_f32_16x16x32_f16 v[116:119], v[194:197], v[156:159], v[116:119]
	v_mfma_f32_16x16x32_f16 v[112:115], v[202:205], v[156:159], v[112:115]
	v_mfma_f32_16x16x32_f16 v[100:103], v[194:197], v[164:167], v[100:103]
	v_mfma_f32_16x16x32_f16 v[96:99], v[202:205], v[164:167], v[96:99]
	v_mfma_f32_16x16x32_f16 v[68:71], v[194:197], v[172:175], v[68:71]
	v_mfma_f32_16x16x32_f16 v[64:67], v[202:205], v[172:175], v[64:67]
	s_barrier
	s_mov_b32 m0, s51
	s_add_u32 s94, s42, 0x80
	s_addc_u32 s95, s43, 0
	ds_read_b128 v[136:139], v232 offset:16384
	ds_read_b128 v[148:151], v232 offset:17408
	ds_read_b128 v[152:155], v232 offset:18432
	ds_read_b128 v[156:159], v232 offset:19456
	ds_read_b128 v[160:163], v232 offset:20480
	ds_read_b128 v[164:167], v232 offset:21504
	ds_read_b128 v[168:171], v232 offset:22528
	ds_read_b128 v[172:175], v232 offset:23552
	global_load_lds_dwordx4 v176, s[42:43]
	s_mov_b32 m0, s52
	s_nop 0
	global_load_lds_dwordx4 v180, s[42:43]
	s_waitcnt vmcnt(10)
	s_barrier
	s_waitcnt lgkmcnt(0)
	v_mfma_f32_16x16x32_f16 v[60:63], v[72:75], v[136:139], v[60:63]
	v_mfma_f32_16x16x32_f16 v[56:59], v[88:91], v[136:139], v[56:59]
	v_mfma_f32_16x16x32_f16 v[44:47], v[72:75], v[152:155], v[44:47]
	v_mfma_f32_16x16x32_f16 v[40:43], v[88:91], v[152:155], v[40:43]
	v_mfma_f32_16x16x32_f16 v[28:31], v[72:75], v[160:163], v[28:31]
	v_mfma_f32_16x16x32_f16 v[24:27], v[88:91], v[160:163], v[24:27]
	v_mfma_f32_16x16x32_f16 v[12:15], v[72:75], v[168:171], v[12:15]
	v_mfma_f32_16x16x32_f16 v[8:11], v[88:91], v[168:171], v[8:11]
	v_mfma_f32_16x16x32_f16 v[60:63], v[80:83], v[148:151], v[60:63]
	v_mfma_f32_16x16x32_f16 v[56:59], v[92:95], v[148:151], v[56:59]
	v_mfma_f32_16x16x32_f16 v[44:47], v[80:83], v[156:159], v[44:47]
	v_mfma_f32_16x16x32_f16 v[40:43], v[92:95], v[156:159], v[40:43]
	v_mfma_f32_16x16x32_f16 v[28:31], v[80:83], v[164:167], v[28:31]
	v_mfma_f32_16x16x32_f16 v[24:27], v[92:95], v[164:167], v[24:27]
	v_mfma_f32_16x16x32_f16 v[12:15], v[80:83], v[172:175], v[12:15]
	v_mfma_f32_16x16x32_f16 v[8:11], v[92:95], v[172:175], v[8:11]
	s_barrier
	s_add_u32 s88, s40, 0xc000
	s_addc_u32 s89, s41, 0
	s_add_i32 s90, s71, s50
	s_mov_b32 m0, s90
	s_nop 0
	global_load_lds_dwordx4 v178, s[88:89]
	s_add_i32 m0, s90, 0x2000
	s_nop 0
	global_load_lds_dwordx4 v182, s[88:89]
	s_add_i32 s88, 0, 0x18000
	v_add_u32_e32 v92, s88, v228
	ds_read_b128 v[72:75], v92
	ds_read_b128 v[80:83], v92 offset:1024
	ds_read_b128 v[88:91], v92 offset:2048
	ds_read_b128 v[92:95], v92 offset:3072
	s_waitcnt vmcnt(6)
	s_barrier
	v_mfma_f32_16x16x32_f16 v[52:55], v[190:193], v[136:139], v[52:55]
	v_mfma_f32_16x16x32_f16 v[48:51], v[198:201], v[136:139], v[48:51]
	v_mfma_f32_16x16x32_f16 v[36:39], v[190:193], v[152:155], v[36:39]
	v_mfma_f32_16x16x32_f16 v[32:35], v[198:201], v[152:155], v[32:35]
	v_mfma_f32_16x16x32_f16 v[20:23], v[190:193], v[160:163], v[20:23]
	v_mfma_f32_16x16x32_f16 v[16:19], v[198:201], v[160:163], v[16:19]
	v_mfma_f32_16x16x32_f16 v[4:7], v[190:193], v[168:171], v[4:7]
	v_mfma_f32_16x16x32_f16 v[0:3], v[198:201], v[168:171], v[0:3]
	v_mfma_f32_16x16x32_f16 v[52:55], v[194:197], v[148:151], v[52:55]
	v_mfma_f32_16x16x32_f16 v[48:51], v[202:205], v[148:151], v[48:51]
	v_mfma_f32_16x16x32_f16 v[36:39], v[194:197], v[156:159], v[36:39]
	v_mfma_f32_16x16x32_f16 v[32:35], v[202:205], v[156:159], v[32:35]
	v_mfma_f32_16x16x32_f16 v[20:23], v[194:197], v[164:167], v[20:23]
	v_mfma_f32_16x16x32_f16 v[16:19], v[202:205], v[164:167], v[16:19]
	v_mfma_f32_16x16x32_f16 v[4:7], v[194:197], v[172:175], v[4:7]
	v_mfma_f32_16x16x32_f16 v[0:3], v[202:205], v[172:175], v[0:3]
	s_barrier
	s_add_u32 s42, s42, 0x30000
	s_addc_u32 s43, s43, 0
	s_mov_b32 m0, s53
	ds_read_b128 v[136:139], v232 offset:32768
	ds_read_b128 v[148:151], v232 offset:33792
	ds_read_b128 v[152:155], v232 offset:34816
	ds_read_b128 v[156:159], v232 offset:35840
	ds_read_b128 v[160:163], v232 offset:36864
	ds_read_b128 v[164:167], v232 offset:37888
	ds_read_b128 v[168:171], v232 offset:38912
	ds_read_b128 v[172:175], v232 offset:39936
	global_load_lds_dwordx4 v176, s[42:43]
	s_mov_b32 m0, s54
	s_nop 0
	global_load_lds_dwordx4 v180, s[42:43]
	s_waitcnt lgkmcnt(8)
	s_barrier
	s_waitcnt lgkmcnt(0)
	v_mfma_f32_16x16x32_f16 v[144:147], v[72:75], v[136:139], v[144:147]
	v_mfma_f32_16x16x32_f16 v[140:143], v[88:91], v[136:139], v[140:143]
	v_mfma_f32_16x16x32_f16 v[124:127], v[72:75], v[152:155], v[124:127]
	v_mfma_f32_16x16x32_f16 v[120:123], v[88:91], v[152:155], v[120:123]
	v_mfma_f32_16x16x32_f16 v[108:111], v[72:75], v[160:163], v[108:111]
	v_mfma_f32_16x16x32_f16 v[104:107], v[88:91], v[160:163], v[104:107]
	v_mfma_f32_16x16x32_f16 v[84:87], v[72:75], v[168:171], v[84:87]
	v_mfma_f32_16x16x32_f16 v[76:79], v[88:91], v[168:171], v[76:79]
	v_mfma_f32_16x16x32_f16 v[144:147], v[80:83], v[148:151], v[144:147]
	v_mfma_f32_16x16x32_f16 v[140:143], v[92:95], v[148:151], v[140:143]
	v_mfma_f32_16x16x32_f16 v[124:127], v[80:83], v[156:159], v[124:127]
	v_mfma_f32_16x16x32_f16 v[120:123], v[92:95], v[156:159], v[120:123]
	v_mfma_f32_16x16x32_f16 v[108:111], v[80:83], v[164:167], v[108:111]
	v_mfma_f32_16x16x32_f16 v[104:107], v[92:95], v[164:167], v[104:107]
	v_mfma_f32_16x16x32_f16 v[84:87], v[80:83], v[172:175], v[84:87]
	v_mfma_f32_16x16x32_f16 v[76:79], v[92:95], v[172:175], v[76:79]
	s_barrier
	s_add_i32 s42, 0, 0x1c000
	s_add_i32 s43, s88, s50
	v_add_u32_e32 v202, s42, v228
	s_mov_b32 m0, s43
	ds_read_b128 v[190:193], v202
	ds_read_b128 v[194:197], v202 offset:1024
	ds_read_b128 v[198:201], v202 offset:2048
	ds_read_b128 v[202:205], v202 offset:3072
	global_load_lds_dwordx4 v178, s[92:93]
	s_add_i32 m0, s43, 0x2000
	s_nop 0
	global_load_lds_dwordx4 v182, s[92:93]
	s_barrier
	s_waitcnt lgkmcnt(0)
	v_mfma_f32_16x16x32_f16 v[132:135], v[190:193], v[136:139], v[132:135]
	v_mfma_f32_16x16x32_f16 v[128:131], v[198:201], v[136:139], v[128:131]
	v_mfma_f32_16x16x32_f16 v[116:119], v[190:193], v[152:155], v[116:119]
	v_mfma_f32_16x16x32_f16 v[112:115], v[198:201], v[152:155], v[112:115]
	v_mfma_f32_16x16x32_f16 v[100:103], v[190:193], v[160:163], v[100:103]
	v_mfma_f32_16x16x32_f16 v[96:99], v[198:201], v[160:163], v[96:99]
	v_mfma_f32_16x16x32_f16 v[68:71], v[190:193], v[168:171], v[68:71]
	v_mfma_f32_16x16x32_f16 v[64:67], v[198:201], v[168:171], v[64:67]
	v_mfma_f32_16x16x32_f16 v[132:135], v[194:197], v[148:151], v[132:135]
	v_mfma_f32_16x16x32_f16 v[128:131], v[202:205], v[148:151], v[128:131]
	v_mfma_f32_16x16x32_f16 v[116:119], v[194:197], v[156:159], v[116:119]
	v_mfma_f32_16x16x32_f16 v[112:115], v[202:205], v[156:159], v[112:115]
	v_mfma_f32_16x16x32_f16 v[100:103], v[194:197], v[164:167], v[100:103]
	v_mfma_f32_16x16x32_f16 v[96:99], v[202:205], v[164:167], v[96:99]
	v_mfma_f32_16x16x32_f16 v[68:71], v[194:197], v[172:175], v[68:71]
	v_mfma_f32_16x16x32_f16 v[64:67], v[202:205], v[172:175], v[64:67]
	s_barrier
	s_mov_b32 m0, s59
	ds_read_b128 v[136:139], v232 offset:49152
	ds_read_b128 v[148:151], v232 offset:50176
	ds_read_b128 v[152:155], v232 offset:51200
	ds_read_b128 v[156:159], v232 offset:52224
	ds_read_b128 v[160:163], v232 offset:53248
	ds_read_b128 v[164:167], v232 offset:54272
	ds_read_b128 v[168:171], v232 offset:55296
	ds_read_b128 v[172:175], v232 offset:56320
	global_load_lds_dwordx4 v176, s[94:95]
	s_mov_b32 m0, s60
	s_nop 0
	global_load_lds_dwordx4 v180, s[94:95]
	s_waitcnt vmcnt(10)
	s_barrier
	s_waitcnt lgkmcnt(0)
	v_mfma_f32_16x16x32_f16 v[60:63], v[72:75], v[136:139], v[60:63]
	v_mfma_f32_16x16x32_f16 v[56:59], v[88:91], v[136:139], v[56:59]
	v_mfma_f32_16x16x32_f16 v[44:47], v[72:75], v[152:155], v[44:47]
	v_mfma_f32_16x16x32_f16 v[40:43], v[88:91], v[152:155], v[40:43]
	v_mfma_f32_16x16x32_f16 v[28:31], v[72:75], v[160:163], v[28:31]
	v_mfma_f32_16x16x32_f16 v[24:27], v[88:91], v[160:163], v[24:27]
	v_mfma_f32_16x16x32_f16 v[12:15], v[72:75], v[168:171], v[12:15]
	v_mfma_f32_16x16x32_f16 v[8:11], v[88:91], v[168:171], v[8:11]
	v_mfma_f32_16x16x32_f16 v[60:63], v[80:83], v[148:151], v[60:63]
	v_mfma_f32_16x16x32_f16 v[56:59], v[92:95], v[148:151], v[56:59]
	v_mfma_f32_16x16x32_f16 v[44:47], v[80:83], v[156:159], v[44:47]
	v_mfma_f32_16x16x32_f16 v[40:43], v[92:95], v[156:159], v[40:43]
	v_mfma_f32_16x16x32_f16 v[28:31], v[80:83], v[164:167], v[28:31]
	v_mfma_f32_16x16x32_f16 v[24:27], v[92:95], v[164:167], v[24:27]
	v_mfma_f32_16x16x32_f16 v[12:15], v[80:83], v[172:175], v[12:15]
	v_mfma_f32_16x16x32_f16 v[8:11], v[92:95], v[172:175], v[8:11]
	s_barrier
	s_add_u32 s40, s40, 0xc080
	s_addc_u32 s41, s41, 0
	s_add_i32 s42, s42, s50
	s_mov_b32 m0, s42
	s_nop 0
	global_load_lds_dwordx4 v178, s[40:41]
	s_add_i32 m0, s42, 0x2000
	s_nop 0
	global_load_lds_dwordx4 v182, s[40:41]
	ds_read_b128 v[72:75], v231
	ds_read_b128 v[80:83], v231 offset:1024
	ds_read_b128 v[88:91], v231 offset:2048
	ds_read_b128 v[92:95], v231 offset:3072
	s_waitcnt vmcnt(6)
	s_barrier
	v_mfma_f32_16x16x32_f16 v[52:55], v[190:193], v[136:139], v[52:55]
	v_mfma_f32_16x16x32_f16 v[48:51], v[198:201], v[136:139], v[48:51]
	v_mfma_f32_16x16x32_f16 v[36:39], v[190:193], v[152:155], v[36:39]
	v_mfma_f32_16x16x32_f16 v[32:35], v[198:201], v[152:155], v[32:35]
	v_mfma_f32_16x16x32_f16 v[20:23], v[190:193], v[160:163], v[20:23]
	v_mfma_f32_16x16x32_f16 v[16:19], v[198:201], v[160:163], v[16:19]
	v_mfma_f32_16x16x32_f16 v[4:7], v[190:193], v[168:171], v[4:7]
	v_mfma_f32_16x16x32_f16 v[0:3], v[198:201], v[168:171], v[0:3]
	v_mfma_f32_16x16x32_f16 v[52:55], v[194:197], v[148:151], v[52:55]
	v_mfma_f32_16x16x32_f16 v[48:51], v[202:205], v[148:151], v[48:51]
	v_mfma_f32_16x16x32_f16 v[36:39], v[194:197], v[156:159], v[36:39]
	v_mfma_f32_16x16x32_f16 v[32:35], v[202:205], v[156:159], v[32:35]
	v_mfma_f32_16x16x32_f16 v[20:23], v[194:197], v[164:167], v[20:23]
	v_mfma_f32_16x16x32_f16 v[16:19], v[202:205], v[164:167], v[16:19]
	v_mfma_f32_16x16x32_f16 v[4:7], v[194:197], v[172:175], v[4:7]
	v_mfma_f32_16x16x32_f16 v[0:3], v[202:205], v[172:175], v[0:3]
	s_barrier
	s_add_i32 s87, s87, 2
	s_add_u32 s38, s38, 0x100
	s_addc_u32 s39, s39, 0
	s_add_u32 s85, s85, 0x100
	s_addc_u32 s86, s86, 0
	s_cmp_gt_u32 s87, 9
	s_cbranch_scc0 .LBB8_27
	s_lshl_b32 s92, s84, 8
	s_add_i32 s92, s92, s58
	s_lshl_b32 s93, s83, 8
	s_or_b32 s93, s93, s61
	v_lshlrev_b32_e32 v237, 2, v226
	s_lshl_b32 s96, s93, 2
	s_add_u32 s94, s16, s96
	s_addc_u32 s95, s17, 0
	global_load_dwordx4 v[72:75], v237, s[94:95] offset:0
	global_load_dwordx4 v[80:83], v237, s[94:95] offset:16
	global_load_dwordx4 v[88:91], v237, s[94:95] offset:128
	global_load_dwordx4 v[92:95], v237, s[94:95] offset:144
	s_add_u32 s94, s18, s96
	s_addc_u32 s95, s19, 0
	global_load_dwordx4 v[136:139], v237, s[94:95] offset:0
	global_load_dwordx4 v[148:151], v237, s[94:95] offset:16
	global_load_dwordx4 v[152:155], v237, s[94:95] offset:128
	global_load_dwordx4 v[156:159], v237, s[94:95] offset:144
	s_add_u32 s94, s14, s96
	s_addc_u32 s95, s15, 0
	global_load_dwordx4 v[160:163], v237, s[94:95] offset:0
	global_load_dwordx4 v[164:167], v237, s[94:95] offset:16
	global_load_dwordx4 v[168:171], v237, s[94:95] offset:128
	global_load_dwordx4 v[172:175], v237, s[94:95] offset:144
	v_lshlrev_b32_e32 v190, 3, v227
	s_lshl_b32 s96, s92, 3
	s_add_u32 s94, s12, s96
	s_addc_u32 s95, s13, 0
	global_load_dwordx2 v[238:239], v190, s[94:95] offset:0
	global_load_dwordx2 v[192:193], v190, s[94:95] offset:128
	global_load_dwordx2 v[194:195], v190, s[94:95] offset:256
	global_load_dwordx2 v[196:197], v190, s[94:95] offset:384
	global_load_dwordx2 v[198:199], v190, s[94:95] offset:1024
	global_load_dwordx2 v[200:201], v190, s[94:95] offset:1152
	global_load_dwordx2 v[202:203], v190, s[94:95] offset:1280
	global_load_dwordx2 v[204:205], v190, s[94:95] offset:1408
	v_mul_u32_u24_e32 v191, 0x600, v227
	v_lshl_add_u32 v191, v226, 1, v191
	s_mul_i32 s96, s92, 0x600
	s_lshl_b32 s97, s93, 1
	s_add_u32 s96, s96, s97
	s_add_u32 s98, s10, s96
	s_addc_u32 s99, s11, 0
	s_add_u32 s94, s98, 0x0
	s_addc_u32 s95, s99, 0
	global_load_dwordx4 v[208:211], v191, s[94:95] offset:0 nt
	global_load_dwordx4 v[212:215], v191, s[94:95] offset:64 nt
	s_add_u32 s94, s98, 0x6000
	s_addc_u32 s95, s99, 0
	global_load_dwordx4 v[216:219], v191, s[94:95] offset:0 nt
	global_load_dwordx4 v[220:223], v191, s[94:95] offset:64 nt
	v_add_u32_e32 v224, s92, v229
	v_mul_u32_u24_e32 v224, 0x600, v224
	s_lshl_b32 s97, s93, 1
	v_add3_u32 v224, v224, v230, s97
	s_lshl_b32 s96, s83, 2
	s_lshr_b32 s97, s61, 6
	s_add_u32 s96, s96, s97
	s_lshl_b32 s96, s96, 19
	s_lshl_b32 s97, s92, 3
	s_add_u32 s96, s96, s97
	s_add_u32 s100, s28, s96
	s_addc_u32 s101, s29, 0
	s_waitcnt vmcnt(19)
	v_pk_add_f32 v[72:73], v[72:73], v[136:137]
	v_pk_add_f32 v[74:75], v[74:75], v[138:139]
	s_waitcnt vmcnt(18)
	v_pk_add_f32 v[80:81], v[80:81], v[148:149]
	v_pk_add_f32 v[82:83], v[82:83], v[150:151]
	s_waitcnt vmcnt(17)
	v_pk_add_f32 v[88:89], v[88:89], v[152:153]
	v_pk_add_f32 v[90:91], v[90:91], v[154:155]
	s_waitcnt vmcnt(16)
	v_pk_add_f32 v[92:93], v[92:93], v[156:157]
	v_pk_add_f32 v[94:95], v[94:95], v[158:159]
	v_pk_add_f32 v[144:145], v[144:145], v[72:73]
	v_pk_add_f32 v[146:147], v[146:147], v[74:75]
	v_pk_add_f32 v[124:125], v[124:125], v[72:73]
	v_pk_add_f32 v[126:127], v[126:127], v[74:75]
	v_pk_add_f32 v[108:109], v[108:109], v[72:73]
	v_pk_add_f32 v[110:111], v[110:111], v[74:75]
	v_pk_add_f32 v[84:85], v[84:85], v[72:73]
	v_pk_add_f32 v[86:87], v[86:87], v[74:75]
	v_pk_add_f32 v[60:61], v[60:61], v[72:73]
	v_pk_add_f32 v[62:63], v[62:63], v[74:75]
	v_pk_add_f32 v[44:45], v[44:45], v[72:73]
	v_pk_add_f32 v[46:47], v[46:47], v[74:75]
	v_pk_add_f32 v[28:29], v[28:29], v[72:73]
	v_pk_add_f32 v[30:31], v[30:31], v[74:75]
	v_pk_add_f32 v[12:13], v[12:13], v[72:73]
	v_pk_add_f32 v[14:15], v[14:15], v[74:75]
	v_pk_add_f32 v[140:141], v[140:141], v[80:81]
	v_pk_add_f32 v[142:143], v[142:143], v[82:83]
	v_pk_add_f32 v[120:121], v[120:121], v[80:81]
	v_pk_add_f32 v[122:123], v[122:123], v[82:83]
	v_pk_add_f32 v[104:105], v[104:105], v[80:81]
	v_pk_add_f32 v[106:107], v[106:107], v[82:83]
	v_pk_add_f32 v[76:77], v[76:77], v[80:81]
	v_pk_add_f32 v[78:79], v[78:79], v[82:83]
	v_pk_add_f32 v[56:57], v[56:57], v[80:81]
	v_pk_add_f32 v[58:59], v[58:59], v[82:83]
	v_pk_add_f32 v[40:41], v[40:41], v[80:81]
	v_pk_add_f32 v[42:43], v[42:43], v[82:83]
	v_pk_add_f32 v[24:25], v[24:25], v[80:81]
	v_pk_add_f32 v[26:27], v[26:27], v[82:83]
	v_pk_add_f32 v[8:9], v[8:9], v[80:81]
	v_pk_add_f32 v[10:11], v[10:11], v[82:83]
	v_pk_add_f32 v[132:133], v[132:133], v[88:89]
	v_pk_add_f32 v[134:135], v[134:135], v[90:91]
	v_pk_add_f32 v[116:117], v[116:117], v[88:89]
	v_pk_add_f32 v[118:119], v[118:119], v[90:91]
	v_pk_add_f32 v[100:101], v[100:101], v[88:89]
	v_pk_add_f32 v[102:103], v[102:103], v[90:91]
	v_pk_add_f32 v[68:69], v[68:69], v[88:89]
	v_pk_add_f32 v[70:71], v[70:71], v[90:91]
	v_pk_add_f32 v[52:53], v[52:53], v[88:89]
	v_pk_add_f32 v[54:55], v[54:55], v[90:91]
	v_pk_add_f32 v[36:37], v[36:37], v[88:89]
	v_pk_add_f32 v[38:39], v[38:39], v[90:91]
	v_pk_add_f32 v[20:21], v[20:21], v[88:89]
	v_pk_add_f32 v[22:23], v[22:23], v[90:91]
	v_pk_add_f32 v[4:5], v[4:5], v[88:89]
	v_pk_add_f32 v[6:7], v[6:7], v[90:91]
	v_pk_add_f32 v[128:129], v[128:129], v[92:93]
	v_pk_add_f32 v[130:131], v[130:131], v[94:95]
	v_pk_add_f32 v[112:113], v[112:113], v[92:93]
	v_pk_add_f32 v[114:115], v[114:115], v[94:95]
	v_pk_add_f32 v[96:97], v[96:97], v[92:93]
	v_pk_add_f32 v[98:99], v[98:99], v[94:95]
	v_pk_add_f32 v[64:65], v[64:65], v[92:93]
	v_pk_add_f32 v[66:67], v[66:67], v[94:95]
	v_pk_add_f32 v[48:49], v[48:49], v[92:93]
	v_pk_add_f32 v[50:51], v[50:51], v[94:95]
	v_pk_add_f32 v[32:33], v[32:33], v[92:93]
	v_pk_add_f32 v[34:35], v[34:35], v[94:95]
	v_pk_add_f32 v[16:17], v[16:17], v[92:93]
	v_pk_add_f32 v[18:19], v[18:19], v[94:95]
	v_pk_add_f32 v[0:1], v[0:1], v[92:93]
	v_pk_add_f32 v[2:3], v[2:3], v[94:95]
	s_add_u32 s94, s98, 0xc000
	s_addc_u32 s95, s99, 0
	global_load_dwordx4 v[240:243], v191, s[94:95] offset:0 nt
	global_load_dwordx4 v[244:247], v191, s[94:95] offset:64 nt
	s_add_u32 s94, s98, 0x12000
	s_addc_u32 s95, s99, 0
	global_load_dwordx4 v[248:251], v191, s[94:95] offset:0 nt
	global_load_dwordx4 v[252:255], v191, s[94:95] offset:64 nt
	s_add_u32 s94, s98, 0x30000
	s_addc_u32 s95, s99, 0
	global_load_dwordx4 v[136:139], v191, s[94:95] offset:0 nt
	global_load_dwordx4 v[148:151], v191, s[94:95] offset:64 nt
	s_add_u32 s94, s98, 0x36000
	s_addc_u32 s95, s99, 0
	global_load_dwordx4 v[152:155], v191, s[94:95] offset:0 nt
	global_load_dwordx4 v[156:159], v191, s[94:95] offset:64 nt
	s_waitcnt vmcnt(19)
	s_waitcnt vmcnt(11)
	v_cvt_f32_f16_e32 v72, v208
	v_cvt_f32_f16_sdwa v73, v208 dst_sel:DWORD dst_unused:UNUSED_PAD src0_sel:WORD_1
	v_cvt_f32_f16_e32 v74, v209
	v_cvt_f32_f16_sdwa v75, v209 dst_sel:DWORD dst_unused:UNUSED_PAD src0_sel:WORD_1
	v_cvt_f32_f16_e32 v80, v210
	v_cvt_f32_f16_sdwa v81, v210 dst_sel:DWORD dst_unused:UNUSED_PAD src0_sel:WORD_1
	v_cvt_f32_f16_e32 v82, v211
	v_cvt_f32_f16_sdwa v83, v211 dst_sel:DWORD dst_unused:UNUSED_PAD src0_sel:WORD_1
	v_sub_f32_e32 v72, v72, v238
	v_sub_f32_e32 v73, v73, v238
	v_sub_f32_e32 v74, v74, v238
	v_sub_f32_e32 v75, v75, v238
	v_sub_f32_e32 v80, v80, v238
	v_sub_f32_e32 v81, v81, v238
	v_sub_f32_e32 v82, v82, v238
	v_sub_f32_e32 v83, v83, v238
	v_pk_mul_f32 v[72:73], v[238:239], v[72:73] op_sel:[1,0]
	v_pk_mul_f32 v[74:75], v[238:239], v[74:75] op_sel:[1,0]
	v_pk_mul_f32 v[80:81], v[238:239], v[80:81] op_sel:[1,0]
	v_pk_mul_f32 v[82:83], v[238:239], v[82:83] op_sel:[1,0]
	v_pk_fma_f32 v[144:145], v[72:73], v[160:161], v[144:145]
	v_pk_fma_f32 v[146:147], v[74:75], v[162:163], v[146:147]
	v_pk_fma_f32 v[140:141], v[80:81], v[164:165], v[140:141]
	v_pk_fma_f32 v[142:143], v[82:83], v[166:167], v[142:143]
	v_cvt_pk_f16_f32 v144, v144, v145
	v_cvt_pk_f16_f32 v145, v146, v147
	v_cvt_pk_f16_f32 v146, v140, v141
	v_cvt_pk_f16_f32 v147, v142, v143
	ds_write_b128 v235, v[144:147]
	v_fma_mix_f32 v206, v144, 1.0, 0 op_sel_hi:[1,0,0]
	v_fma_mix_f32 v207, v144, v144, 0 op_sel_hi:[1,1,0]
	v_fma_mix_f32 v206, v144, 1.0, v206 op_sel:[1,0,0] op_sel_hi:[1,0,0]
	v_fma_mix_f32 v207, v144, v144, v207 op_sel:[1,1,0] op_sel_hi:[1,1,0]
	v_fma_mix_f32 v206, v145, 1.0, v206 op_sel_hi:[1,0,0]
	v_fma_mix_f32 v207, v145, v145, v207 op_sel_hi:[1,1,0]
	v_fma_mix_f32 v206, v145, 1.0, v206 op_sel:[1,0,0] op_sel_hi:[1,0,0]
	v_fma_mix_f32 v207, v145, v145, v207 op_sel:[1,1,0] op_sel_hi:[1,1,0]
	v_fma_mix_f32 v206, v146, 1.0, v206 op_sel_hi:[1,0,0]
	v_fma_mix_f32 v207, v146, v146, v207 op_sel_hi:[1,1,0]
	v_fma_mix_f32 v206, v146, 1.0, v206 op_sel:[1,0,0] op_sel_hi:[1,0,0]
	v_fma_mix_f32 v207, v146, v146, v207 op_sel:[1,1,0] op_sel_hi:[1,1,0]
	v_fma_mix_f32 v206, v147, 1.0, v206 op_sel_hi:[1,0,0]
	v_fma_mix_f32 v207, v147, v147, v207 op_sel_hi:[1,1,0]
	v_fma_mix_f32 v206, v147, 1.0, v206 op_sel:[1,0,0] op_sel_hi:[1,0,0]
	v_fma_mix_f32 v207, v147, v147, v207 op_sel:[1,1,0] op_sel_hi:[1,1,0]
	s_waitcnt vmcnt(10)
	v_cvt_f32_f16_e32 v72, v212
	v_cvt_f32_f16_sdwa v73, v212 dst_sel:DWORD dst_unused:UNUSED_PAD src0_sel:WORD_1
	v_cvt_f32_f16_e32 v74, v213
	v_cvt_f32_f16_sdwa v75, v213 dst_sel:DWORD dst_unused:UNUSED_PAD src0_sel:WORD_1
	v_cvt_f32_f16_e32 v80, v214
	v_cvt_f32_f16_sdwa v81, v214 dst_sel:DWORD dst_unused:UNUSED_PAD src0_sel:WORD_1
	v_cvt_f32_f16_e32 v82, v215
	v_cvt_f32_f16_sdwa v83, v215 dst_sel:DWORD dst_unused:UNUSED_PAD src0_sel:WORD_1
	v_sub_f32_e32 v72, v72, v238
	v_sub_f32_e32 v73, v73, v238
	v_sub_f32_e32 v74, v74, v238
	v_sub_f32_e32 v75, v75, v238
	v_sub_f32_e32 v80, v80, v238
	v_sub_f32_e32 v81, v81, v238
	v_sub_f32_e32 v82, v82, v238
	v_sub_f32_e32 v83, v83, v238
	v_pk_mul_f32 v[72:73], v[238:239], v[72:73] op_sel:[1,0]
	v_pk_mul_f32 v[74:75], v[238:239], v[74:75] op_sel:[1,0]
	v_pk_mul_f32 v[80:81], v[238:239], v[80:81] op_sel:[1,0]
	v_pk_mul_f32 v[82:83], v[238:239], v[82:83] op_sel:[1,0]
	v_pk_fma_f32 v[132:133], v[72:73], v[168:169], v[132:133]
	v_pk_fma_f32 v[134:135], v[74:75], v[170:171], v[134:135]
	v_pk_fma_f32 v[128:129], v[80:81], v[172:173], v[128:129]
	v_pk_fma_f32 v[130:131], v[82:83], v[174:175], v[130:131]
	v_cvt_pk_f16_f32 v132, v132, v133
	v_cvt_pk_f16_f32 v133, v134, v135
	v_cvt_pk_f16_f32 v134, v128, v129
	v_cvt_pk_f16_f32 v135, v130, v131
	ds_write_b128 v235, v[132:135] offset:64
	v_fma_mix_f32 v206, v132, 1.0, v206 op_sel_hi:[1,0,0]
	v_fma_mix_f32 v207, v132, v132, v207 op_sel_hi:[1,1,0]
	v_fma_mix_f32 v206, v132, 1.0, v206 op_sel:[1,0,0] op_sel_hi:[1,0,0]
	v_fma_mix_f32 v207, v132, v132, v207 op_sel:[1,1,0] op_sel_hi:[1,1,0]
	v_fma_mix_f32 v206, v133, 1.0, v206 op_sel_hi:[1,0,0]
	v_fma_mix_f32 v207, v133, v133, v207 op_sel_hi:[1,1,0]
	v_fma_mix_f32 v206, v133, 1.0, v206 op_sel:[1,0,0] op_sel_hi:[1,0,0]
	v_fma_mix_f32 v207, v133, v133, v207 op_sel:[1,1,0] op_sel_hi:[1,1,0]
	v_fma_mix_f32 v206, v134, 1.0, v206 op_sel_hi:[1,0,0]
	v_fma_mix_f32 v207, v134, v134, v207 op_sel_hi:[1,1,0]
	v_fma_mix_f32 v206, v134, 1.0, v206 op_sel:[1,0,0] op_sel_hi:[1,0,0]
	v_fma_mix_f32 v207, v134, v134, v207 op_sel:[1,1,0] op_sel_hi:[1,1,0]
	v_fma_mix_f32 v206, v135, 1.0, v206 op_sel_hi:[1,0,0]
	v_fma_mix_f32 v207, v135, v135, v207 op_sel_hi:[1,1,0]
	v_fma_mix_f32 v206, v135, 1.0, v206 op_sel:[1,0,0] op_sel_hi:[1,0,0]
	v_fma_mix_f32 v207, v135, v135, v207 op_sel:[1,1,0] op_sel_hi:[1,1,0]
	ds_read_b128 v[88:91], v236
	ds_read_b128 v[92:95], v236 offset:1152
	s_waitcnt vmcnt(9)
	v_cvt_f32_f16_e32 v72, v216
	v_cvt_f32_f16_sdwa v73, v216 dst_sel:DWORD dst_unused:UNUSED_PAD src0_sel:WORD_1
	v_cvt_f32_f16_e32 v74, v217
	v_cvt_f32_f16_sdwa v75, v217 dst_sel:DWORD dst_unused:UNUSED_PAD src0_sel:WORD_1
	v_cvt_f32_f16_e32 v80, v218
	v_cvt_f32_f16_sdwa v81, v218 dst_sel:DWORD dst_unused:UNUSED_PAD src0_sel:WORD_1
	v_cvt_f32_f16_e32 v82, v219
	v_cvt_f32_f16_sdwa v83, v219 dst_sel:DWORD dst_unused:UNUSED_PAD src0_sel:WORD_1
	v_sub_f32_e32 v72, v72, v192
	v_sub_f32_e32 v73, v73, v192
	v_sub_f32_e32 v74, v74, v192
	v_sub_f32_e32 v75, v75, v192
	v_sub_f32_e32 v80, v80, v192
	v_sub_f32_e32 v81, v81, v192
	v_sub_f32_e32 v82, v82, v192
	v_sub_f32_e32 v83, v83, v192
	v_pk_mul_f32 v[72:73], v[192:193], v[72:73] op_sel:[1,0]
	v_pk_mul_f32 v[74:75], v[192:193], v[74:75] op_sel:[1,0]
	v_pk_mul_f32 v[80:81], v[192:193], v[80:81] op_sel:[1,0]
	v_pk_mul_f32 v[82:83], v[192:193], v[82:83] op_sel:[1,0]
	v_pk_fma_f32 v[124:125], v[72:73], v[160:161], v[124:125]
	v_pk_fma_f32 v[126:127], v[74:75], v[162:163], v[126:127]
	v_pk_fma_f32 v[120:121], v[80:81], v[164:165], v[120:121]
	v_pk_fma_f32 v[122:123], v[82:83], v[166:167], v[122:123]
	v_cvt_pk_f16_f32 v124, v124, v125
	v_cvt_pk_f16_f32 v125, v126, v127
	v_cvt_pk_f16_f32 v126, v120, v121
	v_cvt_pk_f16_f32 v127, v122, v123
	s_waitcnt lgkmcnt(0)
	buffer_store_dwordx4 v[88:91], v224, s[24:27], 0 offen sc1
	v_add_u32_e32 v82, 0x3000, v224
	buffer_store_dwordx4 v[92:95], v82, s[24:27], 0 offen sc1
	ds_write_b128 v235, v[124:127]
	v_fma_mix_f32 v140, v124, 1.0, 0 op_sel_hi:[1,0,0]
	v_fma_mix_f32 v141, v124, v124, 0 op_sel_hi:[1,1,0]
	v_fma_mix_f32 v140, v124, 1.0, v140 op_sel:[1,0,0] op_sel_hi:[1,0,0]
	v_fma_mix_f32 v141, v124, v124, v141 op_sel:[1,1,0] op_sel_hi:[1,1,0]
	v_fma_mix_f32 v140, v125, 1.0, v140 op_sel_hi:[1,0,0]
	v_fma_mix_f32 v141, v125, v125, v141 op_sel_hi:[1,1,0]
	v_fma_mix_f32 v140, v125, 1.0, v140 op_sel:[1,0,0] op_sel_hi:[1,0,0]
	v_fma_mix_f32 v141, v125, v125, v141 op_sel:[1,1,0] op_sel_hi:[1,1,0]
	v_fma_mix_f32 v140, v126, 1.0, v140 op_sel_hi:[1,0,0]
	v_fma_mix_f32 v141, v126, v126, v141 op_sel_hi:[1,1,0]
	v_fma_mix_f32 v140, v126, 1.0, v140 op_sel:[1,0,0] op_sel_hi:[1,0,0]
	v_fma_mix_f32 v141, v126, v126, v141 op_sel:[1,1,0] op_sel_hi:[1,1,0]
	v_fma_mix_f32 v140, v127, 1.0, v140 op_sel_hi:[1,0,0]
	v_fma_mix_f32 v141, v127, v127, v141 op_sel_hi:[1,1,0]
	v_fma_mix_f32 v140, v127, 1.0, v140 op_sel:[1,0,0] op_sel_hi:[1,0,0]
	v_fma_mix_f32 v141, v127, v127, v141 op_sel:[1,1,0] op_sel_hi:[1,1,0]
	s_waitcnt vmcnt(10)
	v_cvt_f32_f16_e32 v72, v220
	v_cvt_f32_f16_sdwa v73, v220 dst_sel:DWORD dst_unused:UNUSED_PAD src0_sel:WORD_1
	v_cvt_f32_f16_e32 v74, v221
	v_cvt_f32_f16_sdwa v75, v221 dst_sel:DWORD dst_unused:UNUSED_PAD src0_sel:WORD_1
	v_cvt_f32_f16_e32 v80, v222
	v_cvt_f32_f16_sdwa v81, v222 dst_sel:DWORD dst_unused:UNUSED_PAD src0_sel:WORD_1
	v_cvt_f32_f16_e32 v82, v223
	v_cvt_f32_f16_sdwa v83, v223 dst_sel:DWORD dst_unused:UNUSED_PAD src0_sel:WORD_1
	v_sub_f32_e32 v72, v72, v192
	v_sub_f32_e32 v73, v73, v192
	v_sub_f32_e32 v74, v74, v192
	v_sub_f32_e32 v75, v75, v192
	v_sub_f32_e32 v80, v80, v192
	v_sub_f32_e32 v81, v81, v192
	v_sub_f32_e32 v82, v82, v192
	v_sub_f32_e32 v83, v83, v192
	v_pk_mul_f32 v[72:73], v[192:193], v[72:73] op_sel:[1,0]
	v_pk_mul_f32 v[74:75], v[192:193], v[74:75] op_sel:[1,0]
	v_pk_mul_f32 v[80:81], v[192:193], v[80:81] op_sel:[1,0]
	v_pk_mul_f32 v[82:83], v[192:193], v[82:83] op_sel:[1,0]
	v_pk_fma_f32 v[116:117], v[72:73], v[168:169], v[116:117]
	v_pk_fma_f32 v[118:119], v[74:75], v[170:171], v[118:119]
	v_pk_fma_f32 v[112:113], v[80:81], v[172:173], v[112:113]
	v_pk_fma_f32 v[114:115], v[82:83], v[174:175], v[114:115]
	v_cvt_pk_f16_f32 v116, v116, v117
	v_cvt_pk_f16_f32 v117, v118, v119
	v_cvt_pk_f16_f32 v118, v112, v113
	v_cvt_pk_f16_f32 v119, v114, v115
	ds_write_b128 v235, v[116:119] offset:64
	v_fma_mix_f32 v140, v116, 1.0, v140 op_sel_hi:[1,0,0]
	v_fma_mix_f32 v141, v116, v116, v141 op_sel_hi:[1,1,0]
	v_fma_mix_f32 v140, v116, 1.0, v140 op_sel:[1,0,0] op_sel_hi:[1,0,0]
	v_fma_mix_f32 v141, v116, v116, v141 op_sel:[1,1,0] op_sel_hi:[1,1,0]
	v_fma_mix_f32 v140, v117, 1.0, v140 op_sel_hi:[1,0,0]
	v_fma_mix_f32 v141, v117, v117, v141 op_sel_hi:[1,1,0]
	v_fma_mix_f32 v140, v117, 1.0, v140 op_sel:[1,0,0] op_sel_hi:[1,0,0]
	v_fma_mix_f32 v141, v117, v117, v141 op_sel:[1,1,0] op_sel_hi:[1,1,0]
	v_fma_mix_f32 v140, v118, 1.0, v140 op_sel_hi:[1,0,0]
	v_fma_mix_f32 v141, v118, v118, v141 op_sel_hi:[1,1,0]
	v_fma_mix_f32 v140, v118, 1.0, v140 op_sel:[1,0,0] op_sel_hi:[1,0,0]
	v_fma_mix_f32 v141, v118, v118, v141 op_sel:[1,1,0] op_sel_hi:[1,1,0]
	v_fma_mix_f32 v140, v119, 1.0, v140 op_sel_hi:[1,0,0]
	v_fma_mix_f32 v141, v119, v119, v141 op_sel_hi:[1,1,0]
	v_fma_mix_f32 v140, v119, 1.0, v140 op_sel:[1,0,0] op_sel_hi:[1,0,0]
	v_fma_mix_f32 v141, v119, v119, v141 op_sel:[1,1,0] op_sel_hi:[1,1,0]
	ds_read_b128 v[208:211], v236
	ds_read_b128 v[128:131], v236 offset:1152
	s_add_u32 s94, s98, 0x3c000
	s_addc_u32 s95, s99, 0
	global_load_dwordx4 v[212:215], v191, s[94:95] offset:0 nt
	global_load_dwordx4 v[144:147], v191, s[94:95] offset:64 nt
	s_add_u32 s94, s98, 0x42000
	s_addc_u32 s95, s99, 0
	global_load_dwordx4 v[132:135], v191, s[94:95] offset:0 nt
	global_load_dwordx4 v[88:91], v191, s[94:95] offset:64 nt
	s_waitcnt vmcnt(13)
	v_cvt_f32_f16_e32 v72, v240
	v_cvt_f32_f16_sdwa v73, v240 dst_sel:DWORD dst_unused:UNUSED_PAD src0_sel:WORD_1
	v_cvt_f32_f16_e32 v74, v241
	v_cvt_f32_f16_sdwa v75, v241 dst_sel:DWORD dst_unused:UNUSED_PAD src0_sel:WORD_1
	v_cvt_f32_f16_e32 v80, v242
	v_cvt_f32_f16_sdwa v81, v242 dst_sel:DWORD dst_unused:UNUSED_PAD src0_sel:WORD_1
	v_cvt_f32_f16_e32 v82, v243
	v_cvt_f32_f16_sdwa v83, v243 dst_sel:DWORD dst_unused:UNUSED_PAD src0_sel:WORD_1
	v_sub_f32_e32 v72, v72, v194
	v_sub_f32_e32 v73, v73, v194
	v_sub_f32_e32 v74, v74, v194
	v_sub_f32_e32 v75, v75, v194
	v_sub_f32_e32 v80, v80, v194
	v_sub_f32_e32 v81, v81, v194
	v_sub_f32_e32 v82, v82, v194
	v_sub_f32_e32 v83, v83, v194
	v_pk_mul_f32 v[72:73], v[194:195], v[72:73] op_sel:[1,0]
	v_pk_mul_f32 v[74:75], v[194:195], v[74:75] op_sel:[1,0]
	v_pk_mul_f32 v[80:81], v[194:195], v[80:81] op_sel:[1,0]
	v_pk_mul_f32 v[82:83], v[194:195], v[82:83] op_sel:[1,0]
	v_pk_fma_f32 v[108:109], v[72:73], v[160:161], v[108:109]
	v_pk_fma_f32 v[110:111], v[74:75], v[162:163], v[110:111]
	v_pk_fma_f32 v[104:105], v[80:81], v[164:165], v[104:105]
	v_pk_fma_f32 v[106:107], v[82:83], v[166:167], v[106:107]
	v_cvt_pk_f16_f32 v108, v108, v109
	v_cvt_pk_f16_f32 v109, v110, v111
	v_cvt_pk_f16_f32 v110, v104, v105
	v_cvt_pk_f16_f32 v111, v106, v107
	s_waitcnt lgkmcnt(0)
	v_add_u32_e32 v83, 0x6000, v224
	buffer_store_dwordx4 v[208:211], v83, s[24:27], 0 offen sc1
	v_add_u32_e32 v82, 0x9000, v224
	buffer_store_dwordx4 v[128:131], v82, s[24:27], 0 offen sc1
	ds_write_b128 v235, v[108:111]
	v_fma_mix_f32 v142, v108, 1.0, 0 op_sel_hi:[1,0,0]
	v_fma_mix_f32 v143, v108, v108, 0 op_sel_hi:[1,1,0]
	v_fma_mix_f32 v142, v108, 1.0, v142 op_sel:[1,0,0] op_sel_hi:[1,0,0]
	v_fma_mix_f32 v143, v108, v108, v143 op_sel:[1,1,0] op_sel_hi:[1,1,0]
	v_fma_mix_f32 v142, v109, 1.0, v142 op_sel_hi:[1,0,0]
	v_fma_mix_f32 v143, v109, v109, v143 op_sel_hi:[1,1,0]
	v_fma_mix_f32 v142, v109, 1.0, v142 op_sel:[1,0,0] op_sel_hi:[1,0,0]
	v_fma_mix_f32 v143, v109, v109, v143 op_sel:[1,1,0] op_sel_hi:[1,1,0]
	v_fma_mix_f32 v142, v110, 1.0, v142 op_sel_hi:[1,0,0]
	v_fma_mix_f32 v143, v110, v110, v143 op_sel_hi:[1,1,0]
	v_fma_mix_f32 v142, v110, 1.0, v142 op_sel:[1,0,0] op_sel_hi:[1,0,0]
	v_fma_mix_f32 v143, v110, v110, v143 op_sel:[1,1,0] op_sel_hi:[1,1,0]
	v_fma_mix_f32 v142, v111, 1.0, v142 op_sel_hi:[1,0,0]
	v_fma_mix_f32 v143, v111, v111, v143 op_sel_hi:[1,1,0]
	v_fma_mix_f32 v142, v111, 1.0, v142 op_sel:[1,0,0] op_sel_hi:[1,0,0]
	v_fma_mix_f32 v143, v111, v111, v143 op_sel:[1,1,0] op_sel_hi:[1,1,0]
	s_waitcnt vmcnt(14)
	v_cvt_f32_f16_e32 v72, v244
	v_cvt_f32_f16_sdwa v73, v244 dst_sel:DWORD dst_unused:UNUSED_PAD src0_sel:WORD_1
	v_cvt_f32_f16_e32 v74, v245
	v_cvt_f32_f16_sdwa v75, v245 dst_sel:DWORD dst_unused:UNUSED_PAD src0_sel:WORD_1
	v_cvt_f32_f16_e32 v80, v246
	v_cvt_f32_f16_sdwa v81, v246 dst_sel:DWORD dst_unused:UNUSED_PAD src0_sel:WORD_1
	v_cvt_f32_f16_e32 v82, v247
	v_cvt_f32_f16_sdwa v83, v247 dst_sel:DWORD dst_unused:UNUSED_PAD src0_sel:WORD_1
	v_sub_f32_e32 v72, v72, v194
	v_sub_f32_e32 v73, v73, v194
	v_sub_f32_e32 v74, v74, v194
	v_sub_f32_e32 v75, v75, v194
	v_sub_f32_e32 v80, v80, v194
	v_sub_f32_e32 v81, v81, v194
	v_sub_f32_e32 v82, v82, v194
	v_sub_f32_e32 v83, v83, v194
	v_pk_mul_f32 v[72:73], v[194:195], v[72:73] op_sel:[1,0]
	v_pk_mul_f32 v[74:75], v[194:195], v[74:75] op_sel:[1,0]
	v_pk_mul_f32 v[80:81], v[194:195], v[80:81] op_sel:[1,0]
	v_pk_mul_f32 v[82:83], v[194:195], v[82:83] op_sel:[1,0]
	v_pk_fma_f32 v[100:101], v[72:73], v[168:169], v[100:101]
	v_pk_fma_f32 v[102:103], v[74:75], v[170:171], v[102:103]
	v_pk_fma_f32 v[96:97], v[80:81], v[172:173], v[96:97]
	v_pk_fma_f32 v[98:99], v[82:83], v[174:175], v[98:99]
	v_cvt_pk_f16_f32 v100, v100, v101
	v_cvt_pk_f16_f32 v101, v102, v103
	v_cvt_pk_f16_f32 v102, v96, v97
	v_cvt_pk_f16_f32 v103, v98, v99
	ds_write_b128 v235, v[100:103] offset:64
	v_fma_mix_f32 v142, v100, 1.0, v142 op_sel_hi:[1,0,0]
	v_fma_mix_f32 v143, v100, v100, v143 op_sel_hi:[1,1,0]
	v_fma_mix_f32 v142, v100, 1.0, v142 op_sel:[1,0,0] op_sel_hi:[1,0,0]
	v_fma_mix_f32 v143, v100, v100, v143 op_sel:[1,1,0] op_sel_hi:[1,1,0]
	v_fma_mix_f32 v142, v101, 1.0, v142 op_sel_hi:[1,0,0]
	v_fma_mix_f32 v143, v101, v101, v143 op_sel_hi:[1,1,0]
	v_fma_mix_f32 v142, v101, 1.0, v142 op_sel:[1,0,0] op_sel_hi:[1,0,0]
	v_fma_mix_f32 v143, v101, v101, v143 op_sel:[1,1,0] op_sel_hi:[1,1,0]
	v_fma_mix_f32 v142, v102, 1.0, v142 op_sel_hi:[1,0,0]
	v_fma_mix_f32 v143, v102, v102, v143 op_sel_hi:[1,1,0]
	v_fma_mix_f32 v142, v102, 1.0, v142 op_sel:[1,0,0] op_sel_hi:[1,0,0]
	v_fma_mix_f32 v143, v102, v102, v143 op_sel:[1,1,0] op_sel_hi:[1,1,0]
	v_fma_mix_f32 v142, v103, 1.0, v142 op_sel_hi:[1,0,0]
	v_fma_mix_f32 v143, v103, v103, v143 op_sel_hi:[1,1,0]
	v_fma_mix_f32 v142, v103, 1.0, v142 op_sel:[1,0,0] op_sel_hi:[1,0,0]
	v_fma_mix_f32 v143, v103, v103, v143 op_sel:[1,1,0] op_sel_hi:[1,1,0]
	ds_read_b128 v[92:95], v236
	ds_read_b128 v[120:123], v236 offset:1152
	s_waitcnt vmcnt(13)
	v_cvt_f32_f16_e32 v72, v248
	v_cvt_f32_f16_sdwa v73, v248 dst_sel:DWORD dst_unused:UNUSED_PAD src0_sel:WORD_1
	v_cvt_f32_f16_e32 v74, v249
	v_cvt_f32_f16_sdwa v75, v249 dst_sel:DWORD dst_unused:UNUSED_PAD src0_sel:WORD_1
	v_cvt_f32_f16_e32 v80, v250
	v_cvt_f32_f16_sdwa v81, v250 dst_sel:DWORD dst_unused:UNUSED_PAD src0_sel:WORD_1
	v_cvt_f32_f16_e32 v82, v251
	v_cvt_f32_f16_sdwa v83, v251 dst_sel:DWORD dst_unused:UNUSED_PAD src0_sel:WORD_1
	v_sub_f32_e32 v72, v72, v196
	v_sub_f32_e32 v73, v73, v196
	v_sub_f32_e32 v74, v74, v196
	v_sub_f32_e32 v75, v75, v196
	v_sub_f32_e32 v80, v80, v196
	v_sub_f32_e32 v81, v81, v196
	v_sub_f32_e32 v82, v82, v196
	v_sub_f32_e32 v83, v83, v196
	v_pk_mul_f32 v[72:73], v[196:197], v[72:73] op_sel:[1,0]
	v_pk_mul_f32 v[74:75], v[196:197], v[74:75] op_sel:[1,0]
	v_pk_mul_f32 v[80:81], v[196:197], v[80:81] op_sel:[1,0]
	v_pk_mul_f32 v[82:83], v[196:197], v[82:83] op_sel:[1,0]
	v_pk_fma_f32 v[84:85], v[72:73], v[160:161], v[84:85]
	v_pk_fma_f32 v[86:87], v[74:75], v[162:163], v[86:87]
	v_pk_fma_f32 v[76:77], v[80:81], v[164:165], v[76:77]
	v_pk_fma_f32 v[78:79], v[82:83], v[166:167], v[78:79]
	v_cvt_pk_f16_f32 v84, v84, v85
	v_cvt_pk_f16_f32 v85, v86, v87
	v_cvt_pk_f16_f32 v86, v76, v77
	v_cvt_pk_f16_f32 v87, v78, v79
	s_waitcnt lgkmcnt(0)
	v_add_u32_e32 v83, 0xc000, v224
	buffer_store_dwordx4 v[92:95], v83, s[24:27], 0 offen sc1
	v_add_u32_e32 v82, 0xf000, v224
	buffer_store_dwordx4 v[120:123], v82, s[24:27], 0 offen sc1
	ds_write_b128 v235, v[84:87]
	v_fma_mix_f32 v216, v84, 1.0, 0 op_sel_hi:[1,0,0]
	v_fma_mix_f32 v217, v84, v84, 0 op_sel_hi:[1,1,0]
	v_fma_mix_f32 v216, v84, 1.0, v216 op_sel:[1,0,0] op_sel_hi:[1,0,0]
	v_fma_mix_f32 v217, v84, v84, v217 op_sel:[1,1,0] op_sel_hi:[1,1,0]
	v_fma_mix_f32 v216, v85, 1.0, v216 op_sel_hi:[1,0,0]
	v_fma_mix_f32 v217, v85, v85, v217 op_sel_hi:[1,1,0]
	v_fma_mix_f32 v216, v85, 1.0, v216 op_sel:[1,0,0] op_sel_hi:[1,0,0]
	v_fma_mix_f32 v217, v85, v85, v217 op_sel:[1,1,0] op_sel_hi:[1,1,0]
	v_fma_mix_f32 v216, v86, 1.0, v216 op_sel_hi:[1,0,0]
	v_fma_mix_f32 v217, v86, v86, v217 op_sel_hi:[1,1,0]
	v_fma_mix_f32 v216, v86, 1.0, v216 op_sel:[1,0,0] op_sel_hi:[1,0,0]
	v_fma_mix_f32 v217, v86, v86, v217 op_sel:[1,1,0] op_sel_hi:[1,1,0]
	v_fma_mix_f32 v216, v87, 1.0, v216 op_sel_hi:[1,0,0]
	v_fma_mix_f32 v217, v87, v87, v217 op_sel_hi:[1,1,0]
	v_fma_mix_f32 v216, v87, 1.0, v216 op_sel:[1,0,0] op_sel_hi:[1,0,0]
	v_fma_mix_f32 v217, v87, v87, v217 op_sel:[1,1,0] op_sel_hi:[1,1,0]
	s_waitcnt vmcnt(14)
	v_cvt_f32_f16_e32 v72, v252
	v_cvt_f32_f16_sdwa v73, v252 dst_sel:DWORD dst_unused:UNUSED_PAD src0_sel:WORD_1
	v_cvt_f32_f16_e32 v74, v253
	v_cvt_f32_f16_sdwa v75, v253 dst_sel:DWORD dst_unused:UNUSED_PAD src0_sel:WORD_1
	v_cvt_f32_f16_e32 v80, v254
	v_cvt_f32_f16_sdwa v81, v254 dst_sel:DWORD dst_unused:UNUSED_PAD src0_sel:WORD_1
	v_cvt_f32_f16_e32 v82, v255
	v_cvt_f32_f16_sdwa v83, v255 dst_sel:DWORD dst_unused:UNUSED_PAD src0_sel:WORD_1
	v_sub_f32_e32 v72, v72, v196
	v_sub_f32_e32 v73, v73, v196
	v_sub_f32_e32 v74, v74, v196
	v_sub_f32_e32 v75, v75, v196
	v_sub_f32_e32 v80, v80, v196
	v_sub_f32_e32 v81, v81, v196
	v_sub_f32_e32 v82, v82, v196
	v_sub_f32_e32 v83, v83, v196
	v_pk_mul_f32 v[72:73], v[196:197], v[72:73] op_sel:[1,0]
	v_pk_mul_f32 v[74:75], v[196:197], v[74:75] op_sel:[1,0]
	v_pk_mul_f32 v[80:81], v[196:197], v[80:81] op_sel:[1,0]
	v_pk_mul_f32 v[82:83], v[196:197], v[82:83] op_sel:[1,0]
	v_pk_fma_f32 v[68:69], v[72:73], v[168:169], v[68:69]
	v_pk_fma_f32 v[70:71], v[74:75], v[170:171], v[70:71]
	v_pk_fma_f32 v[64:65], v[80:81], v[172:173], v[64:65]
	v_pk_fma_f32 v[66:67], v[82:83], v[174:175], v[66:67]
	v_cvt_pk_f16_f32 v68, v68, v69
	v_cvt_pk_f16_f32 v69, v70, v71
	v_cvt_pk_f16_f32 v70, v64, v65
	v_cvt_pk_f16_f32 v71, v66, v67
	ds_write_b128 v235, v[68:71] offset:64
	v_fma_mix_f32 v216, v68, 1.0, v216 op_sel_hi:[1,0,0]
	v_fma_mix_f32 v217, v68, v68, v217 op_sel_hi:[1,1,0]
	v_fma_mix_f32 v216, v68, 1.0, v216 op_sel:[1,0,0] op_sel_hi:[1,0,0]
	v_fma_mix_f32 v217, v68, v68, v217 op_sel:[1,1,0] op_sel_hi:[1,1,0]
	v_fma_mix_f32 v216, v69, 1.0, v216 op_sel_hi:[1,0,0]
	v_fma_mix_f32 v217, v69, v69, v217 op_sel_hi:[1,1,0]
	v_fma_mix_f32 v216, v69, 1.0, v216 op_sel:[1,0,0] op_sel_hi:[1,0,0]
	v_fma_mix_f32 v217, v69, v69, v217 op_sel:[1,1,0] op_sel_hi:[1,1,0]
	v_fma_mix_f32 v216, v70, 1.0, v216 op_sel_hi:[1,0,0]
	v_fma_mix_f32 v217, v70, v70, v217 op_sel_hi:[1,1,0]
	v_fma_mix_f32 v216, v70, 1.0, v216 op_sel:[1,0,0] op_sel_hi:[1,0,0]
	v_fma_mix_f32 v217, v70, v70, v217 op_sel:[1,1,0] op_sel_hi:[1,1,0]
	v_fma_mix_f32 v216, v71, 1.0, v216 op_sel_hi:[1,0,0]
	v_fma_mix_f32 v217, v71, v71, v217 op_sel_hi:[1,1,0]
	v_fma_mix_f32 v216, v71, 1.0, v216 op_sel:[1,0,0] op_sel_hi:[1,0,0]
	v_fma_mix_f32 v217, v71, v71, v217 op_sel:[1,1,0] op_sel_hi:[1,1,0]
	ds_read_b128 v[112:115], v236
	ds_read_b128 v[220:223], v236 offset:1152
	s_waitcnt vmcnt(13)
	v_cvt_f32_f16_e32 v72, v136
	v_cvt_f32_f16_sdwa v73, v136 dst_sel:DWORD dst_unused:UNUSED_PAD src0_sel:WORD_1
	v_cvt_f32_f16_e32 v74, v137
	v_cvt_f32_f16_sdwa v75, v137 dst_sel:DWORD dst_unused:UNUSED_PAD src0_sel:WORD_1
	v_cvt_f32_f16_e32 v80, v138
	v_cvt_f32_f16_sdwa v81, v138 dst_sel:DWORD dst_unused:UNUSED_PAD src0_sel:WORD_1
	v_cvt_f32_f16_e32 v82, v139
	v_cvt_f32_f16_sdwa v83, v139 dst_sel:DWORD dst_unused:UNUSED_PAD src0_sel:WORD_1
	v_sub_f32_e32 v72, v72, v198
	v_sub_f32_e32 v73, v73, v198
	v_sub_f32_e32 v74, v74, v198
	v_sub_f32_e32 v75, v75, v198
	v_sub_f32_e32 v80, v80, v198
	v_sub_f32_e32 v81, v81, v198
	v_sub_f32_e32 v82, v82, v198
	v_sub_f32_e32 v83, v83, v198
	v_pk_mul_f32 v[72:73], v[198:199], v[72:73] op_sel:[1,0]
	v_pk_mul_f32 v[74:75], v[198:199], v[74:75] op_sel:[1,0]
	v_pk_mul_f32 v[80:81], v[198:199], v[80:81] op_sel:[1,0]
	v_pk_mul_f32 v[82:83], v[198:199], v[82:83] op_sel:[1,0]
	v_pk_fma_f32 v[60:61], v[72:73], v[160:161], v[60:61]
	v_pk_fma_f32 v[62:63], v[74:75], v[162:163], v[62:63]
	v_pk_fma_f32 v[56:57], v[80:81], v[164:165], v[56:57]
	v_pk_fma_f32 v[58:59], v[82:83], v[166:167], v[58:59]
	v_cvt_pk_f16_f32 v60, v60, v61
	v_cvt_pk_f16_f32 v61, v62, v63
	v_cvt_pk_f16_f32 v62, v56, v57
	v_cvt_pk_f16_f32 v63, v58, v59
	s_waitcnt lgkmcnt(0)
	v_add_u32_e32 v83, 0x12000, v224
	buffer_store_dwordx4 v[112:115], v83, s[24:27], 0 offen sc1
	v_add_u32_e32 v82, 0x15000, v224
	buffer_store_dwordx4 v[220:223], v82, s[24:27], 0 offen sc1
	ds_write_b128 v235, v[60:63]
	v_fma_mix_f32 v218, v60, 1.0, 0 op_sel_hi:[1,0,0]
	v_fma_mix_f32 v219, v60, v60, 0 op_sel_hi:[1,1,0]
	v_fma_mix_f32 v218, v60, 1.0, v218 op_sel:[1,0,0] op_sel_hi:[1,0,0]
	v_fma_mix_f32 v219, v60, v60, v219 op_sel:[1,1,0] op_sel_hi:[1,1,0]
	v_fma_mix_f32 v218, v61, 1.0, v218 op_sel_hi:[1,0,0]
	v_fma_mix_f32 v219, v61, v61, v219 op_sel_hi:[1,1,0]
	v_fma_mix_f32 v218, v61, 1.0, v218 op_sel:[1,0,0] op_sel_hi:[1,0,0]
	v_fma_mix_f32 v219, v61, v61, v219 op_sel:[1,1,0] op_sel_hi:[1,1,0]
	v_fma_mix_f32 v218, v62, 1.0, v218 op_sel_hi:[1,0,0]
	v_fma_mix_f32 v219, v62, v62, v219 op_sel_hi:[1,1,0]
	v_fma_mix_f32 v218, v62, 1.0, v218 op_sel:[1,0,0] op_sel_hi:[1,0,0]
	v_fma_mix_f32 v219, v62, v62, v219 op_sel:[1,1,0] op_sel_hi:[1,1,0]
	v_fma_mix_f32 v218, v63, 1.0, v218 op_sel_hi:[1,0,0]
	v_fma_mix_f32 v219, v63, v63, v219 op_sel_hi:[1,1,0]
	v_fma_mix_f32 v218, v63, 1.0, v218 op_sel:[1,0,0] op_sel_hi:[1,0,0]
	v_fma_mix_f32 v219, v63, v63, v219 op_sel:[1,1,0] op_sel_hi:[1,1,0]
	s_waitcnt vmcnt(14)
	v_cvt_f32_f16_e32 v72, v148
	v_cvt_f32_f16_sdwa v73, v148 dst_sel:DWORD dst_unused:UNUSED_PAD src0_sel:WORD_1
	v_cvt_f32_f16_e32 v74, v149
	v_cvt_f32_f16_sdwa v75, v149 dst_sel:DWORD dst_unused:UNUSED_PAD src0_sel:WORD_1
	v_cvt_f32_f16_e32 v80, v150
	v_cvt_f32_f16_sdwa v81, v150 dst_sel:DWORD dst_unused:UNUSED_PAD src0_sel:WORD_1
	v_cvt_f32_f16_e32 v82, v151
	v_cvt_f32_f16_sdwa v83, v151 dst_sel:DWORD dst_unused:UNUSED_PAD src0_sel:WORD_1
	v_sub_f32_e32 v72, v72, v198
	v_sub_f32_e32 v73, v73, v198
	v_sub_f32_e32 v74, v74, v198
	v_sub_f32_e32 v75, v75, v198
	v_sub_f32_e32 v80, v80, v198
	v_sub_f32_e32 v81, v81, v198
	v_sub_f32_e32 v82, v82, v198
	v_sub_f32_e32 v83, v83, v198
	v_pk_mul_f32 v[72:73], v[198:199], v[72:73] op_sel:[1,0]
	v_pk_mul_f32 v[74:75], v[198:199], v[74:75] op_sel:[1,0]
	v_pk_mul_f32 v[80:81], v[198:199], v[80:81] op_sel:[1,0]
	v_pk_mul_f32 v[82:83], v[198:199], v[82:83] op_sel:[1,0]
	v_pk_fma_f32 v[52:53], v[72:73], v[168:169], v[52:53]
	v_pk_fma_f32 v[54:55], v[74:75], v[170:171], v[54:55]
	v_pk_fma_f32 v[48:49], v[80:81], v[172:173], v[48:49]
	v_pk_fma_f32 v[50:51], v[82:83], v[174:175], v[50:51]
	v_cvt_pk_f16_f32 v52, v52, v53
	v_cvt_pk_f16_f32 v53, v54, v55
	v_cvt_pk_f16_f32 v54, v48, v49
	v_cvt_pk_f16_f32 v55, v50, v51
	ds_write_b128 v235, v[52:55] offset:64
	v_fma_mix_f32 v218, v52, 1.0, v218 op_sel_hi:[1,0,0]
	v_fma_mix_f32 v219, v52, v52, v219 op_sel_hi:[1,1,0]
	v_fma_mix_f32 v218, v52, 1.0, v218 op_sel:[1,0,0] op_sel_hi:[1,0,0]
	v_fma_mix_f32 v219, v52, v52, v219 op_sel:[1,1,0] op_sel_hi:[1,1,0]
	v_fma_mix_f32 v218, v53, 1.0, v218 op_sel_hi:[1,0,0]
	v_fma_mix_f32 v219, v53, v53, v219 op_sel_hi:[1,1,0]
	v_fma_mix_f32 v218, v53, 1.0, v218 op_sel:[1,0,0] op_sel_hi:[1,0,0]
	v_fma_mix_f32 v219, v53, v53, v219 op_sel:[1,1,0] op_sel_hi:[1,1,0]
	v_fma_mix_f32 v218, v54, 1.0, v218 op_sel_hi:[1,0,0]
	v_fma_mix_f32 v219, v54, v54, v219 op_sel_hi:[1,1,0]
	v_fma_mix_f32 v218, v54, 1.0, v218 op_sel:[1,0,0] op_sel_hi:[1,0,0]
	v_fma_mix_f32 v219, v54, v54, v219 op_sel:[1,1,0] op_sel_hi:[1,1,0]
	v_fma_mix_f32 v218, v55, 1.0, v218 op_sel_hi:[1,0,0]
	v_fma_mix_f32 v219, v55, v55, v219 op_sel_hi:[1,1,0]
	v_fma_mix_f32 v218, v55, 1.0, v218 op_sel:[1,0,0] op_sel_hi:[1,0,0]
	v_fma_mix_f32 v219, v55, v55, v219 op_sel:[1,1,0] op_sel_hi:[1,1,0]
	ds_read_b128 v[124:127], v236
	ds_read_b128 v[116:119], v236 offset:1152
	s_waitcnt vmcnt(13)
	v_cvt_f32_f16_e32 v72, v152
	v_cvt_f32_f16_sdwa v73, v152 dst_sel:DWORD dst_unused:UNUSED_PAD src0_sel:WORD_1
	v_cvt_f32_f16_e32 v74, v153
	v_cvt_f32_f16_sdwa v75, v153 dst_sel:DWORD dst_unused:UNUSED_PAD src0_sel:WORD_1
	v_cvt_f32_f16_e32 v80, v154
	v_cvt_f32_f16_sdwa v81, v154 dst_sel:DWORD dst_unused:UNUSED_PAD src0_sel:WORD_1
	v_cvt_f32_f16_e32 v82, v155
	v_cvt_f32_f16_sdwa v83, v155 dst_sel:DWORD dst_unused:UNUSED_PAD src0_sel:WORD_1
	v_sub_f32_e32 v72, v72, v200
	v_sub_f32_e32 v73, v73, v200
	v_sub_f32_e32 v74, v74, v200
	v_sub_f32_e32 v75, v75, v200
	v_sub_f32_e32 v80, v80, v200
	v_sub_f32_e32 v81, v81, v200
	v_sub_f32_e32 v82, v82, v200
	v_sub_f32_e32 v83, v83, v200
	v_pk_mul_f32 v[72:73], v[200:201], v[72:73] op_sel:[1,0]
	v_pk_mul_f32 v[74:75], v[200:201], v[74:75] op_sel:[1,0]
	v_pk_mul_f32 v[80:81], v[200:201], v[80:81] op_sel:[1,0]
	v_pk_mul_f32 v[82:83], v[200:201], v[82:83] op_sel:[1,0]
	v_pk_fma_f32 v[44:45], v[72:73], v[160:161], v[44:45]
	v_pk_fma_f32 v[46:47], v[74:75], v[162:163], v[46:47]
	v_pk_fma_f32 v[40:41], v[80:81], v[164:165], v[40:41]
	v_pk_fma_f32 v[42:43], v[82:83], v[166:167], v[42:43]
	v_cvt_pk_f16_f32 v44, v44, v45
	v_cvt_pk_f16_f32 v45, v46, v47
	v_cvt_pk_f16_f32 v46, v40, v41
	v_cvt_pk_f16_f32 v47, v42, v43
	s_waitcnt lgkmcnt(0)
	v_add_u32_e32 v83, 0x30000, v224
	buffer_store_dwordx4 v[124:127], v83, s[24:27], 0 offen sc1
	v_add_u32_e32 v82, 0x33000, v224
	buffer_store_dwordx4 v[116:119], v82, s[24:27], 0 offen sc1
	ds_write_b128 v235, v[44:47]
	v_fma_mix_f32 v208, v44, 1.0, 0 op_sel_hi:[1,0,0]
	v_fma_mix_f32 v209, v44, v44, 0 op_sel_hi:[1,1,0]
	v_fma_mix_f32 v208, v44, 1.0, v208 op_sel:[1,0,0] op_sel_hi:[1,0,0]
	v_fma_mix_f32 v209, v44, v44, v209 op_sel:[1,1,0] op_sel_hi:[1,1,0]
	v_fma_mix_f32 v208, v45, 1.0, v208 op_sel_hi:[1,0,0]
	v_fma_mix_f32 v209, v45, v45, v209 op_sel_hi:[1,1,0]
	v_fma_mix_f32 v208, v45, 1.0, v208 op_sel:[1,0,0] op_sel_hi:[1,0,0]
	v_fma_mix_f32 v209, v45, v45, v209 op_sel:[1,1,0] op_sel_hi:[1,1,0]
	v_fma_mix_f32 v208, v46, 1.0, v208 op_sel_hi:[1,0,0]
	v_fma_mix_f32 v209, v46, v46, v209 op_sel_hi:[1,1,0]
	v_fma_mix_f32 v208, v46, 1.0, v208 op_sel:[1,0,0] op_sel_hi:[1,0,0]
	v_fma_mix_f32 v209, v46, v46, v209 op_sel:[1,1,0] op_sel_hi:[1,1,0]
	v_fma_mix_f32 v208, v47, 1.0, v208 op_sel_hi:[1,0,0]
	v_fma_mix_f32 v209, v47, v47, v209 op_sel_hi:[1,1,0]
	v_fma_mix_f32 v208, v47, 1.0, v208 op_sel:[1,0,0] op_sel_hi:[1,0,0]
	v_fma_mix_f32 v209, v47, v47, v209 op_sel:[1,1,0] op_sel_hi:[1,1,0]
	s_waitcnt vmcnt(14)
	v_cvt_f32_f16_e32 v72, v156
	v_cvt_f32_f16_sdwa v73, v156 dst_sel:DWORD dst_unused:UNUSED_PAD src0_sel:WORD_1
	v_cvt_f32_f16_e32 v74, v157
	v_cvt_f32_f16_sdwa v75, v157 dst_sel:DWORD dst_unused:UNUSED_PAD src0_sel:WORD_1
	v_cvt_f32_f16_e32 v80, v158
	v_cvt_f32_f16_sdwa v81, v158 dst_sel:DWORD dst_unused:UNUSED_PAD src0_sel:WORD_1
	v_cvt_f32_f16_e32 v82, v159
	v_cvt_f32_f16_sdwa v83, v159 dst_sel:DWORD dst_unused:UNUSED_PAD src0_sel:WORD_1
	v_sub_f32_e32 v72, v72, v200
	v_sub_f32_e32 v73, v73, v200
	v_sub_f32_e32 v74, v74, v200
	v_sub_f32_e32 v75, v75, v200
	v_sub_f32_e32 v80, v80, v200
	v_sub_f32_e32 v81, v81, v200
	v_sub_f32_e32 v82, v82, v200
	v_sub_f32_e32 v83, v83, v200
	v_pk_mul_f32 v[72:73], v[200:201], v[72:73] op_sel:[1,0]
	v_pk_mul_f32 v[74:75], v[200:201], v[74:75] op_sel:[1,0]
	v_pk_mul_f32 v[80:81], v[200:201], v[80:81] op_sel:[1,0]
	v_pk_mul_f32 v[82:83], v[200:201], v[82:83] op_sel:[1,0]
	v_pk_fma_f32 v[36:37], v[72:73], v[168:169], v[36:37]
	v_pk_fma_f32 v[38:39], v[74:75], v[170:171], v[38:39]
	v_pk_fma_f32 v[32:33], v[80:81], v[172:173], v[32:33]
	v_pk_fma_f32 v[34:35], v[82:83], v[174:175], v[34:35]
	v_cvt_pk_f16_f32 v36, v36, v37
	v_cvt_pk_f16_f32 v37, v38, v39
	v_cvt_pk_f16_f32 v38, v32, v33
	v_cvt_pk_f16_f32 v39, v34, v35
	ds_write_b128 v235, v[36:39] offset:64
	v_fma_mix_f32 v208, v36, 1.0, v208 op_sel_hi:[1,0,0]
	v_fma_mix_f32 v209, v36, v36, v209 op_sel_hi:[1,1,0]
	v_fma_mix_f32 v208, v36, 1.0, v208 op_sel:[1,0,0] op_sel_hi:[1,0,0]
	v_fma_mix_f32 v209, v36, v36, v209 op_sel:[1,1,0] op_sel_hi:[1,1,0]
	v_fma_mix_f32 v208, v37, 1.0, v208 op_sel_hi:[1,0,0]
	v_fma_mix_f32 v209, v37, v37, v209 op_sel_hi:[1,1,0]
	v_fma_mix_f32 v208, v37, 1.0, v208 op_sel:[1,0,0] op_sel_hi:[1,0,0]
	v_fma_mix_f32 v209, v37, v37, v209 op_sel:[1,1,0] op_sel_hi:[1,1,0]
	v_fma_mix_f32 v208, v38, 1.0, v208 op_sel_hi:[1,0,0]
	v_fma_mix_f32 v209, v38, v38, v209 op_sel_hi:[1,1,0]
	v_fma_mix_f32 v208, v38, 1.0, v208 op_sel:[1,0,0] op_sel_hi:[1,0,0]
	v_fma_mix_f32 v209, v38, v38, v209 op_sel:[1,1,0] op_sel_hi:[1,1,0]
	v_fma_mix_f32 v208, v39, 1.0, v208 op_sel_hi:[1,0,0]
	v_fma_mix_f32 v209, v39, v39, v209 op_sel_hi:[1,1,0]
	v_fma_mix_f32 v208, v39, 1.0, v208 op_sel:[1,0,0] op_sel_hi:[1,0,0]
	v_fma_mix_f32 v209, v39, v39, v209 op_sel:[1,1,0] op_sel_hi:[1,1,0]
	ds_read_b128 v[128:131], v236
	ds_read_b128 v[104:107], v236 offset:1152
	s_waitcnt vmcnt(11)
	v_cvt_f32_f16_e32 v72, v212
	v_cvt_f32_f16_sdwa v73, v212 dst_sel:DWORD dst_unused:UNUSED_PAD src0_sel:WORD_1
	v_cvt_f32_f16_e32 v74, v213
	v_cvt_f32_f16_sdwa v75, v213 dst_sel:DWORD dst_unused:UNUSED_PAD src0_sel:WORD_1
	v_cvt_f32_f16_e32 v80, v214
	v_cvt_f32_f16_sdwa v81, v214 dst_sel:DWORD dst_unused:UNUSED_PAD src0_sel:WORD_1
	v_cvt_f32_f16_e32 v82, v215
	v_cvt_f32_f16_sdwa v83, v215 dst_sel:DWORD dst_unused:UNUSED_PAD src0_sel:WORD_1
	v_sub_f32_e32 v72, v72, v202
	v_sub_f32_e32 v73, v73, v202
	v_sub_f32_e32 v74, v74, v202
	v_sub_f32_e32 v75, v75, v202
	v_sub_f32_e32 v80, v80, v202
	v_sub_f32_e32 v81, v81, v202
	v_sub_f32_e32 v82, v82, v202
	v_sub_f32_e32 v83, v83, v202
	v_pk_mul_f32 v[72:73], v[202:203], v[72:73] op_sel:[1,0]
	v_pk_mul_f32 v[74:75], v[202:203], v[74:75] op_sel:[1,0]
	v_pk_mul_f32 v[80:81], v[202:203], v[80:81] op_sel:[1,0]
	v_pk_mul_f32 v[82:83], v[202:203], v[82:83] op_sel:[1,0]
	v_pk_fma_f32 v[28:29], v[72:73], v[160:161], v[28:29]
	v_pk_fma_f32 v[30:31], v[74:75], v[162:163], v[30:31]
	v_pk_fma_f32 v[24:25], v[80:81], v[164:165], v[24:25]
	v_pk_fma_f32 v[26:27], v[82:83], v[166:167], v[26:27]
	v_cvt_pk_f16_f32 v28, v28, v29
	v_cvt_pk_f16_f32 v29, v30, v31
	v_cvt_pk_f16_f32 v30, v24, v25
	v_cvt_pk_f16_f32 v31, v26, v27
	s_waitcnt lgkmcnt(0)
	v_add_u32_e32 v83, 0x36000, v224
	buffer_store_dwordx4 v[128:131], v83, s[24:27], 0 offen sc1
	v_add_u32_e32 v82, 0x39000, v224
	buffer_store_dwordx4 v[104:107], v82, s[24:27], 0 offen sc1
	ds_write_b128 v235, v[28:31]
	v_fma_mix_f32 v210, v28, 1.0, 0 op_sel_hi:[1,0,0]
	v_fma_mix_f32 v211, v28, v28, 0 op_sel_hi:[1,1,0]
	v_fma_mix_f32 v210, v28, 1.0, v210 op_sel:[1,0,0] op_sel_hi:[1,0,0]
	v_fma_mix_f32 v211, v28, v28, v211 op_sel:[1,1,0] op_sel_hi:[1,1,0]
	v_fma_mix_f32 v210, v29, 1.0, v210 op_sel_hi:[1,0,0]
	v_fma_mix_f32 v211, v29, v29, v211 op_sel_hi:[1,1,0]
	v_fma_mix_f32 v210, v29, 1.0, v210 op_sel:[1,0,0] op_sel_hi:[1,0,0]
	v_fma_mix_f32 v211, v29, v29, v211 op_sel:[1,1,0] op_sel_hi:[1,1,0]
	v_fma_mix_f32 v210, v30, 1.0, v210 op_sel_hi:[1,0,0]
	v_fma_mix_f32 v211, v30, v30, v211 op_sel_hi:[1,1,0]
	v_fma_mix_f32 v210, v30, 1.0, v210 op_sel:[1,0,0] op_sel_hi:[1,0,0]
	v_fma_mix_f32 v211, v30, v30, v211 op_sel:[1,1,0] op_sel_hi:[1,1,0]
	v_fma_mix_f32 v210, v31, 1.0, v210 op_sel_hi:[1,0,0]
	v_fma_mix_f32 v211, v31, v31, v211 op_sel_hi:[1,1,0]
	v_fma_mix_f32 v210, v31, 1.0, v210 op_sel:[1,0,0] op_sel_hi:[1,0,0]
	v_fma_mix_f32 v211, v31, v31, v211 op_sel:[1,1,0] op_sel_hi:[1,1,0]
	s_waitcnt vmcnt(12)
	v_cvt_f32_f16_e32 v72, v144
	v_cvt_f32_f16_sdwa v73, v144 dst_sel:DWORD dst_unused:UNUSED_PAD src0_sel:WORD_1
	v_cvt_f32_f16_e32 v74, v145
	v_cvt_f32_f16_sdwa v75, v145 dst_sel:DWORD dst_unused:UNUSED_PAD src0_sel:WORD_1
	v_cvt_f32_f16_e32 v80, v146
	v_cvt_f32_f16_sdwa v81, v146 dst_sel:DWORD dst_unused:UNUSED_PAD src0_sel:WORD_1
	v_cvt_f32_f16_e32 v82, v147
	v_cvt_f32_f16_sdwa v83, v147 dst_sel:DWORD dst_unused:UNUSED_PAD src0_sel:WORD_1
	v_sub_f32_e32 v72, v72, v202
	v_sub_f32_e32 v73, v73, v202
	v_sub_f32_e32 v74, v74, v202
	v_sub_f32_e32 v75, v75, v202
	v_sub_f32_e32 v80, v80, v202
	v_sub_f32_e32 v81, v81, v202
	v_sub_f32_e32 v82, v82, v202
	v_sub_f32_e32 v83, v83, v202
	v_pk_mul_f32 v[72:73], v[202:203], v[72:73] op_sel:[1,0]
	v_pk_mul_f32 v[74:75], v[202:203], v[74:75] op_sel:[1,0]
	v_pk_mul_f32 v[80:81], v[202:203], v[80:81] op_sel:[1,0]
	v_pk_mul_f32 v[82:83], v[202:203], v[82:83] op_sel:[1,0]
	v_pk_fma_f32 v[20:21], v[72:73], v[168:169], v[20:21]
	v_pk_fma_f32 v[22:23], v[74:75], v[170:171], v[22:23]
	v_pk_fma_f32 v[16:17], v[80:81], v[172:173], v[16:17]
	v_pk_fma_f32 v[18:19], v[82:83], v[174:175], v[18:19]
	v_cvt_pk_f16_f32 v20, v20, v21
	v_cvt_pk_f16_f32 v21, v22, v23
	v_cvt_pk_f16_f32 v22, v16, v17
	v_cvt_pk_f16_f32 v23, v18, v19
	ds_write_b128 v235, v[20:23] offset:64
	v_fma_mix_f32 v210, v20, 1.0, v210 op_sel_hi:[1,0,0]
	v_fma_mix_f32 v211, v20, v20, v211 op_sel_hi:[1,1,0]
	v_fma_mix_f32 v210, v20, 1.0, v210 op_sel:[1,0,0] op_sel_hi:[1,0,0]
	v_fma_mix_f32 v211, v20, v20, v211 op_sel:[1,1,0] op_sel_hi:[1,1,0]
	v_fma_mix_f32 v210, v21, 1.0, v210 op_sel_hi:[1,0,0]
	v_fma_mix_f32 v211, v21, v21, v211 op_sel_hi:[1,1,0]
	v_fma_mix_f32 v210, v21, 1.0, v210 op_sel:[1,0,0] op_sel_hi:[1,0,0]
	v_fma_mix_f32 v211, v21, v21, v211 op_sel:[1,1,0] op_sel_hi:[1,1,0]
	v_fma_mix_f32 v210, v22, 1.0, v210 op_sel_hi:[1,0,0]
	v_fma_mix_f32 v211, v22, v22, v211 op_sel_hi:[1,1,0]
	v_fma_mix_f32 v210, v22, 1.0, v210 op_sel:[1,0,0] op_sel_hi:[1,0,0]
	v_fma_mix_f32 v211, v22, v22, v211 op_sel:[1,1,0] op_sel_hi:[1,1,0]
	v_fma_mix_f32 v210, v23, 1.0, v210 op_sel_hi:[1,0,0]
	v_fma_mix_f32 v211, v23, v23, v211 op_sel_hi:[1,1,0]
	v_fma_mix_f32 v210, v23, 1.0, v210 op_sel:[1,0,0] op_sel_hi:[1,0,0]
	v_fma_mix_f32 v211, v23, v23, v211 op_sel:[1,1,0] op_sel_hi:[1,1,0]
	ds_read_b128 v[240:243], v236
	ds_read_b128 v[96:99], v236 offset:1152
	s_waitcnt vmcnt(11)
	v_cvt_f32_f16_e32 v72, v132
	v_cvt_f32_f16_sdwa v73, v132 dst_sel:DWORD dst_unused:UNUSED_PAD src0_sel:WORD_1
	v_cvt_f32_f16_e32 v74, v133
	v_cvt_f32_f16_sdwa v75, v133 dst_sel:DWORD dst_unused:UNUSED_PAD src0_sel:WORD_1
	v_cvt_f32_f16_e32 v80, v134
	v_cvt_f32_f16_sdwa v81, v134 dst_sel:DWORD dst_unused:UNUSED_PAD src0_sel:WORD_1
	v_cvt_f32_f16_e32 v82, v135
	v_cvt_f32_f16_sdwa v83, v135 dst_sel:DWORD dst_unused:UNUSED_PAD src0_sel:WORD_1
	v_sub_f32_e32 v72, v72, v204
	v_sub_f32_e32 v73, v73, v204
	v_sub_f32_e32 v74, v74, v204
	v_sub_f32_e32 v75, v75, v204
	v_sub_f32_e32 v80, v80, v204
	v_sub_f32_e32 v81, v81, v204
	v_sub_f32_e32 v82, v82, v204
	v_sub_f32_e32 v83, v83, v204
	v_pk_mul_f32 v[72:73], v[204:205], v[72:73] op_sel:[1,0]
	v_pk_mul_f32 v[74:75], v[204:205], v[74:75] op_sel:[1,0]
	v_pk_mul_f32 v[80:81], v[204:205], v[80:81] op_sel:[1,0]
	v_pk_mul_f32 v[82:83], v[204:205], v[82:83] op_sel:[1,0]
	v_pk_fma_f32 v[12:13], v[72:73], v[160:161], v[12:13]
	v_pk_fma_f32 v[14:15], v[74:75], v[162:163], v[14:15]
	v_pk_fma_f32 v[8:9], v[80:81], v[164:165], v[8:9]
	v_pk_fma_f32 v[10:11], v[82:83], v[166:167], v[10:11]
	v_cvt_pk_f16_f32 v12, v12, v13
	v_cvt_pk_f16_f32 v13, v14, v15
	v_cvt_pk_f16_f32 v14, v8, v9
	v_cvt_pk_f16_f32 v15, v10, v11
	s_waitcnt lgkmcnt(0)
	v_add_u32_e32 v83, 0x3c000, v224
	buffer_store_dwordx4 v[240:243], v83, s[24:27], 0 offen sc1
	v_add_u32_e32 v82, 0x3f000, v224
	buffer_store_dwordx4 v[96:99], v82, s[24:27], 0 offen sc1
	ds_write_b128 v235, v[12:15]
	v_fma_mix_f32 v244, v12, 1.0, 0 op_sel_hi:[1,0,0]
	v_fma_mix_f32 v245, v12, v12, 0 op_sel_hi:[1,1,0]
	v_fma_mix_f32 v244, v12, 1.0, v244 op_sel:[1,0,0] op_sel_hi:[1,0,0]
	v_fma_mix_f32 v245, v12, v12, v245 op_sel:[1,1,0] op_sel_hi:[1,1,0]
	v_fma_mix_f32 v244, v13, 1.0, v244 op_sel_hi:[1,0,0]
	v_fma_mix_f32 v245, v13, v13, v245 op_sel_hi:[1,1,0]
	v_fma_mix_f32 v244, v13, 1.0, v244 op_sel:[1,0,0] op_sel_hi:[1,0,0]
	v_fma_mix_f32 v245, v13, v13, v245 op_sel:[1,1,0] op_sel_hi:[1,1,0]
	v_fma_mix_f32 v244, v14, 1.0, v244 op_sel_hi:[1,0,0]
	v_fma_mix_f32 v245, v14, v14, v245 op_sel_hi:[1,1,0]
	v_fma_mix_f32 v244, v14, 1.0, v244 op_sel:[1,0,0] op_sel_hi:[1,0,0]
	v_fma_mix_f32 v245, v14, v14, v245 op_sel:[1,1,0] op_sel_hi:[1,1,0]
	v_fma_mix_f32 v244, v15, 1.0, v244 op_sel_hi:[1,0,0]
	v_fma_mix_f32 v245, v15, v15, v245 op_sel_hi:[1,1,0]
	v_fma_mix_f32 v244, v15, 1.0, v244 op_sel:[1,0,0] op_sel_hi:[1,0,0]
	v_fma_mix_f32 v245, v15, v15, v245 op_sel:[1,1,0] op_sel_hi:[1,1,0]
	s_waitcnt vmcnt(12)
	v_cvt_f32_f16_e32 v72, v88
	v_cvt_f32_f16_sdwa v73, v88 dst_sel:DWORD dst_unused:UNUSED_PAD src0_sel:WORD_1
	v_cvt_f32_f16_e32 v74, v89
	v_cvt_f32_f16_sdwa v75, v89 dst_sel:DWORD dst_unused:UNUSED_PAD src0_sel:WORD_1
	v_cvt_f32_f16_e32 v80, v90
	v_cvt_f32_f16_sdwa v81, v90 dst_sel:DWORD dst_unused:UNUSED_PAD src0_sel:WORD_1
	v_cvt_f32_f16_e32 v82, v91
	v_cvt_f32_f16_sdwa v83, v91 dst_sel:DWORD dst_unused:UNUSED_PAD src0_sel:WORD_1
	v_sub_f32_e32 v72, v72, v204
	v_sub_f32_e32 v73, v73, v204
	v_sub_f32_e32 v74, v74, v204
	v_sub_f32_e32 v75, v75, v204
	v_sub_f32_e32 v80, v80, v204
	v_sub_f32_e32 v81, v81, v204
	v_sub_f32_e32 v82, v82, v204
	v_sub_f32_e32 v83, v83, v204
	v_pk_mul_f32 v[72:73], v[204:205], v[72:73] op_sel:[1,0]
	v_pk_mul_f32 v[74:75], v[204:205], v[74:75] op_sel:[1,0]
	v_pk_mul_f32 v[80:81], v[204:205], v[80:81] op_sel:[1,0]
	v_pk_mul_f32 v[82:83], v[204:205], v[82:83] op_sel:[1,0]
	v_pk_fma_f32 v[4:5], v[72:73], v[168:169], v[4:5]
	v_pk_fma_f32 v[6:7], v[74:75], v[170:171], v[6:7]
	v_pk_fma_f32 v[0:1], v[80:81], v[172:173], v[0:1]
	v_pk_fma_f32 v[2:3], v[82:83], v[174:175], v[2:3]
	v_cvt_pk_f16_f32 v4, v4, v5
	v_cvt_pk_f16_f32 v5, v6, v7
	v_cvt_pk_f16_f32 v6, v0, v1
	v_cvt_pk_f16_f32 v7, v2, v3
	ds_write_b128 v235, v[4:7] offset:64
	v_fma_mix_f32 v244, v4, 1.0, v244 op_sel_hi:[1,0,0]
	v_fma_mix_f32 v245, v4, v4, v245 op_sel_hi:[1,1,0]
	v_fma_mix_f32 v244, v4, 1.0, v244 op_sel:[1,0,0] op_sel_hi:[1,0,0]
	v_fma_mix_f32 v245, v4, v4, v245 op_sel:[1,1,0] op_sel_hi:[1,1,0]
	v_fma_mix_f32 v244, v5, 1.0, v244 op_sel_hi:[1,0,0]
	v_fma_mix_f32 v245, v5, v5, v245 op_sel_hi:[1,1,0]
	v_fma_mix_f32 v244, v5, 1.0, v244 op_sel:[1,0,0] op_sel_hi:[1,0,0]
	v_fma_mix_f32 v245, v5, v5, v245 op_sel:[1,1,0] op_sel_hi:[1,1,0]
	v_fma_mix_f32 v244, v6, 1.0, v244 op_sel_hi:[1,0,0]
	v_fma_mix_f32 v245, v6, v6, v245 op_sel_hi:[1,1,0]
	v_fma_mix_f32 v244, v6, 1.0, v244 op_sel:[1,0,0] op_sel_hi:[1,0,0]
	v_fma_mix_f32 v245, v6, v6, v245 op_sel:[1,1,0] op_sel_hi:[1,1,0]
	v_fma_mix_f32 v244, v7, 1.0, v244 op_sel_hi:[1,0,0]
	v_fma_mix_f32 v245, v7, v7, v245 op_sel_hi:[1,1,0]
	v_fma_mix_f32 v244, v7, 1.0, v244 op_sel:[1,0,0] op_sel_hi:[1,0,0]
	v_fma_mix_f32 v245, v7, v7, v245 op_sel:[1,1,0] op_sel_hi:[1,1,0]
	ds_read_b128 v[108:111], v236
	ds_read_b128 v[100:103], v236 offset:1152
	s_waitcnt lgkmcnt(0)
	v_add_u32_e32 v83, 0x42000, v224
	buffer_store_dwordx4 v[108:111], v83, s[24:27], 0 offen sc1
	v_add_u32_e32 v82, 0x45000, v224
	buffer_store_dwordx4 v[100:103], v82, s[24:27], 0 offen sc1
	v_xor_b32_e32 v225, 16, v234
	v_lshlrev_b32_e32 v225, 2, v225
	v_xor_b32_e32 v246, 32, v234
	v_lshlrev_b32_e32 v246, 2, v246
	ds_bpermute_b32 v92, v225, v206
	ds_bpermute_b32 v93, v225, v207
	ds_bpermute_b32 v94, v225, v140
	ds_bpermute_b32 v95, v225, v141
	ds_bpermute_b32 v120, v225, v142
	ds_bpermute_b32 v121, v225, v143
	ds_bpermute_b32 v122, v225, v216
	ds_bpermute_b32 v123, v225, v217
	s_waitcnt lgkmcnt(0)
	v_pk_add_f32 v[206:207], v[206:207], v[92:93]
	v_pk_add_f32 v[140:141], v[140:141], v[94:95]
	v_pk_add_f32 v[142:143], v[142:143], v[120:121]
	v_pk_add_f32 v[216:217], v[216:217], v[122:123]
	ds_bpermute_b32 v92, v225, v218
	ds_bpermute_b32 v93, v225, v219
	ds_bpermute_b32 v94, v225, v208
	ds_bpermute_b32 v95, v225, v209
	ds_bpermute_b32 v120, v225, v210
	ds_bpermute_b32 v121, v225, v211
	ds_bpermute_b32 v122, v225, v244
	ds_bpermute_b32 v123, v225, v245
	s_waitcnt lgkmcnt(0)
	v_pk_add_f32 v[218:219], v[218:219], v[92:93]
	v_pk_add_f32 v[208:209], v[208:209], v[94:95]
	v_pk_add_f32 v[210:211], v[210:211], v[120:121]
	v_pk_add_f32 v[244:245], v[244:245], v[122:123]
	ds_bpermute_b32 v92, v246, v206
	ds_bpermute_b32 v93, v246, v207
	ds_bpermute_b32 v94, v246, v140
	ds_bpermute_b32 v95, v246, v141
	ds_bpermute_b32 v120, v246, v142
	ds_bpermute_b32 v121, v246, v143
	ds_bpermute_b32 v122, v246, v216
	ds_bpermute_b32 v123, v246, v217
	s_waitcnt lgkmcnt(0)
	v_pk_add_f32 v[206:207], v[206:207], v[92:93]
	v_pk_add_f32 v[140:141], v[140:141], v[94:95]
	v_pk_add_f32 v[142:143], v[142:143], v[120:121]
	v_pk_add_f32 v[216:217], v[216:217], v[122:123]
	ds_bpermute_b32 v92, v246, v218
	ds_bpermute_b32 v93, v246, v219
	ds_bpermute_b32 v94, v246, v208
	ds_bpermute_b32 v95, v246, v209
	ds_bpermute_b32 v120, v246, v210
	ds_bpermute_b32 v121, v246, v211
	ds_bpermute_b32 v122, v246, v244
	ds_bpermute_b32 v123, v246, v245
	s_waitcnt lgkmcnt(0)
	v_pk_add_f32 v[218:219], v[218:219], v[92:93]
	v_pk_add_f32 v[208:209], v[208:209], v[94:95]
	v_pk_add_f32 v[210:211], v[210:211], v[120:121]
	v_pk_add_f32 v[244:245], v[244:245], v[122:123]
	s_mov_b64 exec, 0xffff
	global_store_dwordx2 v190, v[206:207], s[100:101] offset:0
	global_store_dwordx2 v190, v[140:141], s[100:101] offset:128
	global_store_dwordx2 v190, v[142:143], s[100:101] offset:256
	global_store_dwordx2 v190, v[216:217], s[100:101] offset:384
	global_store_dwordx2 v190, v[218:219], s[100:101] offset:1024
	global_store_dwordx2 v190, v[208:209], s[100:101] offset:1152
	global_store_dwordx2 v190, v[210:211], s[100:101] offset:1280
	global_store_dwordx2 v190, v[244:245], s[100:101] offset:1408
	s_mov_b64 exec, -1
	s_mov_b32 s83, s81
	s_mov_b32 s84, s82
	s_mov_b64 s[40:41], s[0:1]
	s_mov_b64 s[38:39], s[8:9]
	s_mov_b64 vcc, s[6:7]
	s_cbranch_vccz .LBB8_12
	s_waitcnt vmcnt(0)
	s_cmpk_gt_u32 s44, 0xff
	s_cbranch_scc1 .LBB8_31
	s_barrier

.LBB9_27:
	s_add_u32 s30, s28, 0xfffd0080
	s_addc_u32 s31, s29, -1
	s_cmp_eq_u32 s73, 8
	s_cselect_b32 s35, s9, s31
	s_cselect_b32 s34, s8, s30
	s_cselect_b32 s31, s1, s72
	s_cselect_b32 s30, s0, s71
	s_add_i32 m0, s43, 0xc000
	ds_read_b128 v[158:161], v173
	ds_read_b128 v[162:165], v173 offset:1024
	ds_read_b128 v[178:181], v173 offset:2048
	ds_read_b128 v[182:185], v173 offset:3072
	ds_read_b128 v[186:189], v173 offset:4096
	ds_read_b128 v[190:193], v173 offset:5120
	ds_read_b128 v[194:197], v173 offset:6144
	ds_read_b128 v[198:201], v173 offset:7168
	global_load_lds_dwordx4 v152, s[28:29]
	s_add_i32 m0, s43, 0xe000
	s_nop 0
	global_load_lds_dwordx4 v154, s[28:29]
	s_waitcnt lgkmcnt(8)
	s_barrier
	s_waitcnt lgkmcnt(0)
	v_mfma_f32_16x16x32_f16 v[124:127], v[128:131], v[158:161], v[124:127]
	v_mfma_f32_16x16x32_f16 v[120:123], v[136:139], v[158:161], v[120:123]
	v_mfma_f32_16x16x32_f16 v[108:111], v[128:131], v[178:181], v[108:111]
	v_mfma_f32_16x16x32_f16 v[104:107], v[136:139], v[178:181], v[104:107]
	v_mfma_f32_16x16x32_f16 v[96:99], v[128:131], v[186:189], v[96:99]
	v_mfma_f32_16x16x32_f16 v[88:91], v[136:139], v[186:189], v[88:91]
	v_mfma_f32_16x16x32_f16 v[80:83], v[128:131], v[194:197], v[80:83]
	v_mfma_f32_16x16x32_f16 v[72:75], v[136:139], v[194:197], v[72:75]
	v_mfma_f32_16x16x32_f16 v[124:127], v[132:135], v[162:165], v[124:127]
	v_mfma_f32_16x16x32_f16 v[120:123], v[140:143], v[162:165], v[120:123]
	v_mfma_f32_16x16x32_f16 v[108:111], v[132:135], v[182:185], v[108:111]
	v_mfma_f32_16x16x32_f16 v[104:107], v[140:143], v[182:185], v[104:107]
	v_mfma_f32_16x16x32_f16 v[96:99], v[132:135], v[190:193], v[96:99]
	v_mfma_f32_16x16x32_f16 v[88:91], v[140:143], v[190:193], v[88:91]
	v_mfma_f32_16x16x32_f16 v[80:83], v[132:135], v[198:201], v[80:83]
	v_mfma_f32_16x16x32_f16 v[72:75], v[140:143], v[198:201], v[72:75]
	s_barrier
	s_add_i32 s74, s65, s42
	s_add_u32 s78, s30, 0x80
	s_addc_u32 s79, s31, 0
	s_mov_b32 m0, s74
	ds_read_b128 v[202:205], v174
	ds_read_b128 v[206:209], v174 offset:1024
	ds_read_b128 v[210:213], v174 offset:2048
	ds_read_b128 v[214:217], v174 offset:3072
	global_load_lds_dwordx4 v146, s[30:31]
	s_add_i32 m0, s74, 0x2000
	s_nop 0
	global_load_lds_dwordx4 v150, s[30:31]
	s_barrier
	s_waitcnt lgkmcnt(0)
	v_mfma_f32_16x16x32_f16 v[116:119], v[202:205], v[158:161], v[116:119]
	v_mfma_f32_16x16x32_f16 v[112:115], v[210:213], v[158:161], v[112:115]
	v_mfma_f32_16x16x32_f16 v[100:103], v[202:205], v[178:181], v[100:103]
	v_mfma_f32_16x16x32_f16 v[92:95], v[210:213], v[178:181], v[92:95]
	v_mfma_f32_16x16x32_f16 v[84:87], v[202:205], v[186:189], v[84:87]
	v_mfma_f32_16x16x32_f16 v[76:79], v[210:213], v[186:189], v[76:79]
	v_mfma_f32_16x16x32_f16 v[68:71], v[202:205], v[194:197], v[68:71]
	v_mfma_f32_16x16x32_f16 v[64:67], v[210:213], v[194:197], v[64:67]
	v_mfma_f32_16x16x32_f16 v[116:119], v[206:209], v[162:165], v[116:119]
	v_mfma_f32_16x16x32_f16 v[112:115], v[214:217], v[162:165], v[112:115]
	v_mfma_f32_16x16x32_f16 v[100:103], v[206:209], v[182:185], v[100:103]
	v_mfma_f32_16x16x32_f16 v[92:95], v[214:217], v[182:185], v[92:95]
	v_mfma_f32_16x16x32_f16 v[84:87], v[206:209], v[190:193], v[84:87]
	v_mfma_f32_16x16x32_f16 v[76:79], v[214:217], v[190:193], v[76:79]
	v_mfma_f32_16x16x32_f16 v[68:71], v[206:209], v[198:201], v[68:71]
	v_mfma_f32_16x16x32_f16 v[64:67], v[214:217], v[198:201], v[64:67]
	s_barrier
	s_mov_b32 m0, s43
	s_add_u32 s80, s34, 0x80
	s_addc_u32 s81, s35, 0
	ds_read_b128 v[158:161], v173 offset:16384
	ds_read_b128 v[162:165], v173 offset:17408
	ds_read_b128 v[178:181], v173 offset:18432
	ds_read_b128 v[182:185], v173 offset:19456
	ds_read_b128 v[186:189], v173 offset:20480
	ds_read_b128 v[190:193], v173 offset:21504
	ds_read_b128 v[194:197], v173 offset:22528
	ds_read_b128 v[198:201], v173 offset:23552
	global_load_lds_dwordx4 v144, s[34:35]
	s_mov_b32 m0, s44
	s_nop 0
	global_load_lds_dwordx4 v148, s[34:35]
	s_waitcnt vmcnt(10)
	s_barrier
	s_waitcnt lgkmcnt(0)
	v_mfma_f32_16x16x32_f16 v[60:63], v[128:131], v[158:161], v[60:63]
	v_mfma_f32_16x16x32_f16 v[56:59], v[136:139], v[158:161], v[56:59]
	v_mfma_f32_16x16x32_f16 v[48:51], v[128:131], v[178:181], v[48:51]
	v_mfma_f32_16x16x32_f16 v[40:43], v[136:139], v[178:181], v[40:43]
	v_mfma_f32_16x16x32_f16 v[32:35], v[128:131], v[186:189], v[32:35]
	v_mfma_f32_16x16x32_f16 v[24:27], v[136:139], v[186:189], v[24:27]
	v_mfma_f32_16x16x32_f16 v[16:19], v[128:131], v[194:197], v[16:19]
	v_mfma_f32_16x16x32_f16 v[8:11], v[136:139], v[194:197], v[8:11]
	v_mfma_f32_16x16x32_f16 v[60:63], v[132:135], v[162:165], v[60:63]
	v_mfma_f32_16x16x32_f16 v[56:59], v[140:143], v[162:165], v[56:59]
	v_mfma_f32_16x16x32_f16 v[48:51], v[132:135], v[182:185], v[48:51]
	v_mfma_f32_16x16x32_f16 v[40:43], v[140:143], v[182:185], v[40:43]
	v_mfma_f32_16x16x32_f16 v[32:35], v[132:135], v[190:193], v[32:35]
	v_mfma_f32_16x16x32_f16 v[24:27], v[140:143], v[190:193], v[24:27]
	v_mfma_f32_16x16x32_f16 v[16:19], v[132:135], v[198:201], v[16:19]
	v_mfma_f32_16x16x32_f16 v[8:11], v[140:143], v[198:201], v[8:11]
	s_barrier
	s_add_u32 s74, s30, 0xc000
	s_addc_u32 s75, s31, 0
	s_add_i32 s76, s66, s42
	s_mov_b32 m0, s76
	s_nop 0
	global_load_lds_dwordx4 v146, s[74:75]
	s_add_i32 m0, s76, 0x2000
	s_nop 0
	global_load_lds_dwordx4 v150, s[74:75]
	s_add_i32 s74, 0, 0x18000
	v_add_u32_e32 v140, s74, v168
	ds_read_b128 v[128:131], v140
	ds_read_b128 v[132:135], v140 offset:1024
	ds_read_b128 v[136:139], v140 offset:2048
	ds_read_b128 v[140:143], v140 offset:3072
	s_waitcnt vmcnt(6)
	s_barrier
	v_mfma_f32_16x16x32_f16 v[52:55], v[202:205], v[158:161], v[52:55]
	v_mfma_f32_16x16x32_f16 v[44:47], v[210:213], v[158:161], v[44:47]
	v_mfma_f32_16x16x32_f16 v[36:39], v[202:205], v[178:181], v[36:39]
	v_mfma_f32_16x16x32_f16 v[28:31], v[210:213], v[178:181], v[28:31]
	v_mfma_f32_16x16x32_f16 v[20:23], v[202:205], v[186:189], v[20:23]
	v_mfma_f32_16x16x32_f16 v[12:15], v[210:213], v[186:189], v[12:15]
	v_mfma_f32_16x16x32_f16 v[4:7], v[202:205], v[194:197], v[4:7]
	v_mfma_f32_16x16x32_f16 v[0:3], v[210:213], v[194:197], v[0:3]
	v_mfma_f32_16x16x32_f16 v[52:55], v[206:209], v[162:165], v[52:55]
	v_mfma_f32_16x16x32_f16 v[44:47], v[214:217], v[162:165], v[44:47]
	v_mfma_f32_16x16x32_f16 v[36:39], v[206:209], v[182:185], v[36:39]
	v_mfma_f32_16x16x32_f16 v[28:31], v[214:217], v[182:185], v[28:31]
	v_mfma_f32_16x16x32_f16 v[20:23], v[206:209], v[190:193], v[20:23]
	v_mfma_f32_16x16x32_f16 v[12:15], v[214:217], v[190:193], v[12:15]
	v_mfma_f32_16x16x32_f16 v[4:7], v[206:209], v[198:201], v[4:7]
	v_mfma_f32_16x16x32_f16 v[0:3], v[214:217], v[198:201], v[0:3]
	s_barrier
	s_add_u32 s34, s34, 0x30000
	s_addc_u32 s35, s35, 0
	s_mov_b32 m0, s45
	ds_read_b128 v[158:161], v173 offset:32768
	ds_read_b128 v[162:165], v173 offset:33792
	ds_read_b128 v[178:181], v173 offset:34816
	ds_read_b128 v[182:185], v173 offset:35840
	ds_read_b128 v[186:189], v173 offset:36864
	ds_read_b128 v[190:193], v173 offset:37888
	ds_read_b128 v[194:197], v173 offset:38912
	ds_read_b128 v[198:201], v173 offset:39936
	global_load_lds_dwordx4 v144, s[34:35]
	s_mov_b32 m0, s46
	s_nop 0
	global_load_lds_dwordx4 v148, s[34:35]
	s_waitcnt lgkmcnt(8)
	s_barrier
	s_waitcnt lgkmcnt(0)
	v_mfma_f32_16x16x32_f16 v[124:127], v[128:131], v[158:161], v[124:127]
	v_mfma_f32_16x16x32_f16 v[120:123], v[136:139], v[158:161], v[120:123]
	v_mfma_f32_16x16x32_f16 v[108:111], v[128:131], v[178:181], v[108:111]
	v_mfma_f32_16x16x32_f16 v[104:107], v[136:139], v[178:181], v[104:107]
	v_mfma_f32_16x16x32_f16 v[96:99], v[128:131], v[186:189], v[96:99]
	v_mfma_f32_16x16x32_f16 v[88:91], v[136:139], v[186:189], v[88:91]
	v_mfma_f32_16x16x32_f16 v[80:83], v[128:131], v[194:197], v[80:83]
	v_mfma_f32_16x16x32_f16 v[72:75], v[136:139], v[194:197], v[72:75]
	v_mfma_f32_16x16x32_f16 v[124:127], v[132:135], v[162:165], v[124:127]
	v_mfma_f32_16x16x32_f16 v[120:123], v[140:143], v[162:165], v[120:123]
	v_mfma_f32_16x16x32_f16 v[108:111], v[132:135], v[182:185], v[108:111]
	v_mfma_f32_16x16x32_f16 v[104:107], v[140:143], v[182:185], v[104:107]
	v_mfma_f32_16x16x32_f16 v[96:99], v[132:135], v[190:193], v[96:99]
	v_mfma_f32_16x16x32_f16 v[88:91], v[140:143], v[190:193], v[88:91]
	v_mfma_f32_16x16x32_f16 v[80:83], v[132:135], v[198:201], v[80:83]
	v_mfma_f32_16x16x32_f16 v[72:75], v[140:143], v[198:201], v[72:75]
	s_barrier
	s_add_i32 s34, 0, 0x1c000
	s_add_i32 s35, s74, s42
	v_add_u32_e32 v177, s34, v168
	s_mov_b32 m0, s35
	ds_read_b128 v[202:205], v177
	ds_read_b128 v[206:209], v177 offset:1024
	ds_read_b128 v[210:213], v177 offset:2048
	ds_read_b128 v[214:217], v177 offset:3072
	global_load_lds_dwordx4 v146, s[78:79]
	s_add_i32 m0, s35, 0x2000
	s_nop 0
	global_load_lds_dwordx4 v150, s[78:79]
	s_barrier
	s_waitcnt lgkmcnt(0)
	v_mfma_f32_16x16x32_f16 v[116:119], v[202:205], v[158:161], v[116:119]
	v_mfma_f32_16x16x32_f16 v[112:115], v[210:213], v[158:161], v[112:115]
	v_mfma_f32_16x16x32_f16 v[100:103], v[202:205], v[178:181], v[100:103]
	v_mfma_f32_16x16x32_f16 v[92:95], v[210:213], v[178:181], v[92:95]
	v_mfma_f32_16x16x32_f16 v[84:87], v[202:205], v[186:189], v[84:87]
	v_mfma_f32_16x16x32_f16 v[76:79], v[210:213], v[186:189], v[76:79]
	v_mfma_f32_16x16x32_f16 v[68:71], v[202:205], v[194:197], v[68:71]
	v_mfma_f32_16x16x32_f16 v[64:67], v[210:213], v[194:197], v[64:67]
	v_mfma_f32_16x16x32_f16 v[116:119], v[206:209], v[162:165], v[116:119]
	v_mfma_f32_16x16x32_f16 v[112:115], v[214:217], v[162:165], v[112:115]
	v_mfma_f32_16x16x32_f16 v[100:103], v[206:209], v[182:185], v[100:103]
	v_mfma_f32_16x16x32_f16 v[92:95], v[214:217], v[182:185], v[92:95]
	v_mfma_f32_16x16x32_f16 v[84:87], v[206:209], v[190:193], v[84:87]
	v_mfma_f32_16x16x32_f16 v[76:79], v[214:217], v[190:193], v[76:79]
	v_mfma_f32_16x16x32_f16 v[68:71], v[206:209], v[198:201], v[68:71]
	v_mfma_f32_16x16x32_f16 v[64:67], v[214:217], v[198:201], v[64:67]
	s_barrier
	s_mov_b32 m0, s49
	ds_read_b128 v[158:161], v173 offset:49152
	ds_read_b128 v[162:165], v173 offset:50176
	ds_read_b128 v[178:181], v173 offset:51200
	ds_read_b128 v[182:185], v173 offset:52224
	ds_read_b128 v[186:189], v173 offset:53248
	ds_read_b128 v[190:193], v173 offset:54272
	ds_read_b128 v[194:197], v173 offset:55296
	ds_read_b128 v[198:201], v173 offset:56320
	global_load_lds_dwordx4 v144, s[80:81]
	s_mov_b32 m0, s50
	s_nop 0
	global_load_lds_dwordx4 v148, s[80:81]
	s_waitcnt vmcnt(10)
	s_barrier
	s_waitcnt lgkmcnt(0)
	v_mfma_f32_16x16x32_f16 v[60:63], v[128:131], v[158:161], v[60:63]
	v_mfma_f32_16x16x32_f16 v[56:59], v[136:139], v[158:161], v[56:59]
	v_mfma_f32_16x16x32_f16 v[48:51], v[128:131], v[178:181], v[48:51]
	v_mfma_f32_16x16x32_f16 v[40:43], v[136:139], v[178:181], v[40:43]
	v_mfma_f32_16x16x32_f16 v[32:35], v[128:131], v[186:189], v[32:35]
	v_mfma_f32_16x16x32_f16 v[24:27], v[136:139], v[186:189], v[24:27]
	v_mfma_f32_16x16x32_f16 v[16:19], v[128:131], v[194:197], v[16:19]
	v_mfma_f32_16x16x32_f16 v[8:11], v[136:139], v[194:197], v[8:11]
	v_mfma_f32_16x16x32_f16 v[60:63], v[132:135], v[162:165], v[60:63]
	v_mfma_f32_16x16x32_f16 v[56:59], v[140:143], v[162:165], v[56:59]
	v_mfma_f32_16x16x32_f16 v[48:51], v[132:135], v[182:185], v[48:51]
	v_mfma_f32_16x16x32_f16 v[40:43], v[140:143], v[182:185], v[40:43]
	v_mfma_f32_16x16x32_f16 v[32:35], v[132:135], v[190:193], v[32:35]
	v_mfma_f32_16x16x32_f16 v[24:27], v[140:143], v[190:193], v[24:27]
	v_mfma_f32_16x16x32_f16 v[16:19], v[132:135], v[198:201], v[16:19]
	v_mfma_f32_16x16x32_f16 v[8:11], v[140:143], v[198:201], v[8:11]
	s_barrier
	s_add_u32 s30, s30, 0xc080
	s_addc_u32 s31, s31, 0
	s_add_i32 s34, s34, s42
	s_mov_b32 m0, s34
	s_nop 0
	global_load_lds_dwordx4 v146, s[30:31]
	s_add_i32 m0, s34, 0x2000
	s_nop 0
	global_load_lds_dwordx4 v150, s[30:31]
	ds_read_b128 v[128:131], v172
	ds_read_b128 v[132:135], v172 offset:1024
	ds_read_b128 v[136:139], v172 offset:2048
	ds_read_b128 v[140:143], v172 offset:3072
	s_waitcnt vmcnt(6)
	s_barrier
	v_mfma_f32_16x16x32_f16 v[52:55], v[202:205], v[158:161], v[52:55]
	v_mfma_f32_16x16x32_f16 v[44:47], v[210:213], v[158:161], v[44:47]
	v_mfma_f32_16x16x32_f16 v[36:39], v[202:205], v[178:181], v[36:39]
	v_mfma_f32_16x16x32_f16 v[28:31], v[210:213], v[178:181], v[28:31]
	v_mfma_f32_16x16x32_f16 v[20:23], v[202:205], v[186:189], v[20:23]
	v_mfma_f32_16x16x32_f16 v[12:15], v[210:213], v[186:189], v[12:15]
	v_mfma_f32_16x16x32_f16 v[4:7], v[202:205], v[194:197], v[4:7]
	v_mfma_f32_16x16x32_f16 v[0:3], v[210:213], v[194:197], v[0:3]
	v_mfma_f32_16x16x32_f16 v[52:55], v[206:209], v[162:165], v[52:55]
	v_mfma_f32_16x16x32_f16 v[44:47], v[214:217], v[162:165], v[44:47]
	v_mfma_f32_16x16x32_f16 v[36:39], v[206:209], v[182:185], v[36:39]
	v_mfma_f32_16x16x32_f16 v[28:31], v[214:217], v[182:185], v[28:31]
	v_mfma_f32_16x16x32_f16 v[20:23], v[206:209], v[190:193], v[20:23]
	v_mfma_f32_16x16x32_f16 v[12:15], v[214:217], v[190:193], v[12:15]
	v_mfma_f32_16x16x32_f16 v[4:7], v[206:209], v[198:201], v[4:7]
	v_mfma_f32_16x16x32_f16 v[0:3], v[214:217], v[198:201], v[0:3]
	s_barrier
	s_add_i32 s73, s73, 2
	s_add_u32 s28, s28, 0x100
	s_addc_u32 s29, s29, 0
	s_add_u32 s71, s71, 0x100
	s_addc_u32 s72, s72, 0
	s_cmp_gt_u32 s73, 9
	s_cbranch_scc0 .LBB9_27
	s_lshl_b32 s28, s70, 8
	s_add_i32 s28, s28, s48
	s_lshl_b32 s29, s68, 8
	s_or_b32 s29, s29, s51
	s_waitcnt vmcnt(6)
	v_pk_fma_f32 v[126:127], v[126:127], v[226:227], v[236:237] op_sel_hi:[1,0,1]
	v_pk_fma_f32 v[124:125], v[124:125], v[226:227], v[234:235] op_sel_hi:[1,0,1]
	v_pk_fma_f32 v[122:123], v[122:123], v[226:227], v[240:241] op_sel_hi:[1,0,1]
	v_pk_fma_f32 v[120:121], v[120:121], v[226:227], v[238:239] op_sel_hi:[1,0,1]
	v_cvt_pk_f16_f32 v124, v124, v125
	v_cvt_pk_f16_f32 v125, v126, v127
	v_cvt_pk_f16_f32 v126, v120, v121
	v_cvt_pk_f16_f32 v123, v122, v123
	v_pk_fma_f32 v[118:119], v[118:119], v[226:227], v[244:245] op_sel_hi:[1,0,1]
	v_pk_fma_f32 v[116:117], v[116:117], v[226:227], v[242:243] op_sel_hi:[1,0,1]
	v_pk_fma_f32 v[114:115], v[114:115], v[226:227], v[248:249] op_sel_hi:[1,0,1]
	v_pk_fma_f32 v[112:113], v[112:113], v[226:227], v[246:247] op_sel_hi:[1,0,1]
	v_pk_max_f16 v120, v124, 0
	v_pk_max_f16 v121, v125, 0
	v_pk_max_f16 v122, v126, 0
	v_pk_max_f16 v123, v123, 0
	v_cvt_pk_f16_f32 v116, v116, v117
	v_cvt_pk_f16_f32 v117, v118, v119
	v_cvt_pk_f16_f32 v118, v112, v113
	v_cvt_pk_f16_f32 v115, v114, v115
	v_pk_fma_f32 v[110:111], v[110:111], v[226:227], v[236:237] op_sel:[0,1,0]
	v_pk_fma_f32 v[108:109], v[108:109], v[226:227], v[234:235] op_sel:[0,1,0]
	v_pk_fma_f32 v[106:107], v[106:107], v[226:227], v[240:241] op_sel:[0,1,0]
	v_pk_fma_f32 v[104:105], v[104:105], v[226:227], v[238:239] op_sel:[0,1,0]
	v_pk_fma_f32 v[102:103], v[102:103], v[226:227], v[244:245] op_sel:[0,1,0]
	v_pk_fma_f32 v[100:101], v[100:101], v[226:227], v[242:243] op_sel:[0,1,0]
	v_pk_fma_f32 v[94:95], v[94:95], v[226:227], v[248:249] op_sel:[0,1,0]
	v_pk_fma_f32 v[92:93], v[92:93], v[226:227], v[246:247] op_sel:[0,1,0]
	ds_write_b128 v175, v[120:123]
	v_or_b32_e32 v120, s28, v169
	v_pk_max_f16 v112, v116, 0
	v_pk_max_f16 v113, v117, 0
	v_pk_max_f16 v114, v118, 0
	v_pk_max_f16 v115, v115, 0
	v_cvt_pk_f16_f32 v108, v108, v109
	v_cvt_pk_f16_f32 v109, v110, v111
	v_cvt_pk_f16_f32 v110, v104, v105
	v_cvt_pk_f16_f32 v107, v106, v107
	v_cvt_pk_f16_f32 v100, v100, v101
	v_cvt_pk_f16_f32 v101, v102, v103
	v_cvt_pk_f16_f32 v102, v92, v93
	v_cvt_pk_f16_f32 v95, v94, v95
	ds_write_b128 v175, v[112:115] offset:64
	v_mul_lo_u32 v116, v120, s10
	v_pk_max_f16 v104, v108, 0
	v_pk_max_f16 v105, v109, 0
	v_pk_max_f16 v106, v110, 0
	v_pk_max_f16 v107, v107, 0
	v_pk_max_f16 v92, v100, 0
	v_pk_max_f16 v93, v101, 0
	v_pk_max_f16 v94, v102, 0
	v_pk_max_f16 v95, v95, 0
	ds_read_b128 v[112:115], v176
	v_add_u32_e32 v120, s29, v116
	ds_read_b128 v[116:119], v176 offset:1152
	ds_write_b128 v175, v[104:107]
	ds_write_b128 v175, v[92:95] offset:64
	ds_read_b128 v[92:95], v176
	ds_read_b128 v[100:103], v176 offset:1152
	v_lshlrev_b32_e32 v121, 1, v120
	v_add_u32_e32 v122, v121, v170
	v_add_u32_e32 v104, s55, v121
	s_waitcnt lgkmcnt(0)
	buffer_store_dwordx4 v[112:115], v122, s[20:23], 0 offen sc1
	v_add_u32_e32 v105, v104, v170
	v_pk_fma_f32 v[90:91], v[90:91], v[228:229], v[240:241] op_sel_hi:[1,0,1]
	v_add_u32_e32 v112, v121, v171
	buffer_store_dwordx4 v[116:119], v112, s[20:23], 0 offen sc1
	buffer_store_dwordx4 v[92:95], v105, s[20:23], 0 offen sc1
	v_pk_fma_f32 v[88:89], v[88:89], v[228:229], v[238:239] op_sel_hi:[1,0,1]
	v_pk_fma_f32 v[86:87], v[86:87], v[228:229], v[244:245] op_sel_hi:[1,0,1]
	v_pk_fma_f32 v[92:93], v[98:99], v[228:229], v[236:237] op_sel_hi:[1,0,1]
	v_pk_fma_f32 v[94:95], v[96:97], v[228:229], v[234:235] op_sel_hi:[1,0,1]
	v_pk_fma_f32 v[84:85], v[84:85], v[228:229], v[242:243] op_sel_hi:[1,0,1]
	v_pk_fma_f32 v[78:79], v[78:79], v[228:229], v[248:249] op_sel_hi:[1,0,1]
	v_pk_fma_f32 v[76:77], v[76:77], v[228:229], v[246:247] op_sel_hi:[1,0,1]
	v_cvt_pk_f16_f32 v94, v94, v95
	v_cvt_pk_f16_f32 v92, v92, v93
	v_cvt_pk_f16_f32 v93, v88, v89
	v_cvt_pk_f16_f32 v91, v90, v91
	v_cvt_pk_f16_f32 v84, v84, v85
	v_cvt_pk_f16_f32 v85, v86, v87
	v_cvt_pk_f16_f32 v86, v76, v77
	v_cvt_pk_f16_f32 v79, v78, v79
	v_pk_max_f16 v88, v94, 0
	v_pk_max_f16 v89, v92, 0
	v_pk_max_f16 v90, v93, 0
	v_pk_max_f16 v91, v91, 0
	v_pk_max_f16 v76, v84, 0
	v_pk_max_f16 v77, v85, 0
	v_pk_max_f16 v78, v86, 0
	v_pk_max_f16 v79, v79, 0
	ds_write_b128 v175, v[88:91]
	ds_write_b128 v175, v[76:79] offset:64
	ds_read_b128 v[76:79], v176
	ds_read_b128 v[84:87], v176 offset:1152
	v_add_u32_e32 v88, s55, v104
	v_add_u32_e32 v105, v104, v171
	v_add_u32_e32 v89, v88, v170
	buffer_store_dwordx4 v[100:103], v105, s[20:23], 0 offen sc1
	s_waitcnt lgkmcnt(1)
	buffer_store_dwordx4 v[76:79], v89, s[20:23], 0 offen sc1
	v_pk_fma_f32 v[74:75], v[74:75], v[228:229], v[240:241] op_sel:[0,1,0]
	v_pk_fma_f32 v[72:73], v[72:73], v[228:229], v[238:239] op_sel:[0,1,0]
	v_add_u32_e32 v76, v88, v171
	s_waitcnt lgkmcnt(0)
	buffer_store_dwordx4 v[84:87], v76, s[20:23], 0 offen sc1
	v_pk_fma_f32 v[76:77], v[82:83], v[228:229], v[236:237] op_sel:[0,1,0]
	v_pk_fma_f32 v[78:79], v[80:81], v[228:229], v[234:235] op_sel:[0,1,0]
	v_pk_fma_f32 v[70:71], v[70:71], v[228:229], v[244:245] op_sel:[0,1,0]
	v_pk_fma_f32 v[68:69], v[68:69], v[228:229], v[242:243] op_sel:[0,1,0]
	v_pk_fma_f32 v[66:67], v[66:67], v[228:229], v[248:249] op_sel:[0,1,0]
	v_pk_fma_f32 v[64:65], v[64:65], v[228:229], v[246:247] op_sel:[0,1,0]
	v_cvt_pk_f16_f32 v78, v78, v79
	v_cvt_pk_f16_f32 v76, v76, v77
	v_cvt_pk_f16_f32 v77, v72, v73
	v_cvt_pk_f16_f32 v75, v74, v75
	v_cvt_pk_f16_f32 v68, v68, v69
	v_cvt_pk_f16_f32 v69, v70, v71
	v_cvt_pk_f16_f32 v70, v64, v65
	v_cvt_pk_f16_f32 v67, v66, v67
	v_pk_fma_f32 v[62:63], v[62:63], v[230:231], v[236:237] op_sel_hi:[1,0,1]
	v_pk_fma_f32 v[60:61], v[60:61], v[230:231], v[234:235] op_sel_hi:[1,0,1]
	v_pk_fma_f32 v[58:59], v[58:59], v[230:231], v[240:241] op_sel_hi:[1,0,1]
	v_pk_fma_f32 v[56:57], v[56:57], v[230:231], v[238:239] op_sel_hi:[1,0,1]
	v_pk_fma_f32 v[54:55], v[54:55], v[230:231], v[244:245] op_sel_hi:[1,0,1]
	v_pk_fma_f32 v[52:53], v[52:53], v[230:231], v[242:243] op_sel_hi:[1,0,1]
	v_pk_fma_f32 v[46:47], v[46:47], v[230:231], v[248:249] op_sel_hi:[1,0,1]
	v_pk_fma_f32 v[44:45], v[44:45], v[230:231], v[246:247] op_sel_hi:[1,0,1]
	v_pk_max_f16 v72, v78, 0
	v_pk_max_f16 v73, v76, 0
	v_pk_max_f16 v74, v77, 0
	v_pk_max_f16 v75, v75, 0
	v_pk_max_f16 v64, v68, 0
	v_pk_max_f16 v65, v69, 0
	v_pk_max_f16 v66, v70, 0
	v_pk_max_f16 v67, v67, 0
	v_cvt_pk_f16_f32 v60, v60, v61
	v_cvt_pk_f16_f32 v61, v62, v63
	v_cvt_pk_f16_f32 v62, v56, v57
	v_cvt_pk_f16_f32 v59, v58, v59
	v_cvt_pk_f16_f32 v52, v52, v53
	v_cvt_pk_f16_f32 v53, v54, v55
	v_cvt_pk_f16_f32 v54, v44, v45
	v_cvt_pk_f16_f32 v47, v46, v47
	ds_write_b128 v175, v[72:75]
	ds_write_b128 v175, v[64:67] offset:64
	v_pk_max_f16 v56, v60, 0
	v_pk_max_f16 v57, v61, 0
	v_pk_max_f16 v58, v62, 0
	v_pk_max_f16 v59, v59, 0
	v_pk_max_f16 v44, v52, 0
	v_pk_max_f16 v45, v53, 0
	v_pk_max_f16 v46, v54, 0
	v_pk_max_f16 v47, v47, 0
	ds_read_b128 v[64:67], v176
	ds_read_b128 v[68:71], v176 offset:1152
	ds_write_b128 v175, v[56:59]
	ds_write_b128 v175, v[44:47] offset:64
	ds_read_b128 v[44:47], v176
	ds_read_b128 v[52:55], v176 offset:1152
	v_add_u32_e32 v72, s56, v120
	v_lshlrev_b32_e32 v73, 1, v72
	v_add_u32_e32 v74, v73, v170
	v_add_u32_e32 v56, s62, v88
	s_waitcnt lgkmcnt(5)
	buffer_store_dwordx4 v[64:67], v74, s[20:23], 0 offen sc1
	v_add_u32_e32 v57, v56, v170
	v_pk_fma_f32 v[42:43], v[42:43], v[230:231], v[240:241] op_sel:[0,1,0]
	v_add_u32_e32 v64, v73, v171
	s_waitcnt lgkmcnt(4)
	buffer_store_dwordx4 v[68:71], v64, s[20:23], 0 offen sc1
	s_waitcnt lgkmcnt(1)
	buffer_store_dwordx4 v[44:47], v57, s[20:23], 0 offen sc1
	v_pk_fma_f32 v[40:41], v[40:41], v[230:231], v[238:239] op_sel:[0,1,0]
	v_pk_fma_f32 v[38:39], v[38:39], v[230:231], v[244:245] op_sel:[0,1,0]
	v_add_u32_e32 v44, v56, v171
	s_waitcnt lgkmcnt(0)
	buffer_store_dwordx4 v[52:55], v44, s[20:23], 0 offen sc1
	v_pk_fma_f32 v[44:45], v[50:51], v[230:231], v[236:237] op_sel:[0,1,0]
	v_pk_fma_f32 v[46:47], v[48:49], v[230:231], v[234:235] op_sel:[0,1,0]
	v_pk_fma_f32 v[36:37], v[36:37], v[230:231], v[242:243] op_sel:[0,1,0]
	v_pk_fma_f32 v[30:31], v[30:31], v[230:231], v[248:249] op_sel:[0,1,0]
	v_pk_fma_f32 v[28:29], v[28:29], v[230:231], v[246:247] op_sel:[0,1,0]
	v_cvt_pk_f16_f32 v46, v46, v47
	v_cvt_pk_f16_f32 v44, v44, v45
	v_cvt_pk_f16_f32 v45, v40, v41
	v_cvt_pk_f16_f32 v43, v42, v43
	v_cvt_pk_f16_f32 v36, v36, v37
	v_cvt_pk_f16_f32 v37, v38, v39
	v_cvt_pk_f16_f32 v38, v28, v29
	v_cvt_pk_f16_f32 v31, v30, v31
	v_pk_max_f16 v40, v46, 0
	v_pk_max_f16 v41, v44, 0
	v_pk_max_f16 v42, v45, 0
	v_pk_max_f16 v43, v43, 0
	v_pk_max_f16 v28, v36, 0
	v_pk_max_f16 v29, v37, 0
	v_pk_max_f16 v30, v38, 0
	v_pk_max_f16 v31, v31, 0
	ds_write_b128 v175, v[40:43]
	ds_write_b128 v175, v[28:31] offset:64
	ds_read_b128 v[28:31], v176
	ds_read_b128 v[36:39], v176 offset:1152
	v_add_u32_e32 v40, s63, v72
	v_lshlrev_b32_e32 v41, 1, v40
	v_add_u32_e32 v42, v41, v170
	s_waitcnt lgkmcnt(1)
	buffer_store_dwordx4 v[28:31], v42, s[20:23], 0 offen sc1
	v_pk_fma_f32 v[26:27], v[26:27], v[232:233], v[240:241] op_sel_hi:[1,0,1]
	v_pk_fma_f32 v[24:25], v[24:25], v[232:233], v[238:239] op_sel_hi:[1,0,1]
	v_add_u32_e32 v28, v41, v171
	s_waitcnt lgkmcnt(0)
	buffer_store_dwordx4 v[36:39], v28, s[20:23], 0 offen sc1
	v_pk_fma_f32 v[28:29], v[34:35], v[232:233], v[236:237] op_sel_hi:[1,0,1]
	v_pk_fma_f32 v[30:31], v[32:33], v[232:233], v[234:235] op_sel_hi:[1,0,1]
	v_pk_fma_f32 v[22:23], v[22:23], v[232:233], v[244:245] op_sel_hi:[1,0,1]
	v_pk_fma_f32 v[20:21], v[20:21], v[232:233], v[242:243] op_sel_hi:[1,0,1]
	v_pk_fma_f32 v[14:15], v[14:15], v[232:233], v[248:249] op_sel_hi:[1,0,1]
	v_pk_fma_f32 v[12:13], v[12:13], v[232:233], v[246:247] op_sel_hi:[1,0,1]
	v_cvt_pk_f16_f32 v30, v30, v31
	v_cvt_pk_f16_f32 v28, v28, v29
	v_cvt_pk_f16_f32 v29, v24, v25
	v_cvt_pk_f16_f32 v27, v26, v27
	v_cvt_pk_f16_f32 v20, v20, v21
	v_cvt_pk_f16_f32 v21, v22, v23
	v_cvt_pk_f16_f32 v22, v12, v13
	v_cvt_pk_f16_f32 v15, v14, v15
	v_pk_max_f16 v24, v30, 0
	v_pk_max_f16 v25, v28, 0
	v_pk_max_f16 v26, v29, 0
	v_pk_max_f16 v27, v27, 0
	v_pk_max_f16 v12, v20, 0
	v_pk_max_f16 v13, v21, 0
	v_pk_max_f16 v14, v22, 0
	v_pk_max_f16 v15, v15, 0
	ds_write_b128 v175, v[24:27]
	ds_write_b128 v175, v[12:15] offset:64
	ds_read_b128 v[12:15], v176
	ds_read_b128 v[20:23], v176 offset:1152
	v_add_u32_e32 v24, s64, v40
	v_lshlrev_b32_e32 v25, 1, v24
	v_add_u32_e32 v26, v25, v170
	s_waitcnt lgkmcnt(1)
	buffer_store_dwordx4 v[12:15], v26, s[20:23], 0 offen sc1
	v_pk_fma_f32 v[10:11], v[10:11], v[232:233], v[240:241] op_sel:[0,1,0]
	v_pk_fma_f32 v[8:9], v[8:9], v[232:233], v[238:239] op_sel:[0,1,0]
	v_pk_fma_f32 v[12:13], v[18:19], v[232:233], v[236:237] op_sel:[0,1,0]
	v_pk_fma_f32 v[14:15], v[16:17], v[232:233], v[234:235] op_sel:[0,1,0]
	v_pk_fma_f32 v[6:7], v[6:7], v[232:233], v[244:245] op_sel:[0,1,0]
	v_pk_fma_f32 v[4:5], v[4:5], v[232:233], v[242:243] op_sel:[0,1,0]
	v_pk_fma_f32 v[2:3], v[2:3], v[232:233], v[248:249] op_sel:[0,1,0]
	v_pk_fma_f32 v[0:1], v[0:1], v[232:233], v[246:247] op_sel:[0,1,0]
	v_cvt_pk_f16_f32 v14, v14, v15
	v_cvt_pk_f16_f32 v12, v12, v13
	v_cvt_pk_f16_f32 v13, v8, v9
	v_cvt_pk_f16_f32 v11, v10, v11
	v_cvt_pk_f16_f32 v4, v4, v5
	v_cvt_pk_f16_f32 v5, v6, v7
	v_cvt_pk_f16_f32 v6, v0, v1
	v_cvt_pk_f16_f32 v3, v2, v3
	v_pk_max_f16 v8, v14, 0
	v_pk_max_f16 v9, v12, 0
	v_pk_max_f16 v10, v13, 0
	v_pk_max_f16 v11, v11, 0
	v_pk_max_f16 v0, v4, 0
	v_pk_max_f16 v1, v5, 0
	v_pk_max_f16 v2, v6, 0
	v_pk_max_f16 v3, v3, 0
	ds_write_b128 v175, v[8:11]
	ds_write_b128 v175, v[0:3] offset:64
	ds_read_b128 v[0:3], v176
	ds_read_b128 v[4:7], v176 offset:1152
	v_add_lshl_u32 v8, v24, s64, 1
	v_add_u32_e32 v25, v25, v171
	v_add_u32_e32 v9, v8, v170
	s_waitcnt lgkmcnt(4)
	buffer_store_dwordx4 v[20:23], v25, s[20:23], 0 offen sc1
	s_waitcnt lgkmcnt(1)
	buffer_store_dwordx4 v[0:3], v9, s[20:23], 0 offen sc1
	s_mov_b32 s68, s67
	s_mov_b32 s70, s69
	v_add_u32_e32 v0, v8, v171
	s_mov_b64 s[30:31], s[0:1]
	s_mov_b64 s[28:29], s[8:9]
	s_mov_b64 vcc, s[6:7]
	s_waitcnt lgkmcnt(0)
	buffer_store_dwordx4 v[4:7], v0, s[20:23], 0 offen sc1
	s_cbranch_vccz .LBB9_12
	s_waitcnt vmcnt(0)
	s_cmpk_gt_u32 s36, 0xff
	s_cbranch_scc1 .LBB9_31
	s_barrier

.LBB10_27:
	s_add_u32 s40, s38, 0xfff40080
	s_addc_u32 s41, s39, -1
	s_cmp_eq_u32 s87, 44
	s_cselect_b32 s43, s9, s41
	s_cselect_b32 s42, s8, s40
	s_cselect_b32 s41, s1, s86
	s_cselect_b32 s40, s0, s85
	s_add_i32 m0, s51, 0xc000
	ds_read_b128 v[136:139], v232
	ds_read_b128 v[148:151], v232 offset:1024
	ds_read_b128 v[152:155], v232 offset:2048
	ds_read_b128 v[156:159], v232 offset:3072
	ds_read_b128 v[160:163], v232 offset:4096
	ds_read_b128 v[164:167], v232 offset:5120
	ds_read_b128 v[168:171], v232 offset:6144
	ds_read_b128 v[172:175], v232 offset:7168
	global_load_lds_dwordx4 v184, s[38:39]
	s_add_i32 m0, s51, 0xe000
	s_nop 0
	global_load_lds_dwordx4 v186, s[38:39]
	s_waitcnt lgkmcnt(8)
	s_barrier
	s_waitcnt lgkmcnt(0)
	v_mfma_f32_16x16x32_f16 v[144:147], v[72:75], v[136:139], v[144:147]
	v_mfma_f32_16x16x32_f16 v[140:143], v[88:91], v[136:139], v[140:143]
	v_mfma_f32_16x16x32_f16 v[124:127], v[72:75], v[152:155], v[124:127]
	v_mfma_f32_16x16x32_f16 v[120:123], v[88:91], v[152:155], v[120:123]
	v_mfma_f32_16x16x32_f16 v[108:111], v[72:75], v[160:163], v[108:111]
	v_mfma_f32_16x16x32_f16 v[104:107], v[88:91], v[160:163], v[104:107]
	v_mfma_f32_16x16x32_f16 v[84:87], v[72:75], v[168:171], v[84:87]
	v_mfma_f32_16x16x32_f16 v[76:79], v[88:91], v[168:171], v[76:79]
	v_mfma_f32_16x16x32_f16 v[144:147], v[80:83], v[148:151], v[144:147]
	v_mfma_f32_16x16x32_f16 v[140:143], v[92:95], v[148:151], v[140:143]
	v_mfma_f32_16x16x32_f16 v[124:127], v[80:83], v[156:159], v[124:127]
	v_mfma_f32_16x16x32_f16 v[120:123], v[92:95], v[156:159], v[120:123]
	v_mfma_f32_16x16x32_f16 v[108:111], v[80:83], v[164:167], v[108:111]
	v_mfma_f32_16x16x32_f16 v[104:107], v[92:95], v[164:167], v[104:107]
	v_mfma_f32_16x16x32_f16 v[84:87], v[80:83], v[172:175], v[84:87]
	v_mfma_f32_16x16x32_f16 v[76:79], v[92:95], v[172:175], v[76:79]
	s_barrier
	s_add_i32 s88, s69, s50
	s_add_u32 s92, s40, 0x80
	s_addc_u32 s93, s41, 0
	s_mov_b32 m0, s88
	ds_read_b128 v[190:193], v233
	ds_read_b128 v[194:197], v233 offset:1024
	ds_read_b128 v[198:201], v233 offset:2048
	ds_read_b128 v[202:205], v233 offset:3072
	global_load_lds_dwordx4 v178, s[40:41]
	s_add_i32 m0, s88, 0x2000
	s_nop 0
	global_load_lds_dwordx4 v182, s[40:41]
	s_barrier
	s_waitcnt lgkmcnt(0)
	v_mfma_f32_16x16x32_f16 v[132:135], v[190:193], v[136:139], v[132:135]
	v_mfma_f32_16x16x32_f16 v[128:131], v[198:201], v[136:139], v[128:131]
	v_mfma_f32_16x16x32_f16 v[116:119], v[190:193], v[152:155], v[116:119]
	v_mfma_f32_16x16x32_f16 v[112:115], v[198:201], v[152:155], v[112:115]
	v_mfma_f32_16x16x32_f16 v[100:103], v[190:193], v[160:163], v[100:103]
	v_mfma_f32_16x16x32_f16 v[96:99], v[198:201], v[160:163], v[96:99]
	v_mfma_f32_16x16x32_f16 v[68:71], v[190:193], v[168:171], v[68:71]
	v_mfma_f32_16x16x32_f16 v[64:67], v[198:201], v[168:171], v[64:67]
	v_mfma_f32_16x16x32_f16 v[132:135], v[194:197], v[148:151], v[132:135]
	v_mfma_f32_16x16x32_f16 v[128:131], v[202:205], v[148:151], v[128:131]
	v_mfma_f32_16x16x32_f16 v[116:119], v[194:197], v[156:159], v[116:119]
	v_mfma_f32_16x16x32_f16 v[112:115], v[202:205], v[156:159], v[112:115]
	v_mfma_f32_16x16x32_f16 v[100:103], v[194:197], v[164:167], v[100:103]
	v_mfma_f32_16x16x32_f16 v[96:99], v[202:205], v[164:167], v[96:99]
	v_mfma_f32_16x16x32_f16 v[68:71], v[194:197], v[172:175], v[68:71]
	v_mfma_f32_16x16x32_f16 v[64:67], v[202:205], v[172:175], v[64:67]
	s_barrier
	s_mov_b32 m0, s51
	s_add_u32 s94, s42, 0x80
	s_addc_u32 s95, s43, 0
	ds_read_b128 v[136:139], v232 offset:16384
	ds_read_b128 v[148:151], v232 offset:17408
	ds_read_b128 v[152:155], v232 offset:18432
	ds_read_b128 v[156:159], v232 offset:19456
	ds_read_b128 v[160:163], v232 offset:20480
	ds_read_b128 v[164:167], v232 offset:21504
	ds_read_b128 v[168:171], v232 offset:22528
	ds_read_b128 v[172:175], v232 offset:23552
	global_load_lds_dwordx4 v176, s[42:43]
	s_mov_b32 m0, s52
	s_nop 0
	global_load_lds_dwordx4 v180, s[42:43]
	s_waitcnt vmcnt(10)
	s_barrier
	s_waitcnt lgkmcnt(0)
	v_mfma_f32_16x16x32_f16 v[60:63], v[72:75], v[136:139], v[60:63]
	v_mfma_f32_16x16x32_f16 v[56:59], v[88:91], v[136:139], v[56:59]
	v_mfma_f32_16x16x32_f16 v[44:47], v[72:75], v[152:155], v[44:47]
	v_mfma_f32_16x16x32_f16 v[40:43], v[88:91], v[152:155], v[40:43]
	v_mfma_f32_16x16x32_f16 v[28:31], v[72:75], v[160:163], v[28:31]
	v_mfma_f32_16x16x32_f16 v[24:27], v[88:91], v[160:163], v[24:27]
	v_mfma_f32_16x16x32_f16 v[12:15], v[72:75], v[168:171], v[12:15]
	v_mfma_f32_16x16x32_f16 v[8:11], v[88:91], v[168:171], v[8:11]
	v_mfma_f32_16x16x32_f16 v[60:63], v[80:83], v[148:151], v[60:63]
	v_mfma_f32_16x16x32_f16 v[56:59], v[92:95], v[148:151], v[56:59]
	v_mfma_f32_16x16x32_f16 v[44:47], v[80:83], v[156:159], v[44:47]
	v_mfma_f32_16x16x32_f16 v[40:43], v[92:95], v[156:159], v[40:43]
	v_mfma_f32_16x16x32_f16 v[28:31], v[80:83], v[164:167], v[28:31]
	v_mfma_f32_16x16x32_f16 v[24:27], v[92:95], v[164:167], v[24:27]
	v_mfma_f32_16x16x32_f16 v[12:15], v[80:83], v[172:175], v[12:15]
	v_mfma_f32_16x16x32_f16 v[8:11], v[92:95], v[172:175], v[8:11]
	s_barrier
	s_add_u32 s88, s40, 0x30000
	s_addc_u32 s89, s41, 0
	s_add_i32 s90, s70, s50
	s_mov_b32 m0, s90
	s_nop 0
	global_load_lds_dwordx4 v178, s[88:89]
	s_add_i32 m0, s90, 0x2000
	s_nop 0
	global_load_lds_dwordx4 v182, s[88:89]
	s_add_i32 s88, 0, 0x18000
	v_add_u32_e32 v92, s88, v228
	ds_read_b128 v[72:75], v92
	ds_read_b128 v[80:83], v92 offset:1024
	ds_read_b128 v[88:91], v92 offset:2048
	ds_read_b128 v[92:95], v92 offset:3072
	s_waitcnt vmcnt(6)
	s_barrier
	v_mfma_f32_16x16x32_f16 v[52:55], v[190:193], v[136:139], v[52:55]
	v_mfma_f32_16x16x32_f16 v[48:51], v[198:201], v[136:139], v[48:51]
	v_mfma_f32_16x16x32_f16 v[36:39], v[190:193], v[152:155], v[36:39]
	v_mfma_f32_16x16x32_f16 v[32:35], v[198:201], v[152:155], v[32:35]
	v_mfma_f32_16x16x32_f16 v[20:23], v[190:193], v[160:163], v[20:23]
	v_mfma_f32_16x16x32_f16 v[16:19], v[198:201], v[160:163], v[16:19]
	v_mfma_f32_16x16x32_f16 v[4:7], v[190:193], v[168:171], v[4:7]
	v_mfma_f32_16x16x32_f16 v[0:3], v[198:201], v[168:171], v[0:3]
	v_mfma_f32_16x16x32_f16 v[52:55], v[194:197], v[148:151], v[52:55]
	v_mfma_f32_16x16x32_f16 v[48:51], v[202:205], v[148:151], v[48:51]
	v_mfma_f32_16x16x32_f16 v[36:39], v[194:197], v[156:159], v[36:39]
	v_mfma_f32_16x16x32_f16 v[32:35], v[202:205], v[156:159], v[32:35]
	v_mfma_f32_16x16x32_f16 v[20:23], v[194:197], v[164:167], v[20:23]
	v_mfma_f32_16x16x32_f16 v[16:19], v[202:205], v[164:167], v[16:19]
	v_mfma_f32_16x16x32_f16 v[4:7], v[194:197], v[172:175], v[4:7]
	v_mfma_f32_16x16x32_f16 v[0:3], v[202:205], v[172:175], v[0:3]
	s_barrier
	s_add_u32 s42, s42, 0xc0000
	s_addc_u32 s43, s43, 0
	s_mov_b32 m0, s53
	ds_read_b128 v[136:139], v232 offset:32768
	ds_read_b128 v[148:151], v232 offset:33792
	ds_read_b128 v[152:155], v232 offset:34816
	ds_read_b128 v[156:159], v232 offset:35840
	ds_read_b128 v[160:163], v232 offset:36864
	ds_read_b128 v[164:167], v232 offset:37888
	ds_read_b128 v[168:171], v232 offset:38912
	ds_read_b128 v[172:175], v232 offset:39936
	global_load_lds_dwordx4 v176, s[42:43]
	s_mov_b32 m0, s54
	s_nop 0
	global_load_lds_dwordx4 v180, s[42:43]
	s_waitcnt lgkmcnt(8)
	s_barrier
	s_waitcnt lgkmcnt(0)
	v_mfma_f32_16x16x32_f16 v[144:147], v[72:75], v[136:139], v[144:147]
	v_mfma_f32_16x16x32_f16 v[140:143], v[88:91], v[136:139], v[140:143]
	v_mfma_f32_16x16x32_f16 v[124:127], v[72:75], v[152:155], v[124:127]
	v_mfma_f32_16x16x32_f16 v[120:123], v[88:91], v[152:155], v[120:123]
	v_mfma_f32_16x16x32_f16 v[108:111], v[72:75], v[160:163], v[108:111]
	v_mfma_f32_16x16x32_f16 v[104:107], v[88:91], v[160:163], v[104:107]
	v_mfma_f32_16x16x32_f16 v[84:87], v[72:75], v[168:171], v[84:87]
	v_mfma_f32_16x16x32_f16 v[76:79], v[88:91], v[168:171], v[76:79]
	v_mfma_f32_16x16x32_f16 v[144:147], v[80:83], v[148:151], v[144:147]
	v_mfma_f32_16x16x32_f16 v[140:143], v[92:95], v[148:151], v[140:143]
	v_mfma_f32_16x16x32_f16 v[124:127], v[80:83], v[156:159], v[124:127]
	v_mfma_f32_16x16x32_f16 v[120:123], v[92:95], v[156:159], v[120:123]
	v_mfma_f32_16x16x32_f16 v[108:111], v[80:83], v[164:167], v[108:111]
	v_mfma_f32_16x16x32_f16 v[104:107], v[92:95], v[164:167], v[104:107]
	v_mfma_f32_16x16x32_f16 v[84:87], v[80:83], v[172:175], v[84:87]
	v_mfma_f32_16x16x32_f16 v[76:79], v[92:95], v[172:175], v[76:79]
	s_barrier
	s_add_i32 s42, 0, 0x1c000
	s_add_i32 s43, s88, s50
	v_add_u32_e32 v202, s42, v228
	s_mov_b32 m0, s43
	ds_read_b128 v[190:193], v202
	ds_read_b128 v[194:197], v202 offset:1024
	ds_read_b128 v[198:201], v202 offset:2048
	ds_read_b128 v[202:205], v202 offset:3072
	global_load_lds_dwordx4 v178, s[92:93]
	s_add_i32 m0, s43, 0x2000
	s_nop 0
	global_load_lds_dwordx4 v182, s[92:93]
	s_barrier
	s_waitcnt lgkmcnt(0)
	v_mfma_f32_16x16x32_f16 v[132:135], v[190:193], v[136:139], v[132:135]
	v_mfma_f32_16x16x32_f16 v[128:131], v[198:201], v[136:139], v[128:131]
	v_mfma_f32_16x16x32_f16 v[116:119], v[190:193], v[152:155], v[116:119]
	v_mfma_f32_16x16x32_f16 v[112:115], v[198:201], v[152:155], v[112:115]
	v_mfma_f32_16x16x32_f16 v[100:103], v[190:193], v[160:163], v[100:103]
	v_mfma_f32_16x16x32_f16 v[96:99], v[198:201], v[160:163], v[96:99]
	v_mfma_f32_16x16x32_f16 v[68:71], v[190:193], v[168:171], v[68:71]
	v_mfma_f32_16x16x32_f16 v[64:67], v[198:201], v[168:171], v[64:67]
	v_mfma_f32_16x16x32_f16 v[132:135], v[194:197], v[148:151], v[132:135]
	v_mfma_f32_16x16x32_f16 v[128:131], v[202:205], v[148:151], v[128:131]
	v_mfma_f32_16x16x32_f16 v[116:119], v[194:197], v[156:159], v[116:119]
	v_mfma_f32_16x16x32_f16 v[112:115], v[202:205], v[156:159], v[112:115]
	v_mfma_f32_16x16x32_f16 v[100:103], v[194:197], v[164:167], v[100:103]
	v_mfma_f32_16x16x32_f16 v[96:99], v[202:205], v[164:167], v[96:99]
	v_mfma_f32_16x16x32_f16 v[68:71], v[194:197], v[172:175], v[68:71]
	v_mfma_f32_16x16x32_f16 v[64:67], v[202:205], v[172:175], v[64:67]
	s_barrier
	s_mov_b32 m0, s58
	ds_read_b128 v[136:139], v232 offset:49152
	ds_read_b128 v[148:151], v232 offset:50176
	ds_read_b128 v[152:155], v232 offset:51200
	ds_read_b128 v[156:159], v232 offset:52224
	ds_read_b128 v[160:163], v232 offset:53248
	ds_read_b128 v[164:167], v232 offset:54272
	ds_read_b128 v[168:171], v232 offset:55296
	ds_read_b128 v[172:175], v232 offset:56320
	global_load_lds_dwordx4 v176, s[94:95]
	s_mov_b32 m0, s59
	s_nop 0
	global_load_lds_dwordx4 v180, s[94:95]
	s_waitcnt vmcnt(10)
	s_barrier
	s_waitcnt lgkmcnt(0)
	v_mfma_f32_16x16x32_f16 v[60:63], v[72:75], v[136:139], v[60:63]
	v_mfma_f32_16x16x32_f16 v[56:59], v[88:91], v[136:139], v[56:59]
	v_mfma_f32_16x16x32_f16 v[44:47], v[72:75], v[152:155], v[44:47]
	v_mfma_f32_16x16x32_f16 v[40:43], v[88:91], v[152:155], v[40:43]
	v_mfma_f32_16x16x32_f16 v[28:31], v[72:75], v[160:163], v[28:31]
	v_mfma_f32_16x16x32_f16 v[24:27], v[88:91], v[160:163], v[24:27]
	v_mfma_f32_16x16x32_f16 v[12:15], v[72:75], v[168:171], v[12:15]
	v_mfma_f32_16x16x32_f16 v[8:11], v[88:91], v[168:171], v[8:11]
	v_mfma_f32_16x16x32_f16 v[60:63], v[80:83], v[148:151], v[60:63]
	v_mfma_f32_16x16x32_f16 v[56:59], v[92:95], v[148:151], v[56:59]
	v_mfma_f32_16x16x32_f16 v[44:47], v[80:83], v[156:159], v[44:47]
	v_mfma_f32_16x16x32_f16 v[40:43], v[92:95], v[156:159], v[40:43]
	v_mfma_f32_16x16x32_f16 v[28:31], v[80:83], v[164:167], v[28:31]
	v_mfma_f32_16x16x32_f16 v[24:27], v[92:95], v[164:167], v[24:27]
	v_mfma_f32_16x16x32_f16 v[12:15], v[80:83], v[172:175], v[12:15]
	v_mfma_f32_16x16x32_f16 v[8:11], v[92:95], v[172:175], v[8:11]
	s_barrier
	s_add_u32 s40, s40, 0x30080
	s_addc_u32 s41, s41, 0
	s_add_i32 s42, s42, s50
	s_mov_b32 m0, s42
	s_nop 0
	global_load_lds_dwordx4 v178, s[40:41]
	s_add_i32 m0, s42, 0x2000
	s_nop 0
	global_load_lds_dwordx4 v182, s[40:41]
	ds_read_b128 v[72:75], v231
	ds_read_b128 v[80:83], v231 offset:1024
	ds_read_b128 v[88:91], v231 offset:2048
	ds_read_b128 v[92:95], v231 offset:3072
	s_waitcnt vmcnt(6)
	s_barrier
	v_mfma_f32_16x16x32_f16 v[52:55], v[190:193], v[136:139], v[52:55]
	v_mfma_f32_16x16x32_f16 v[48:51], v[198:201], v[136:139], v[48:51]
	v_mfma_f32_16x16x32_f16 v[36:39], v[190:193], v[152:155], v[36:39]
	v_mfma_f32_16x16x32_f16 v[32:35], v[198:201], v[152:155], v[32:35]
	v_mfma_f32_16x16x32_f16 v[20:23], v[190:193], v[160:163], v[20:23]
	v_mfma_f32_16x16x32_f16 v[16:19], v[198:201], v[160:163], v[16:19]
	v_mfma_f32_16x16x32_f16 v[4:7], v[190:193], v[168:171], v[4:7]
	v_mfma_f32_16x16x32_f16 v[0:3], v[198:201], v[168:171], v[0:3]
	v_mfma_f32_16x16x32_f16 v[52:55], v[194:197], v[148:151], v[52:55]
	v_mfma_f32_16x16x32_f16 v[48:51], v[202:205], v[148:151], v[48:51]
	v_mfma_f32_16x16x32_f16 v[36:39], v[194:197], v[156:159], v[36:39]
	v_mfma_f32_16x16x32_f16 v[32:35], v[202:205], v[156:159], v[32:35]
	v_mfma_f32_16x16x32_f16 v[20:23], v[194:197], v[164:167], v[20:23]
	v_mfma_f32_16x16x32_f16 v[16:19], v[202:205], v[164:167], v[16:19]
	v_mfma_f32_16x16x32_f16 v[4:7], v[194:197], v[172:175], v[4:7]
	v_mfma_f32_16x16x32_f16 v[0:3], v[202:205], v[172:175], v[0:3]
	s_barrier
	s_add_i32 s87, s87, 2
	s_add_u32 s38, s38, 0x100
	s_addc_u32 s39, s39, 0
	s_add_u32 s85, s85, 0x100
	s_addc_u32 s86, s86, 0
	s_cmp_gt_u32 s87, 45
	s_cbranch_scc0 .LBB10_27
	s_lshl_b32 s92, s84, 8
	s_add_i32 s92, s92, s57
	s_lshl_b32 s93, s83, 8
	s_or_b32 s93, s93, s60
	v_lshlrev_b32_e32 v237, 2, v226
	s_lshl_b32 s96, s93, 2
	s_add_u32 s94, s16, s96
	s_addc_u32 s95, s17, 0
	global_load_dwordx4 v[72:75], v237, s[94:95] offset:0
	global_load_dwordx4 v[80:83], v237, s[94:95] offset:16
	global_load_dwordx4 v[88:91], v237, s[94:95] offset:128
	global_load_dwordx4 v[92:95], v237, s[94:95] offset:144
	s_add_u32 s94, s18, s96
	s_addc_u32 s95, s19, 0
	global_load_dwordx4 v[136:139], v237, s[94:95] offset:0
	global_load_dwordx4 v[148:151], v237, s[94:95] offset:16
	global_load_dwordx4 v[152:155], v237, s[94:95] offset:128
	global_load_dwordx4 v[156:159], v237, s[94:95] offset:144
	s_add_u32 s94, s14, s96
	s_addc_u32 s95, s15, 0
	global_load_dwordx4 v[160:163], v237, s[94:95] offset:0
	global_load_dwordx4 v[164:167], v237, s[94:95] offset:16
	global_load_dwordx4 v[168:171], v237, s[94:95] offset:128
	global_load_dwordx4 v[172:175], v237, s[94:95] offset:144
	v_lshlrev_b32_e32 v190, 3, v227
	s_lshl_b32 s96, s92, 3
	s_add_u32 s94, s12, s96
	s_addc_u32 s95, s13, 0
	global_load_dwordx2 v[238:239], v190, s[94:95] offset:0
	global_load_dwordx2 v[192:193], v190, s[94:95] offset:128
	global_load_dwordx2 v[194:195], v190, s[94:95] offset:256
	global_load_dwordx2 v[196:197], v190, s[94:95] offset:384
	global_load_dwordx2 v[198:199], v190, s[94:95] offset:1024
	global_load_dwordx2 v[200:201], v190, s[94:95] offset:1152
	global_load_dwordx2 v[202:203], v190, s[94:95] offset:1280
	global_load_dwordx2 v[204:205], v190, s[94:95] offset:1408
	v_mul_u32_u24_e32 v191, 0x600, v227
	v_lshl_add_u32 v191, v226, 1, v191
	s_mul_i32 s96, s92, 0x600
	s_lshl_b32 s97, s93, 1
	s_add_u32 s96, s96, s97
	s_add_u32 s98, s10, s96
	s_addc_u32 s99, s11, 0
	s_add_u32 s94, s98, 0x0
	s_addc_u32 s95, s99, 0
	global_load_dwordx4 v[208:211], v191, s[94:95] offset:0 nt
	global_load_dwordx4 v[212:215], v191, s[94:95] offset:64 nt
	s_add_u32 s94, s98, 0x6000
	s_addc_u32 s95, s99, 0
	global_load_dwordx4 v[216:219], v191, s[94:95] offset:0 nt
	global_load_dwordx4 v[220:223], v191, s[94:95] offset:64 nt
	v_add_u32_e32 v224, s92, v229
	v_mul_u32_u24_e32 v224, 0x600, v224
	s_lshl_b32 s97, s93, 1
	v_add3_u32 v224, v224, v230, s97
	s_lshl_b32 s96, s83, 2
	s_lshr_b32 s97, s60, 6
	s_add_u32 s96, s96, s97
	s_lshl_b32 s96, s96, 19
	s_lshl_b32 s97, s92, 3
	s_add_u32 s96, s96, s97
	s_add_u32 s100, s28, s96
	s_addc_u32 s101, s29, 0
	s_waitcnt vmcnt(19)
	v_pk_add_f32 v[72:73], v[72:73], v[136:137]
	v_pk_add_f32 v[74:75], v[74:75], v[138:139]
	s_waitcnt vmcnt(18)
	v_pk_add_f32 v[80:81], v[80:81], v[148:149]
	v_pk_add_f32 v[82:83], v[82:83], v[150:151]
	s_waitcnt vmcnt(17)
	v_pk_add_f32 v[88:89], v[88:89], v[152:153]
	v_pk_add_f32 v[90:91], v[90:91], v[154:155]
	s_waitcnt vmcnt(16)
	v_pk_add_f32 v[92:93], v[92:93], v[156:157]
	v_pk_add_f32 v[94:95], v[94:95], v[158:159]
	v_pk_add_f32 v[144:145], v[144:145], v[72:73]
	v_pk_add_f32 v[146:147], v[146:147], v[74:75]
	v_pk_add_f32 v[124:125], v[124:125], v[72:73]
	v_pk_add_f32 v[126:127], v[126:127], v[74:75]
	v_pk_add_f32 v[108:109], v[108:109], v[72:73]
	v_pk_add_f32 v[110:111], v[110:111], v[74:75]
	v_pk_add_f32 v[84:85], v[84:85], v[72:73]
	v_pk_add_f32 v[86:87], v[86:87], v[74:75]
	v_pk_add_f32 v[60:61], v[60:61], v[72:73]
	v_pk_add_f32 v[62:63], v[62:63], v[74:75]
	v_pk_add_f32 v[44:45], v[44:45], v[72:73]
	v_pk_add_f32 v[46:47], v[46:47], v[74:75]
	v_pk_add_f32 v[28:29], v[28:29], v[72:73]
	v_pk_add_f32 v[30:31], v[30:31], v[74:75]
	v_pk_add_f32 v[12:13], v[12:13], v[72:73]
	v_pk_add_f32 v[14:15], v[14:15], v[74:75]
	v_pk_add_f32 v[140:141], v[140:141], v[80:81]
	v_pk_add_f32 v[142:143], v[142:143], v[82:83]
	v_pk_add_f32 v[120:121], v[120:121], v[80:81]
	v_pk_add_f32 v[122:123], v[122:123], v[82:83]
	v_pk_add_f32 v[104:105], v[104:105], v[80:81]
	v_pk_add_f32 v[106:107], v[106:107], v[82:83]
	v_pk_add_f32 v[76:77], v[76:77], v[80:81]
	v_pk_add_f32 v[78:79], v[78:79], v[82:83]
	v_pk_add_f32 v[56:57], v[56:57], v[80:81]
	v_pk_add_f32 v[58:59], v[58:59], v[82:83]
	v_pk_add_f32 v[40:41], v[40:41], v[80:81]
	v_pk_add_f32 v[42:43], v[42:43], v[82:83]
	v_pk_add_f32 v[24:25], v[24:25], v[80:81]
	v_pk_add_f32 v[26:27], v[26:27], v[82:83]
	v_pk_add_f32 v[8:9], v[8:9], v[80:81]
	v_pk_add_f32 v[10:11], v[10:11], v[82:83]
	v_pk_add_f32 v[132:133], v[132:133], v[88:89]
	v_pk_add_f32 v[134:135], v[134:135], v[90:91]
	v_pk_add_f32 v[116:117], v[116:117], v[88:89]
	v_pk_add_f32 v[118:119], v[118:119], v[90:91]
	v_pk_add_f32 v[100:101], v[100:101], v[88:89]
	v_pk_add_f32 v[102:103], v[102:103], v[90:91]
	v_pk_add_f32 v[68:69], v[68:69], v[88:89]
	v_pk_add_f32 v[70:71], v[70:71], v[90:91]
	v_pk_add_f32 v[52:53], v[52:53], v[88:89]
	v_pk_add_f32 v[54:55], v[54:55], v[90:91]
	v_pk_add_f32 v[36:37], v[36:37], v[88:89]
	v_pk_add_f32 v[38:39], v[38:39], v[90:91]
	v_pk_add_f32 v[20:21], v[20:21], v[88:89]
	v_pk_add_f32 v[22:23], v[22:23], v[90:91]
	v_pk_add_f32 v[4:5], v[4:5], v[88:89]
	v_pk_add_f32 v[6:7], v[6:7], v[90:91]
	v_pk_add_f32 v[128:129], v[128:129], v[92:93]
	v_pk_add_f32 v[130:131], v[130:131], v[94:95]
	v_pk_add_f32 v[112:113], v[112:113], v[92:93]
	v_pk_add_f32 v[114:115], v[114:115], v[94:95]
	v_pk_add_f32 v[96:97], v[96:97], v[92:93]
	v_pk_add_f32 v[98:99], v[98:99], v[94:95]
	v_pk_add_f32 v[64:65], v[64:65], v[92:93]
	v_pk_add_f32 v[66:67], v[66:67], v[94:95]
	v_pk_add_f32 v[48:49], v[48:49], v[92:93]
	v_pk_add_f32 v[50:51], v[50:51], v[94:95]
	v_pk_add_f32 v[32:33], v[32:33], v[92:93]
	v_pk_add_f32 v[34:35], v[34:35], v[94:95]
	v_pk_add_f32 v[16:17], v[16:17], v[92:93]
	v_pk_add_f32 v[18:19], v[18:19], v[94:95]
	v_pk_add_f32 v[0:1], v[0:1], v[92:93]
	v_pk_add_f32 v[2:3], v[2:3], v[94:95]
	s_add_u32 s94, s98, 0xc000
	s_addc_u32 s95, s99, 0
	global_load_dwordx4 v[240:243], v191, s[94:95] offset:0 nt
	global_load_dwordx4 v[244:247], v191, s[94:95] offset:64 nt
	s_add_u32 s94, s98, 0x12000
	s_addc_u32 s95, s99, 0
	global_load_dwordx4 v[248:251], v191, s[94:95] offset:0 nt
	global_load_dwordx4 v[252:255], v191, s[94:95] offset:64 nt
	s_add_u32 s94, s98, 0x30000
	s_addc_u32 s95, s99, 0
	global_load_dwordx4 v[136:139], v191, s[94:95] offset:0 nt
	global_load_dwordx4 v[148:151], v191, s[94:95] offset:64 nt
	s_add_u32 s94, s98, 0x36000
	s_addc_u32 s95, s99, 0
	global_load_dwordx4 v[152:155], v191, s[94:95] offset:0 nt
	global_load_dwordx4 v[156:159], v191, s[94:95] offset:64 nt
	s_waitcnt vmcnt(19)
	s_waitcnt vmcnt(11)
	v_cvt_f32_f16_e32 v72, v208
	v_cvt_f32_f16_sdwa v73, v208 dst_sel:DWORD dst_unused:UNUSED_PAD src0_sel:WORD_1
	v_cvt_f32_f16_e32 v74, v209
	v_cvt_f32_f16_sdwa v75, v209 dst_sel:DWORD dst_unused:UNUSED_PAD src0_sel:WORD_1
	v_cvt_f32_f16_e32 v80, v210
	v_cvt_f32_f16_sdwa v81, v210 dst_sel:DWORD dst_unused:UNUSED_PAD src0_sel:WORD_1
	v_cvt_f32_f16_e32 v82, v211
	v_cvt_f32_f16_sdwa v83, v211 dst_sel:DWORD dst_unused:UNUSED_PAD src0_sel:WORD_1
	v_sub_f32_e32 v72, v72, v238
	v_sub_f32_e32 v73, v73, v238
	v_sub_f32_e32 v74, v74, v238
	v_sub_f32_e32 v75, v75, v238
	v_sub_f32_e32 v80, v80, v238
	v_sub_f32_e32 v81, v81, v238
	v_sub_f32_e32 v82, v82, v238
	v_sub_f32_e32 v83, v83, v238
	v_pk_mul_f32 v[72:73], v[238:239], v[72:73] op_sel:[1,0]
	v_pk_mul_f32 v[74:75], v[238:239], v[74:75] op_sel:[1,0]
	v_pk_mul_f32 v[80:81], v[238:239], v[80:81] op_sel:[1,0]
	v_pk_mul_f32 v[82:83], v[238:239], v[82:83] op_sel:[1,0]
	v_pk_fma_f32 v[144:145], v[72:73], v[160:161], v[144:145]
	v_pk_fma_f32 v[146:147], v[74:75], v[162:163], v[146:147]
	v_pk_fma_f32 v[140:141], v[80:81], v[164:165], v[140:141]
	v_pk_fma_f32 v[142:143], v[82:83], v[166:167], v[142:143]
	v_cvt_pk_f16_f32 v144, v144, v145
	v_cvt_pk_f16_f32 v145, v146, v147
	v_cvt_pk_f16_f32 v146, v140, v141
	v_cvt_pk_f16_f32 v147, v142, v143
	ds_write_b128 v235, v[144:147]
	v_fma_mix_f32 v206, v144, 1.0, 0 op_sel_hi:[1,0,0]
	v_fma_mix_f32 v207, v144, v144, 0 op_sel_hi:[1,1,0]
	v_fma_mix_f32 v206, v144, 1.0, v206 op_sel:[1,0,0] op_sel_hi:[1,0,0]
	v_fma_mix_f32 v207, v144, v144, v207 op_sel:[1,1,0] op_sel_hi:[1,1,0]
	v_fma_mix_f32 v206, v145, 1.0, v206 op_sel_hi:[1,0,0]
	v_fma_mix_f32 v207, v145, v145, v207 op_sel_hi:[1,1,0]
	v_fma_mix_f32 v206, v145, 1.0, v206 op_sel:[1,0,0] op_sel_hi:[1,0,0]
	v_fma_mix_f32 v207, v145, v145, v207 op_sel:[1,1,0] op_sel_hi:[1,1,0]
	v_fma_mix_f32 v206, v146, 1.0, v206 op_sel_hi:[1,0,0]
	v_fma_mix_f32 v207, v146, v146, v207 op_sel_hi:[1,1,0]
	v_fma_mix_f32 v206, v146, 1.0, v206 op_sel:[1,0,0] op_sel_hi:[1,0,0]
	v_fma_mix_f32 v207, v146, v146, v207 op_sel:[1,1,0] op_sel_hi:[1,1,0]
	v_fma_mix_f32 v206, v147, 1.0, v206 op_sel_hi:[1,0,0]
	v_fma_mix_f32 v207, v147, v147, v207 op_sel_hi:[1,1,0]
	v_fma_mix_f32 v206, v147, 1.0, v206 op_sel:[1,0,0] op_sel_hi:[1,0,0]
	v_fma_mix_f32 v207, v147, v147, v207 op_sel:[1,1,0] op_sel_hi:[1,1,0]
	s_waitcnt vmcnt(10)
	v_cvt_f32_f16_e32 v72, v212
	v_cvt_f32_f16_sdwa v73, v212 dst_sel:DWORD dst_unused:UNUSED_PAD src0_sel:WORD_1
	v_cvt_f32_f16_e32 v74, v213
	v_cvt_f32_f16_sdwa v75, v213 dst_sel:DWORD dst_unused:UNUSED_PAD src0_sel:WORD_1
	v_cvt_f32_f16_e32 v80, v214
	v_cvt_f32_f16_sdwa v81, v214 dst_sel:DWORD dst_unused:UNUSED_PAD src0_sel:WORD_1
	v_cvt_f32_f16_e32 v82, v215
	v_cvt_f32_f16_sdwa v83, v215 dst_sel:DWORD dst_unused:UNUSED_PAD src0_sel:WORD_1
	v_sub_f32_e32 v72, v72, v238
	v_sub_f32_e32 v73, v73, v238
	v_sub_f32_e32 v74, v74, v238
	v_sub_f32_e32 v75, v75, v238
	v_sub_f32_e32 v80, v80, v238
	v_sub_f32_e32 v81, v81, v238
	v_sub_f32_e32 v82, v82, v238
	v_sub_f32_e32 v83, v83, v238
	v_pk_mul_f32 v[72:73], v[238:239], v[72:73] op_sel:[1,0]
	v_pk_mul_f32 v[74:75], v[238:239], v[74:75] op_sel:[1,0]
	v_pk_mul_f32 v[80:81], v[238:239], v[80:81] op_sel:[1,0]
	v_pk_mul_f32 v[82:83], v[238:239], v[82:83] op_sel:[1,0]
	v_pk_fma_f32 v[132:133], v[72:73], v[168:169], v[132:133]
	v_pk_fma_f32 v[134:135], v[74:75], v[170:171], v[134:135]
	v_pk_fma_f32 v[128:129], v[80:81], v[172:173], v[128:129]
	v_pk_fma_f32 v[130:131], v[82:83], v[174:175], v[130:131]
	v_cvt_pk_f16_f32 v132, v132, v133
	v_cvt_pk_f16_f32 v133, v134, v135
	v_cvt_pk_f16_f32 v134, v128, v129
	v_cvt_pk_f16_f32 v135, v130, v131
	ds_write_b128 v235, v[132:135] offset:64
	v_fma_mix_f32 v206, v132, 1.0, v206 op_sel_hi:[1,0,0]
	v_fma_mix_f32 v207, v132, v132, v207 op_sel_hi:[1,1,0]
	v_fma_mix_f32 v206, v132, 1.0, v206 op_sel:[1,0,0] op_sel_hi:[1,0,0]
	v_fma_mix_f32 v207, v132, v132, v207 op_sel:[1,1,0] op_sel_hi:[1,1,0]
	v_fma_mix_f32 v206, v133, 1.0, v206 op_sel_hi:[1,0,0]
	v_fma_mix_f32 v207, v133, v133, v207 op_sel_hi:[1,1,0]
	v_fma_mix_f32 v206, v133, 1.0, v206 op_sel:[1,0,0] op_sel_hi:[1,0,0]
	v_fma_mix_f32 v207, v133, v133, v207 op_sel:[1,1,0] op_sel_hi:[1,1,0]
	v_fma_mix_f32 v206, v134, 1.0, v206 op_sel_hi:[1,0,0]
	v_fma_mix_f32 v207, v134, v134, v207 op_sel_hi:[1,1,0]
	v_fma_mix_f32 v206, v134, 1.0, v206 op_sel:[1,0,0] op_sel_hi:[1,0,0]
	v_fma_mix_f32 v207, v134, v134, v207 op_sel:[1,1,0] op_sel_hi:[1,1,0]
	v_fma_mix_f32 v206, v135, 1.0, v206 op_sel_hi:[1,0,0]
	v_fma_mix_f32 v207, v135, v135, v207 op_sel_hi:[1,1,0]
	v_fma_mix_f32 v206, v135, 1.0, v206 op_sel:[1,0,0] op_sel_hi:[1,0,0]
	v_fma_mix_f32 v207, v135, v135, v207 op_sel:[1,1,0] op_sel_hi:[1,1,0]
	ds_read_b128 v[88:91], v236
	ds_read_b128 v[92:95], v236 offset:1152
	s_waitcnt vmcnt(9)
	v_cvt_f32_f16_e32 v72, v216
	v_cvt_f32_f16_sdwa v73, v216 dst_sel:DWORD dst_unused:UNUSED_PAD src0_sel:WORD_1
	v_cvt_f32_f16_e32 v74, v217
	v_cvt_f32_f16_sdwa v75, v217 dst_sel:DWORD dst_unused:UNUSED_PAD src0_sel:WORD_1
	v_cvt_f32_f16_e32 v80, v218
	v_cvt_f32_f16_sdwa v81, v218 dst_sel:DWORD dst_unused:UNUSED_PAD src0_sel:WORD_1
	v_cvt_f32_f16_e32 v82, v219
	v_cvt_f32_f16_sdwa v83, v219 dst_sel:DWORD dst_unused:UNUSED_PAD src0_sel:WORD_1
	v_sub_f32_e32 v72, v72, v192
	v_sub_f32_e32 v73, v73, v192
	v_sub_f32_e32 v74, v74, v192
	v_sub_f32_e32 v75, v75, v192
	v_sub_f32_e32 v80, v80, v192
	v_sub_f32_e32 v81, v81, v192
	v_sub_f32_e32 v82, v82, v192
	v_sub_f32_e32 v83, v83, v192
	v_pk_mul_f32 v[72:73], v[192:193], v[72:73] op_sel:[1,0]
	v_pk_mul_f32 v[74:75], v[192:193], v[74:75] op_sel:[1,0]
	v_pk_mul_f32 v[80:81], v[192:193], v[80:81] op_sel:[1,0]
	v_pk_mul_f32 v[82:83], v[192:193], v[82:83] op_sel:[1,0]
	v_pk_fma_f32 v[124:125], v[72:73], v[160:161], v[124:125]
	v_pk_fma_f32 v[126:127], v[74:75], v[162:163], v[126:127]
	v_pk_fma_f32 v[120:121], v[80:81], v[164:165], v[120:121]
	v_pk_fma_f32 v[122:123], v[82:83], v[166:167], v[122:123]
	v_cvt_pk_f16_f32 v124, v124, v125
	v_cvt_pk_f16_f32 v125, v126, v127
	v_cvt_pk_f16_f32 v126, v120, v121
	v_cvt_pk_f16_f32 v127, v122, v123
	s_waitcnt lgkmcnt(0)
	buffer_store_dwordx4 v[88:91], v224, s[24:27], 0 offen sc1
	v_add_u32_e32 v82, 0x3000, v224
	buffer_store_dwordx4 v[92:95], v82, s[24:27], 0 offen sc1
	ds_write_b128 v235, v[124:127]
	v_fma_mix_f32 v140, v124, 1.0, 0 op_sel_hi:[1,0,0]
	v_fma_mix_f32 v141, v124, v124, 0 op_sel_hi:[1,1,0]
	v_fma_mix_f32 v140, v124, 1.0, v140 op_sel:[1,0,0] op_sel_hi:[1,0,0]
	v_fma_mix_f32 v141, v124, v124, v141 op_sel:[1,1,0] op_sel_hi:[1,1,0]
	v_fma_mix_f32 v140, v125, 1.0, v140 op_sel_hi:[1,0,0]
	v_fma_mix_f32 v141, v125, v125, v141 op_sel_hi:[1,1,0]
	v_fma_mix_f32 v140, v125, 1.0, v140 op_sel:[1,0,0] op_sel_hi:[1,0,0]
	v_fma_mix_f32 v141, v125, v125, v141 op_sel:[1,1,0] op_sel_hi:[1,1,0]
	v_fma_mix_f32 v140, v126, 1.0, v140 op_sel_hi:[1,0,0]
	v_fma_mix_f32 v141, v126, v126, v141 op_sel_hi:[1,1,0]
	v_fma_mix_f32 v140, v126, 1.0, v140 op_sel:[1,0,0] op_sel_hi:[1,0,0]
	v_fma_mix_f32 v141, v126, v126, v141 op_sel:[1,1,0] op_sel_hi:[1,1,0]
	v_fma_mix_f32 v140, v127, 1.0, v140 op_sel_hi:[1,0,0]
	v_fma_mix_f32 v141, v127, v127, v141 op_sel_hi:[1,1,0]
	v_fma_mix_f32 v140, v127, 1.0, v140 op_sel:[1,0,0] op_sel_hi:[1,0,0]
	v_fma_mix_f32 v141, v127, v127, v141 op_sel:[1,1,0] op_sel_hi:[1,1,0]
	s_waitcnt vmcnt(10)
	v_cvt_f32_f16_e32 v72, v220
	v_cvt_f32_f16_sdwa v73, v220 dst_sel:DWORD dst_unused:UNUSED_PAD src0_sel:WORD_1
	v_cvt_f32_f16_e32 v74, v221
	v_cvt_f32_f16_sdwa v75, v221 dst_sel:DWORD dst_unused:UNUSED_PAD src0_sel:WORD_1
	v_cvt_f32_f16_e32 v80, v222
	v_cvt_f32_f16_sdwa v81, v222 dst_sel:DWORD dst_unused:UNUSED_PAD src0_sel:WORD_1
	v_cvt_f32_f16_e32 v82, v223
	v_cvt_f32_f16_sdwa v83, v223 dst_sel:DWORD dst_unused:UNUSED_PAD src0_sel:WORD_1
	v_sub_f32_e32 v72, v72, v192
	v_sub_f32_e32 v73, v73, v192
	v_sub_f32_e32 v74, v74, v192
	v_sub_f32_e32 v75, v75, v192
	v_sub_f32_e32 v80, v80, v192
	v_sub_f32_e32 v81, v81, v192
	v_sub_f32_e32 v82, v82, v192
	v_sub_f32_e32 v83, v83, v192
	v_pk_mul_f32 v[72:73], v[192:193], v[72:73] op_sel:[1,0]
	v_pk_mul_f32 v[74:75], v[192:193], v[74:75] op_sel:[1,0]
	v_pk_mul_f32 v[80:81], v[192:193], v[80:81] op_sel:[1,0]
	v_pk_mul_f32 v[82:83], v[192:193], v[82:83] op_sel:[1,0]
	v_pk_fma_f32 v[116:117], v[72:73], v[168:169], v[116:117]
	v_pk_fma_f32 v[118:119], v[74:75], v[170:171], v[118:119]
	v_pk_fma_f32 v[112:113], v[80:81], v[172:173], v[112:113]
	v_pk_fma_f32 v[114:115], v[82:83], v[174:175], v[114:115]
	v_cvt_pk_f16_f32 v116, v116, v117
	v_cvt_pk_f16_f32 v117, v118, v119
	v_cvt_pk_f16_f32 v118, v112, v113
	v_cvt_pk_f16_f32 v119, v114, v115
	ds_write_b128 v235, v[116:119] offset:64
	v_fma_mix_f32 v140, v116, 1.0, v140 op_sel_hi:[1,0,0]
	v_fma_mix_f32 v141, v116, v116, v141 op_sel_hi:[1,1,0]
	v_fma_mix_f32 v140, v116, 1.0, v140 op_sel:[1,0,0] op_sel_hi:[1,0,0]
	v_fma_mix_f32 v141, v116, v116, v141 op_sel:[1,1,0] op_sel_hi:[1,1,0]
	v_fma_mix_f32 v140, v117, 1.0, v140 op_sel_hi:[1,0,0]
	v_fma_mix_f32 v141, v117, v117, v141 op_sel_hi:[1,1,0]
	v_fma_mix_f32 v140, v117, 1.0, v140 op_sel:[1,0,0] op_sel_hi:[1,0,0]
	v_fma_mix_f32 v141, v117, v117, v141 op_sel:[1,1,0] op_sel_hi:[1,1,0]
	v_fma_mix_f32 v140, v118, 1.0, v140 op_sel_hi:[1,0,0]
	v_fma_mix_f32 v141, v118, v118, v141 op_sel_hi:[1,1,0]
	v_fma_mix_f32 v140, v118, 1.0, v140 op_sel:[1,0,0] op_sel_hi:[1,0,0]
	v_fma_mix_f32 v141, v118, v118, v141 op_sel:[1,1,0] op_sel_hi:[1,1,0]
	v_fma_mix_f32 v140, v119, 1.0, v140 op_sel_hi:[1,0,0]
	v_fma_mix_f32 v141, v119, v119, v141 op_sel_hi:[1,1,0]
	v_fma_mix_f32 v140, v119, 1.0, v140 op_sel:[1,0,0] op_sel_hi:[1,0,0]
	v_fma_mix_f32 v141, v119, v119, v141 op_sel:[1,1,0] op_sel_hi:[1,1,0]
	ds_read_b128 v[208:211], v236
	ds_read_b128 v[128:131], v236 offset:1152
	s_add_u32 s94, s98, 0x3c000
	s_addc_u32 s95, s99, 0
	global_load_dwordx4 v[212:215], v191, s[94:95] offset:0 nt
	global_load_dwordx4 v[144:147], v191, s[94:95] offset:64 nt
	s_add_u32 s94, s98, 0x42000
	s_addc_u32 s95, s99, 0
	global_load_dwordx4 v[132:135], v191, s[94:95] offset:0 nt
	global_load_dwordx4 v[88:91], v191, s[94:95] offset:64 nt
	s_waitcnt vmcnt(13)
	v_cvt_f32_f16_e32 v72, v240
	v_cvt_f32_f16_sdwa v73, v240 dst_sel:DWORD dst_unused:UNUSED_PAD src0_sel:WORD_1
	v_cvt_f32_f16_e32 v74, v241
	v_cvt_f32_f16_sdwa v75, v241 dst_sel:DWORD dst_unused:UNUSED_PAD src0_sel:WORD_1
	v_cvt_f32_f16_e32 v80, v242
	v_cvt_f32_f16_sdwa v81, v242 dst_sel:DWORD dst_unused:UNUSED_PAD src0_sel:WORD_1
	v_cvt_f32_f16_e32 v82, v243
	v_cvt_f32_f16_sdwa v83, v243 dst_sel:DWORD dst_unused:UNUSED_PAD src0_sel:WORD_1
	v_sub_f32_e32 v72, v72, v194
	v_sub_f32_e32 v73, v73, v194
	v_sub_f32_e32 v74, v74, v194
	v_sub_f32_e32 v75, v75, v194
	v_sub_f32_e32 v80, v80, v194
	v_sub_f32_e32 v81, v81, v194
	v_sub_f32_e32 v82, v82, v194
	v_sub_f32_e32 v83, v83, v194
	v_pk_mul_f32 v[72:73], v[194:195], v[72:73] op_sel:[1,0]
	v_pk_mul_f32 v[74:75], v[194:195], v[74:75] op_sel:[1,0]
	v_pk_mul_f32 v[80:81], v[194:195], v[80:81] op_sel:[1,0]
	v_pk_mul_f32 v[82:83], v[194:195], v[82:83] op_sel:[1,0]
	v_pk_fma_f32 v[108:109], v[72:73], v[160:161], v[108:109]
	v_pk_fma_f32 v[110:111], v[74:75], v[162:163], v[110:111]
	v_pk_fma_f32 v[104:105], v[80:81], v[164:165], v[104:105]
	v_pk_fma_f32 v[106:107], v[82:83], v[166:167], v[106:107]
	v_cvt_pk_f16_f32 v108, v108, v109
	v_cvt_pk_f16_f32 v109, v110, v111
	v_cvt_pk_f16_f32 v110, v104, v105
	v_cvt_pk_f16_f32 v111, v106, v107
	s_waitcnt lgkmcnt(0)
	v_add_u32_e32 v83, 0x6000, v224
	buffer_store_dwordx4 v[208:211], v83, s[24:27], 0 offen sc1
	v_add_u32_e32 v82, 0x9000, v224
	buffer_store_dwordx4 v[128:131], v82, s[24:27], 0 offen sc1
	ds_write_b128 v235, v[108:111]
	v_fma_mix_f32 v142, v108, 1.0, 0 op_sel_hi:[1,0,0]
	v_fma_mix_f32 v143, v108, v108, 0 op_sel_hi:[1,1,0]
	v_fma_mix_f32 v142, v108, 1.0, v142 op_sel:[1,0,0] op_sel_hi:[1,0,0]
	v_fma_mix_f32 v143, v108, v108, v143 op_sel:[1,1,0] op_sel_hi:[1,1,0]
	v_fma_mix_f32 v142, v109, 1.0, v142 op_sel_hi:[1,0,0]
	v_fma_mix_f32 v143, v109, v109, v143 op_sel_hi:[1,1,0]
	v_fma_mix_f32 v142, v109, 1.0, v142 op_sel:[1,0,0] op_sel_hi:[1,0,0]
	v_fma_mix_f32 v143, v109, v109, v143 op_sel:[1,1,0] op_sel_hi:[1,1,0]
	v_fma_mix_f32 v142, v110, 1.0, v142 op_sel_hi:[1,0,0]
	v_fma_mix_f32 v143, v110, v110, v143 op_sel_hi:[1,1,0]
	v_fma_mix_f32 v142, v110, 1.0, v142 op_sel:[1,0,0] op_sel_hi:[1,0,0]
	v_fma_mix_f32 v143, v110, v110, v143 op_sel:[1,1,0] op_sel_hi:[1,1,0]
	v_fma_mix_f32 v142, v111, 1.0, v142 op_sel_hi:[1,0,0]
	v_fma_mix_f32 v143, v111, v111, v143 op_sel_hi:[1,1,0]
	v_fma_mix_f32 v142, v111, 1.0, v142 op_sel:[1,0,0] op_sel_hi:[1,0,0]
	v_fma_mix_f32 v143, v111, v111, v143 op_sel:[1,1,0] op_sel_hi:[1,1,0]
	s_waitcnt vmcnt(14)
	v_cvt_f32_f16_e32 v72, v244
	v_cvt_f32_f16_sdwa v73, v244 dst_sel:DWORD dst_unused:UNUSED_PAD src0_sel:WORD_1
	v_cvt_f32_f16_e32 v74, v245
	v_cvt_f32_f16_sdwa v75, v245 dst_sel:DWORD dst_unused:UNUSED_PAD src0_sel:WORD_1
	v_cvt_f32_f16_e32 v80, v246
	v_cvt_f32_f16_sdwa v81, v246 dst_sel:DWORD dst_unused:UNUSED_PAD src0_sel:WORD_1
	v_cvt_f32_f16_e32 v82, v247
	v_cvt_f32_f16_sdwa v83, v247 dst_sel:DWORD dst_unused:UNUSED_PAD src0_sel:WORD_1
	v_sub_f32_e32 v72, v72, v194
	v_sub_f32_e32 v73, v73, v194
	v_sub_f32_e32 v74, v74, v194
	v_sub_f32_e32 v75, v75, v194
	v_sub_f32_e32 v80, v80, v194
	v_sub_f32_e32 v81, v81, v194
	v_sub_f32_e32 v82, v82, v194
	v_sub_f32_e32 v83, v83, v194
	v_pk_mul_f32 v[72:73], v[194:195], v[72:73] op_sel:[1,0]
	v_pk_mul_f32 v[74:75], v[194:195], v[74:75] op_sel:[1,0]
	v_pk_mul_f32 v[80:81], v[194:195], v[80:81] op_sel:[1,0]
	v_pk_mul_f32 v[82:83], v[194:195], v[82:83] op_sel:[1,0]
	v_pk_fma_f32 v[100:101], v[72:73], v[168:169], v[100:101]
	v_pk_fma_f32 v[102:103], v[74:75], v[170:171], v[102:103]
	v_pk_fma_f32 v[96:97], v[80:81], v[172:173], v[96:97]
	v_pk_fma_f32 v[98:99], v[82:83], v[174:175], v[98:99]
	v_cvt_pk_f16_f32 v100, v100, v101
	v_cvt_pk_f16_f32 v101, v102, v103
	v_cvt_pk_f16_f32 v102, v96, v97
	v_cvt_pk_f16_f32 v103, v98, v99
	ds_write_b128 v235, v[100:103] offset:64
	v_fma_mix_f32 v142, v100, 1.0, v142 op_sel_hi:[1,0,0]
	v_fma_mix_f32 v143, v100, v100, v143 op_sel_hi:[1,1,0]
	v_fma_mix_f32 v142, v100, 1.0, v142 op_sel:[1,0,0] op_sel_hi:[1,0,0]
	v_fma_mix_f32 v143, v100, v100, v143 op_sel:[1,1,0] op_sel_hi:[1,1,0]
	v_fma_mix_f32 v142, v101, 1.0, v142 op_sel_hi:[1,0,0]
	v_fma_mix_f32 v143, v101, v101, v143 op_sel_hi:[1,1,0]
	v_fma_mix_f32 v142, v101, 1.0, v142 op_sel:[1,0,0] op_sel_hi:[1,0,0]
	v_fma_mix_f32 v143, v101, v101, v143 op_sel:[1,1,0] op_sel_hi:[1,1,0]
	v_fma_mix_f32 v142, v102, 1.0, v142 op_sel_hi:[1,0,0]
	v_fma_mix_f32 v143, v102, v102, v143 op_sel_hi:[1,1,0]
	v_fma_mix_f32 v142, v102, 1.0, v142 op_sel:[1,0,0] op_sel_hi:[1,0,0]
	v_fma_mix_f32 v143, v102, v102, v143 op_sel:[1,1,0] op_sel_hi:[1,1,0]
	v_fma_mix_f32 v142, v103, 1.0, v142 op_sel_hi:[1,0,0]
	v_fma_mix_f32 v143, v103, v103, v143 op_sel_hi:[1,1,0]
	v_fma_mix_f32 v142, v103, 1.0, v142 op_sel:[1,0,0] op_sel_hi:[1,0,0]
	v_fma_mix_f32 v143, v103, v103, v143 op_sel:[1,1,0] op_sel_hi:[1,1,0]
	ds_read_b128 v[92:95], v236
	ds_read_b128 v[120:123], v236 offset:1152
	s_waitcnt vmcnt(13)
	v_cvt_f32_f16_e32 v72, v248
	v_cvt_f32_f16_sdwa v73, v248 dst_sel:DWORD dst_unused:UNUSED_PAD src0_sel:WORD_1
	v_cvt_f32_f16_e32 v74, v249
	v_cvt_f32_f16_sdwa v75, v249 dst_sel:DWORD dst_unused:UNUSED_PAD src0_sel:WORD_1
	v_cvt_f32_f16_e32 v80, v250
	v_cvt_f32_f16_sdwa v81, v250 dst_sel:DWORD dst_unused:UNUSED_PAD src0_sel:WORD_1
	v_cvt_f32_f16_e32 v82, v251
	v_cvt_f32_f16_sdwa v83, v251 dst_sel:DWORD dst_unused:UNUSED_PAD src0_sel:WORD_1
	v_sub_f32_e32 v72, v72, v196
	v_sub_f32_e32 v73, v73, v196
	v_sub_f32_e32 v74, v74, v196
	v_sub_f32_e32 v75, v75, v196
	v_sub_f32_e32 v80, v80, v196
	v_sub_f32_e32 v81, v81, v196
	v_sub_f32_e32 v82, v82, v196
	v_sub_f32_e32 v83, v83, v196
	v_pk_mul_f32 v[72:73], v[196:197], v[72:73] op_sel:[1,0]
	v_pk_mul_f32 v[74:75], v[196:197], v[74:75] op_sel:[1,0]
	v_pk_mul_f32 v[80:81], v[196:197], v[80:81] op_sel:[1,0]
	v_pk_mul_f32 v[82:83], v[196:197], v[82:83] op_sel:[1,0]
	v_pk_fma_f32 v[84:85], v[72:73], v[160:161], v[84:85]
	v_pk_fma_f32 v[86:87], v[74:75], v[162:163], v[86:87]
	v_pk_fma_f32 v[76:77], v[80:81], v[164:165], v[76:77]
	v_pk_fma_f32 v[78:79], v[82:83], v[166:167], v[78:79]
	v_cvt_pk_f16_f32 v84, v84, v85
	v_cvt_pk_f16_f32 v85, v86, v87
	v_cvt_pk_f16_f32 v86, v76, v77
	v_cvt_pk_f16_f32 v87, v78, v79
	s_waitcnt lgkmcnt(0)
	v_add_u32_e32 v83, 0xc000, v224
	buffer_store_dwordx4 v[92:95], v83, s[24:27], 0 offen sc1
	v_add_u32_e32 v82, 0xf000, v224
	buffer_store_dwordx4 v[120:123], v82, s[24:27], 0 offen sc1
	ds_write_b128 v235, v[84:87]
	v_fma_mix_f32 v216, v84, 1.0, 0 op_sel_hi:[1,0,0]
	v_fma_mix_f32 v217, v84, v84, 0 op_sel_hi:[1,1,0]
	v_fma_mix_f32 v216, v84, 1.0, v216 op_sel:[1,0,0] op_sel_hi:[1,0,0]
	v_fma_mix_f32 v217, v84, v84, v217 op_sel:[1,1,0] op_sel_hi:[1,1,0]
	v_fma_mix_f32 v216, v85, 1.0, v216 op_sel_hi:[1,0,0]
	v_fma_mix_f32 v217, v85, v85, v217 op_sel_hi:[1,1,0]
	v_fma_mix_f32 v216, v85, 1.0, v216 op_sel:[1,0,0] op_sel_hi:[1,0,0]
	v_fma_mix_f32 v217, v85, v85, v217 op_sel:[1,1,0] op_sel_hi:[1,1,0]
	v_fma_mix_f32 v216, v86, 1.0, v216 op_sel_hi:[1,0,0]
	v_fma_mix_f32 v217, v86, v86, v217 op_sel_hi:[1,1,0]
	v_fma_mix_f32 v216, v86, 1.0, v216 op_sel:[1,0,0] op_sel_hi:[1,0,0]
	v_fma_mix_f32 v217, v86, v86, v217 op_sel:[1,1,0] op_sel_hi:[1,1,0]
	v_fma_mix_f32 v216, v87, 1.0, v216 op_sel_hi:[1,0,0]
	v_fma_mix_f32 v217, v87, v87, v217 op_sel_hi:[1,1,0]
	v_fma_mix_f32 v216, v87, 1.0, v216 op_sel:[1,0,0] op_sel_hi:[1,0,0]
	v_fma_mix_f32 v217, v87, v87, v217 op_sel:[1,1,0] op_sel_hi:[1,1,0]
	s_waitcnt vmcnt(14)
	v_cvt_f32_f16_e32 v72, v252
	v_cvt_f32_f16_sdwa v73, v252 dst_sel:DWORD dst_unused:UNUSED_PAD src0_sel:WORD_1
	v_cvt_f32_f16_e32 v74, v253
	v_cvt_f32_f16_sdwa v75, v253 dst_sel:DWORD dst_unused:UNUSED_PAD src0_sel:WORD_1
	v_cvt_f32_f16_e32 v80, v254
	v_cvt_f32_f16_sdwa v81, v254 dst_sel:DWORD dst_unused:UNUSED_PAD src0_sel:WORD_1
	v_cvt_f32_f16_e32 v82, v255
	v_cvt_f32_f16_sdwa v83, v255 dst_sel:DWORD dst_unused:UNUSED_PAD src0_sel:WORD_1
	v_sub_f32_e32 v72, v72, v196
	v_sub_f32_e32 v73, v73, v196
	v_sub_f32_e32 v74, v74, v196
	v_sub_f32_e32 v75, v75, v196
	v_sub_f32_e32 v80, v80, v196
	v_sub_f32_e32 v81, v81, v196
	v_sub_f32_e32 v82, v82, v196
	v_sub_f32_e32 v83, v83, v196
	v_pk_mul_f32 v[72:73], v[196:197], v[72:73] op_sel:[1,0]
	v_pk_mul_f32 v[74:75], v[196:197], v[74:75] op_sel:[1,0]
	v_pk_mul_f32 v[80:81], v[196:197], v[80:81] op_sel:[1,0]
	v_pk_mul_f32 v[82:83], v[196:197], v[82:83] op_sel:[1,0]
	v_pk_fma_f32 v[68:69], v[72:73], v[168:169], v[68:69]
	v_pk_fma_f32 v[70:71], v[74:75], v[170:171], v[70:71]
	v_pk_fma_f32 v[64:65], v[80:81], v[172:173], v[64:65]
	v_pk_fma_f32 v[66:67], v[82:83], v[174:175], v[66:67]
	v_cvt_pk_f16_f32 v68, v68, v69
	v_cvt_pk_f16_f32 v69, v70, v71
	v_cvt_pk_f16_f32 v70, v64, v65
	v_cvt_pk_f16_f32 v71, v66, v67
	ds_write_b128 v235, v[68:71] offset:64
	v_fma_mix_f32 v216, v68, 1.0, v216 op_sel_hi:[1,0,0]
	v_fma_mix_f32 v217, v68, v68, v217 op_sel_hi:[1,1,0]
	v_fma_mix_f32 v216, v68, 1.0, v216 op_sel:[1,0,0] op_sel_hi:[1,0,0]
	v_fma_mix_f32 v217, v68, v68, v217 op_sel:[1,1,0] op_sel_hi:[1,1,0]
	v_fma_mix_f32 v216, v69, 1.0, v216 op_sel_hi:[1,0,0]
	v_fma_mix_f32 v217, v69, v69, v217 op_sel_hi:[1,1,0]
	v_fma_mix_f32 v216, v69, 1.0, v216 op_sel:[1,0,0] op_sel_hi:[1,0,0]
	v_fma_mix_f32 v217, v69, v69, v217 op_sel:[1,1,0] op_sel_hi:[1,1,0]
	v_fma_mix_f32 v216, v70, 1.0, v216 op_sel_hi:[1,0,0]
	v_fma_mix_f32 v217, v70, v70, v217 op_sel_hi:[1,1,0]
	v_fma_mix_f32 v216, v70, 1.0, v216 op_sel:[1,0,0] op_sel_hi:[1,0,0]
	v_fma_mix_f32 v217, v70, v70, v217 op_sel:[1,1,0] op_sel_hi:[1,1,0]
	v_fma_mix_f32 v216, v71, 1.0, v216 op_sel_hi:[1,0,0]
	v_fma_mix_f32 v217, v71, v71, v217 op_sel_hi:[1,1,0]
	v_fma_mix_f32 v216, v71, 1.0, v216 op_sel:[1,0,0] op_sel_hi:[1,0,0]
	v_fma_mix_f32 v217, v71, v71, v217 op_sel:[1,1,0] op_sel_hi:[1,1,0]
	ds_read_b128 v[112:115], v236
	ds_read_b128 v[220:223], v236 offset:1152
	s_waitcnt vmcnt(13)
	v_cvt_f32_f16_e32 v72, v136
	v_cvt_f32_f16_sdwa v73, v136 dst_sel:DWORD dst_unused:UNUSED_PAD src0_sel:WORD_1
	v_cvt_f32_f16_e32 v74, v137
	v_cvt_f32_f16_sdwa v75, v137 dst_sel:DWORD dst_unused:UNUSED_PAD src0_sel:WORD_1
	v_cvt_f32_f16_e32 v80, v138
	v_cvt_f32_f16_sdwa v81, v138 dst_sel:DWORD dst_unused:UNUSED_PAD src0_sel:WORD_1
	v_cvt_f32_f16_e32 v82, v139
	v_cvt_f32_f16_sdwa v83, v139 dst_sel:DWORD dst_unused:UNUSED_PAD src0_sel:WORD_1
	v_sub_f32_e32 v72, v72, v198
	v_sub_f32_e32 v73, v73, v198
	v_sub_f32_e32 v74, v74, v198
	v_sub_f32_e32 v75, v75, v198
	v_sub_f32_e32 v80, v80, v198
	v_sub_f32_e32 v81, v81, v198
	v_sub_f32_e32 v82, v82, v198
	v_sub_f32_e32 v83, v83, v198
	v_pk_mul_f32 v[72:73], v[198:199], v[72:73] op_sel:[1,0]
	v_pk_mul_f32 v[74:75], v[198:199], v[74:75] op_sel:[1,0]
	v_pk_mul_f32 v[80:81], v[198:199], v[80:81] op_sel:[1,0]
	v_pk_mul_f32 v[82:83], v[198:199], v[82:83] op_sel:[1,0]
	v_pk_fma_f32 v[60:61], v[72:73], v[160:161], v[60:61]
	v_pk_fma_f32 v[62:63], v[74:75], v[162:163], v[62:63]
	v_pk_fma_f32 v[56:57], v[80:81], v[164:165], v[56:57]
	v_pk_fma_f32 v[58:59], v[82:83], v[166:167], v[58:59]
	v_cvt_pk_f16_f32 v60, v60, v61
	v_cvt_pk_f16_f32 v61, v62, v63
	v_cvt_pk_f16_f32 v62, v56, v57
	v_cvt_pk_f16_f32 v63, v58, v59
	s_waitcnt lgkmcnt(0)
	v_add_u32_e32 v83, 0x12000, v224
	buffer_store_dwordx4 v[112:115], v83, s[24:27], 0 offen sc1
	v_add_u32_e32 v82, 0x15000, v224
	buffer_store_dwordx4 v[220:223], v82, s[24:27], 0 offen sc1
	ds_write_b128 v235, v[60:63]
	v_fma_mix_f32 v218, v60, 1.0, 0 op_sel_hi:[1,0,0]
	v_fma_mix_f32 v219, v60, v60, 0 op_sel_hi:[1,1,0]
	v_fma_mix_f32 v218, v60, 1.0, v218 op_sel:[1,0,0] op_sel_hi:[1,0,0]
	v_fma_mix_f32 v219, v60, v60, v219 op_sel:[1,1,0] op_sel_hi:[1,1,0]
	v_fma_mix_f32 v218, v61, 1.0, v218 op_sel_hi:[1,0,0]
	v_fma_mix_f32 v219, v61, v61, v219 op_sel_hi:[1,1,0]
	v_fma_mix_f32 v218, v61, 1.0, v218 op_sel:[1,0,0] op_sel_hi:[1,0,0]
	v_fma_mix_f32 v219, v61, v61, v219 op_sel:[1,1,0] op_sel_hi:[1,1,0]
	v_fma_mix_f32 v218, v62, 1.0, v218 op_sel_hi:[1,0,0]
	v_fma_mix_f32 v219, v62, v62, v219 op_sel_hi:[1,1,0]
	v_fma_mix_f32 v218, v62, 1.0, v218 op_sel:[1,0,0] op_sel_hi:[1,0,0]
	v_fma_mix_f32 v219, v62, v62, v219 op_sel:[1,1,0] op_sel_hi:[1,1,0]
	v_fma_mix_f32 v218, v63, 1.0, v218 op_sel_hi:[1,0,0]
	v_fma_mix_f32 v219, v63, v63, v219 op_sel_hi:[1,1,0]
	v_fma_mix_f32 v218, v63, 1.0, v218 op_sel:[1,0,0] op_sel_hi:[1,0,0]
	v_fma_mix_f32 v219, v63, v63, v219 op_sel:[1,1,0] op_sel_hi:[1,1,0]
	s_waitcnt vmcnt(14)
	v_cvt_f32_f16_e32 v72, v148
	v_cvt_f32_f16_sdwa v73, v148 dst_sel:DWORD dst_unused:UNUSED_PAD src0_sel:WORD_1
	v_cvt_f32_f16_e32 v74, v149
	v_cvt_f32_f16_sdwa v75, v149 dst_sel:DWORD dst_unused:UNUSED_PAD src0_sel:WORD_1
	v_cvt_f32_f16_e32 v80, v150
	v_cvt_f32_f16_sdwa v81, v150 dst_sel:DWORD dst_unused:UNUSED_PAD src0_sel:WORD_1
	v_cvt_f32_f16_e32 v82, v151
	v_cvt_f32_f16_sdwa v83, v151 dst_sel:DWORD dst_unused:UNUSED_PAD src0_sel:WORD_1
	v_sub_f32_e32 v72, v72, v198
	v_sub_f32_e32 v73, v73, v198
	v_sub_f32_e32 v74, v74, v198
	v_sub_f32_e32 v75, v75, v198
	v_sub_f32_e32 v80, v80, v198
	v_sub_f32_e32 v81, v81, v198
	v_sub_f32_e32 v82, v82, v198
	v_sub_f32_e32 v83, v83, v198
	v_pk_mul_f32 v[72:73], v[198:199], v[72:73] op_sel:[1,0]
	v_pk_mul_f32 v[74:75], v[198:199], v[74:75] op_sel:[1,0]
	v_pk_mul_f32 v[80:81], v[198:199], v[80:81] op_sel:[1,0]
	v_pk_mul_f32 v[82:83], v[198:199], v[82:83] op_sel:[1,0]
	v_pk_fma_f32 v[52:53], v[72:73], v[168:169], v[52:53]
	v_pk_fma_f32 v[54:55], v[74:75], v[170:171], v[54:55]
	v_pk_fma_f32 v[48:49], v[80:81], v[172:173], v[48:49]
	v_pk_fma_f32 v[50:51], v[82:83], v[174:175], v[50:51]
	v_cvt_pk_f16_f32 v52, v52, v53
	v_cvt_pk_f16_f32 v53, v54, v55
	v_cvt_pk_f16_f32 v54, v48, v49
	v_cvt_pk_f16_f32 v55, v50, v51
	ds_write_b128 v235, v[52:55] offset:64
	v_fma_mix_f32 v218, v52, 1.0, v218 op_sel_hi:[1,0,0]
	v_fma_mix_f32 v219, v52, v52, v219 op_sel_hi:[1,1,0]
	v_fma_mix_f32 v218, v52, 1.0, v218 op_sel:[1,0,0] op_sel_hi:[1,0,0]
	v_fma_mix_f32 v219, v52, v52, v219 op_sel:[1,1,0] op_sel_hi:[1,1,0]
	v_fma_mix_f32 v218, v53, 1.0, v218 op_sel_hi:[1,0,0]
	v_fma_mix_f32 v219, v53, v53, v219 op_sel_hi:[1,1,0]
	v_fma_mix_f32 v218, v53, 1.0, v218 op_sel:[1,0,0] op_sel_hi:[1,0,0]
	v_fma_mix_f32 v219, v53, v53, v219 op_sel:[1,1,0] op_sel_hi:[1,1,0]
	v_fma_mix_f32 v218, v54, 1.0, v218 op_sel_hi:[1,0,0]
	v_fma_mix_f32 v219, v54, v54, v219 op_sel_hi:[1,1,0]
	v_fma_mix_f32 v218, v54, 1.0, v218 op_sel:[1,0,0] op_sel_hi:[1,0,0]
	v_fma_mix_f32 v219, v54, v54, v219 op_sel:[1,1,0] op_sel_hi:[1,1,0]
	v_fma_mix_f32 v218, v55, 1.0, v218 op_sel_hi:[1,0,0]
	v_fma_mix_f32 v219, v55, v55, v219 op_sel_hi:[1,1,0]
	v_fma_mix_f32 v218, v55, 1.0, v218 op_sel:[1,0,0] op_sel_hi:[1,0,0]
	v_fma_mix_f32 v219, v55, v55, v219 op_sel:[1,1,0] op_sel_hi:[1,1,0]
	ds_read_b128 v[124:127], v236
	ds_read_b128 v[116:119], v236 offset:1152
	s_waitcnt vmcnt(13)
	v_cvt_f32_f16_e32 v72, v152
	v_cvt_f32_f16_sdwa v73, v152 dst_sel:DWORD dst_unused:UNUSED_PAD src0_sel:WORD_1
	v_cvt_f32_f16_e32 v74, v153
	v_cvt_f32_f16_sdwa v75, v153 dst_sel:DWORD dst_unused:UNUSED_PAD src0_sel:WORD_1
	v_cvt_f32_f16_e32 v80, v154
	v_cvt_f32_f16_sdwa v81, v154 dst_sel:DWORD dst_unused:UNUSED_PAD src0_sel:WORD_1
	v_cvt_f32_f16_e32 v82, v155
	v_cvt_f32_f16_sdwa v83, v155 dst_sel:DWORD dst_unused:UNUSED_PAD src0_sel:WORD_1
	v_sub_f32_e32 v72, v72, v200
	v_sub_f32_e32 v73, v73, v200
	v_sub_f32_e32 v74, v74, v200
	v_sub_f32_e32 v75, v75, v200
	v_sub_f32_e32 v80, v80, v200
	v_sub_f32_e32 v81, v81, v200
	v_sub_f32_e32 v82, v82, v200
	v_sub_f32_e32 v83, v83, v200
	v_pk_mul_f32 v[72:73], v[200:201], v[72:73] op_sel:[1,0]
	v_pk_mul_f32 v[74:75], v[200:201], v[74:75] op_sel:[1,0]
	v_pk_mul_f32 v[80:81], v[200:201], v[80:81] op_sel:[1,0]
	v_pk_mul_f32 v[82:83], v[200:201], v[82:83] op_sel:[1,0]
	v_pk_fma_f32 v[44:45], v[72:73], v[160:161], v[44:45]
	v_pk_fma_f32 v[46:47], v[74:75], v[162:163], v[46:47]
	v_pk_fma_f32 v[40:41], v[80:81], v[164:165], v[40:41]
	v_pk_fma_f32 v[42:43], v[82:83], v[166:167], v[42:43]
	v_cvt_pk_f16_f32 v44, v44, v45
	v_cvt_pk_f16_f32 v45, v46, v47
	v_cvt_pk_f16_f32 v46, v40, v41
	v_cvt_pk_f16_f32 v47, v42, v43
	s_waitcnt lgkmcnt(0)
	v_add_u32_e32 v83, 0x30000, v224
	buffer_store_dwordx4 v[124:127], v83, s[24:27], 0 offen sc1
	v_add_u32_e32 v82, 0x33000, v224
	buffer_store_dwordx4 v[116:119], v82, s[24:27], 0 offen sc1
	ds_write_b128 v235, v[44:47]
	v_fma_mix_f32 v208, v44, 1.0, 0 op_sel_hi:[1,0,0]
	v_fma_mix_f32 v209, v44, v44, 0 op_sel_hi:[1,1,0]
	v_fma_mix_f32 v208, v44, 1.0, v208 op_sel:[1,0,0] op_sel_hi:[1,0,0]
	v_fma_mix_f32 v209, v44, v44, v209 op_sel:[1,1,0] op_sel_hi:[1,1,0]
	v_fma_mix_f32 v208, v45, 1.0, v208 op_sel_hi:[1,0,0]
	v_fma_mix_f32 v209, v45, v45, v209 op_sel_hi:[1,1,0]
	v_fma_mix_f32 v208, v45, 1.0, v208 op_sel:[1,0,0] op_sel_hi:[1,0,0]
	v_fma_mix_f32 v209, v45, v45, v209 op_sel:[1,1,0] op_sel_hi:[1,1,0]
	v_fma_mix_f32 v208, v46, 1.0, v208 op_sel_hi:[1,0,0]
	v_fma_mix_f32 v209, v46, v46, v209 op_sel_hi:[1,1,0]
	v_fma_mix_f32 v208, v46, 1.0, v208 op_sel:[1,0,0] op_sel_hi:[1,0,0]
	v_fma_mix_f32 v209, v46, v46, v209 op_sel:[1,1,0] op_sel_hi:[1,1,0]
	v_fma_mix_f32 v208, v47, 1.0, v208 op_sel_hi:[1,0,0]
	v_fma_mix_f32 v209, v47, v47, v209 op_sel_hi:[1,1,0]
	v_fma_mix_f32 v208, v47, 1.0, v208 op_sel:[1,0,0] op_sel_hi:[1,0,0]
	v_fma_mix_f32 v209, v47, v47, v209 op_sel:[1,1,0] op_sel_hi:[1,1,0]
	s_waitcnt vmcnt(14)
	v_cvt_f32_f16_e32 v72, v156
	v_cvt_f32_f16_sdwa v73, v156 dst_sel:DWORD dst_unused:UNUSED_PAD src0_sel:WORD_1
	v_cvt_f32_f16_e32 v74, v157
	v_cvt_f32_f16_sdwa v75, v157 dst_sel:DWORD dst_unused:UNUSED_PAD src0_sel:WORD_1
	v_cvt_f32_f16_e32 v80, v158
	v_cvt_f32_f16_sdwa v81, v158 dst_sel:DWORD dst_unused:UNUSED_PAD src0_sel:WORD_1
	v_cvt_f32_f16_e32 v82, v159
	v_cvt_f32_f16_sdwa v83, v159 dst_sel:DWORD dst_unused:UNUSED_PAD src0_sel:WORD_1
	v_sub_f32_e32 v72, v72, v200
	v_sub_f32_e32 v73, v73, v200
	v_sub_f32_e32 v74, v74, v200
	v_sub_f32_e32 v75, v75, v200
	v_sub_f32_e32 v80, v80, v200
	v_sub_f32_e32 v81, v81, v200
	v_sub_f32_e32 v82, v82, v200
	v_sub_f32_e32 v83, v83, v200
	v_pk_mul_f32 v[72:73], v[200:201], v[72:73] op_sel:[1,0]
	v_pk_mul_f32 v[74:75], v[200:201], v[74:75] op_sel:[1,0]
	v_pk_mul_f32 v[80:81], v[200:201], v[80:81] op_sel:[1,0]
	v_pk_mul_f32 v[82:83], v[200:201], v[82:83] op_sel:[1,0]
	v_pk_fma_f32 v[36:37], v[72:73], v[168:169], v[36:37]
	v_pk_fma_f32 v[38:39], v[74:75], v[170:171], v[38:39]
	v_pk_fma_f32 v[32:33], v[80:81], v[172:173], v[32:33]
	v_pk_fma_f32 v[34:35], v[82:83], v[174:175], v[34:35]
	v_cvt_pk_f16_f32 v36, v36, v37
	v_cvt_pk_f16_f32 v37, v38, v39
	v_cvt_pk_f16_f32 v38, v32, v33
	v_cvt_pk_f16_f32 v39, v34, v35
	ds_write_b128 v235, v[36:39] offset:64
	v_fma_mix_f32 v208, v36, 1.0, v208 op_sel_hi:[1,0,0]
	v_fma_mix_f32 v209, v36, v36, v209 op_sel_hi:[1,1,0]
	v_fma_mix_f32 v208, v36, 1.0, v208 op_sel:[1,0,0] op_sel_hi:[1,0,0]
	v_fma_mix_f32 v209, v36, v36, v209 op_sel:[1,1,0] op_sel_hi:[1,1,0]
	v_fma_mix_f32 v208, v37, 1.0, v208 op_sel_hi:[1,0,0]
	v_fma_mix_f32 v209, v37, v37, v209 op_sel_hi:[1,1,0]
	v_fma_mix_f32 v208, v37, 1.0, v208 op_sel:[1,0,0] op_sel_hi:[1,0,0]
	v_fma_mix_f32 v209, v37, v37, v209 op_sel:[1,1,0] op_sel_hi:[1,1,0]
	v_fma_mix_f32 v208, v38, 1.0, v208 op_sel_hi:[1,0,0]
	v_fma_mix_f32 v209, v38, v38, v209 op_sel_hi:[1,1,0]
	v_fma_mix_f32 v208, v38, 1.0, v208 op_sel:[1,0,0] op_sel_hi:[1,0,0]
	v_fma_mix_f32 v209, v38, v38, v209 op_sel:[1,1,0] op_sel_hi:[1,1,0]
	v_fma_mix_f32 v208, v39, 1.0, v208 op_sel_hi:[1,0,0]
	v_fma_mix_f32 v209, v39, v39, v209 op_sel_hi:[1,1,0]
	v_fma_mix_f32 v208, v39, 1.0, v208 op_sel:[1,0,0] op_sel_hi:[1,0,0]
	v_fma_mix_f32 v209, v39, v39, v209 op_sel:[1,1,0] op_sel_hi:[1,1,0]
	ds_read_b128 v[128:131], v236
	ds_read_b128 v[104:107], v236 offset:1152
	s_waitcnt vmcnt(11)
	v_cvt_f32_f16_e32 v72, v212
	v_cvt_f32_f16_sdwa v73, v212 dst_sel:DWORD dst_unused:UNUSED_PAD src0_sel:WORD_1
	v_cvt_f32_f16_e32 v74, v213
	v_cvt_f32_f16_sdwa v75, v213 dst_sel:DWORD dst_unused:UNUSED_PAD src0_sel:WORD_1
	v_cvt_f32_f16_e32 v80, v214
	v_cvt_f32_f16_sdwa v81, v214 dst_sel:DWORD dst_unused:UNUSED_PAD src0_sel:WORD_1
	v_cvt_f32_f16_e32 v82, v215
	v_cvt_f32_f16_sdwa v83, v215 dst_sel:DWORD dst_unused:UNUSED_PAD src0_sel:WORD_1
	v_sub_f32_e32 v72, v72, v202
	v_sub_f32_e32 v73, v73, v202
	v_sub_f32_e32 v74, v74, v202
	v_sub_f32_e32 v75, v75, v202
	v_sub_f32_e32 v80, v80, v202
	v_sub_f32_e32 v81, v81, v202
	v_sub_f32_e32 v82, v82, v202
	v_sub_f32_e32 v83, v83, v202
	v_pk_mul_f32 v[72:73], v[202:203], v[72:73] op_sel:[1,0]
	v_pk_mul_f32 v[74:75], v[202:203], v[74:75] op_sel:[1,0]
	v_pk_mul_f32 v[80:81], v[202:203], v[80:81] op_sel:[1,0]
	v_pk_mul_f32 v[82:83], v[202:203], v[82:83] op_sel:[1,0]
	v_pk_fma_f32 v[28:29], v[72:73], v[160:161], v[28:29]
	v_pk_fma_f32 v[30:31], v[74:75], v[162:163], v[30:31]
	v_pk_fma_f32 v[24:25], v[80:81], v[164:165], v[24:25]
	v_pk_fma_f32 v[26:27], v[82:83], v[166:167], v[26:27]
	v_cvt_pk_f16_f32 v28, v28, v29
	v_cvt_pk_f16_f32 v29, v30, v31
	v_cvt_pk_f16_f32 v30, v24, v25
	v_cvt_pk_f16_f32 v31, v26, v27
	s_waitcnt lgkmcnt(0)
	v_add_u32_e32 v83, 0x36000, v224
	buffer_store_dwordx4 v[128:131], v83, s[24:27], 0 offen sc1
	v_add_u32_e32 v82, 0x39000, v224
	buffer_store_dwordx4 v[104:107], v82, s[24:27], 0 offen sc1
	ds_write_b128 v235, v[28:31]
	v_fma_mix_f32 v210, v28, 1.0, 0 op_sel_hi:[1,0,0]
	v_fma_mix_f32 v211, v28, v28, 0 op_sel_hi:[1,1,0]
	v_fma_mix_f32 v210, v28, 1.0, v210 op_sel:[1,0,0] op_sel_hi:[1,0,0]
	v_fma_mix_f32 v211, v28, v28, v211 op_sel:[1,1,0] op_sel_hi:[1,1,0]
	v_fma_mix_f32 v210, v29, 1.0, v210 op_sel_hi:[1,0,0]
	v_fma_mix_f32 v211, v29, v29, v211 op_sel_hi:[1,1,0]
	v_fma_mix_f32 v210, v29, 1.0, v210 op_sel:[1,0,0] op_sel_hi:[1,0,0]
	v_fma_mix_f32 v211, v29, v29, v211 op_sel:[1,1,0] op_sel_hi:[1,1,0]
	v_fma_mix_f32 v210, v30, 1.0, v210 op_sel_hi:[1,0,0]
	v_fma_mix_f32 v211, v30, v30, v211 op_sel_hi:[1,1,0]
	v_fma_mix_f32 v210, v30, 1.0, v210 op_sel:[1,0,0] op_sel_hi:[1,0,0]
	v_fma_mix_f32 v211, v30, v30, v211 op_sel:[1,1,0] op_sel_hi:[1,1,0]
	v_fma_mix_f32 v210, v31, 1.0, v210 op_sel_hi:[1,0,0]
	v_fma_mix_f32 v211, v31, v31, v211 op_sel_hi:[1,1,0]
	v_fma_mix_f32 v210, v31, 1.0, v210 op_sel:[1,0,0] op_sel_hi:[1,0,0]
	v_fma_mix_f32 v211, v31, v31, v211 op_sel:[1,1,0] op_sel_hi:[1,1,0]
	s_waitcnt vmcnt(12)
	v_cvt_f32_f16_e32 v72, v144
	v_cvt_f32_f16_sdwa v73, v144 dst_sel:DWORD dst_unused:UNUSED_PAD src0_sel:WORD_1
	v_cvt_f32_f16_e32 v74, v145
	v_cvt_f32_f16_sdwa v75, v145 dst_sel:DWORD dst_unused:UNUSED_PAD src0_sel:WORD_1
	v_cvt_f32_f16_e32 v80, v146
	v_cvt_f32_f16_sdwa v81, v146 dst_sel:DWORD dst_unused:UNUSED_PAD src0_sel:WORD_1
	v_cvt_f32_f16_e32 v82, v147
	v_cvt_f32_f16_sdwa v83, v147 dst_sel:DWORD dst_unused:UNUSED_PAD src0_sel:WORD_1
	v_sub_f32_e32 v72, v72, v202
	v_sub_f32_e32 v73, v73, v202
	v_sub_f32_e32 v74, v74, v202
	v_sub_f32_e32 v75, v75, v202
	v_sub_f32_e32 v80, v80, v202
	v_sub_f32_e32 v81, v81, v202
	v_sub_f32_e32 v82, v82, v202
	v_sub_f32_e32 v83, v83, v202
	v_pk_mul_f32 v[72:73], v[202:203], v[72:73] op_sel:[1,0]
	v_pk_mul_f32 v[74:75], v[202:203], v[74:75] op_sel:[1,0]
	v_pk_mul_f32 v[80:81], v[202:203], v[80:81] op_sel:[1,0]
	v_pk_mul_f32 v[82:83], v[202:203], v[82:83] op_sel:[1,0]
	v_pk_fma_f32 v[20:21], v[72:73], v[168:169], v[20:21]
	v_pk_fma_f32 v[22:23], v[74:75], v[170:171], v[22:23]
	v_pk_fma_f32 v[16:17], v[80:81], v[172:173], v[16:17]
	v_pk_fma_f32 v[18:19], v[82:83], v[174:175], v[18:19]
	v_cvt_pk_f16_f32 v20, v20, v21
	v_cvt_pk_f16_f32 v21, v22, v23
	v_cvt_pk_f16_f32 v22, v16, v17
	v_cvt_pk_f16_f32 v23, v18, v19
	ds_write_b128 v235, v[20:23] offset:64
	v_fma_mix_f32 v210, v20, 1.0, v210 op_sel_hi:[1,0,0]
	v_fma_mix_f32 v211, v20, v20, v211 op_sel_hi:[1,1,0]
	v_fma_mix_f32 v210, v20, 1.0, v210 op_sel:[1,0,0] op_sel_hi:[1,0,0]
	v_fma_mix_f32 v211, v20, v20, v211 op_sel:[1,1,0] op_sel_hi:[1,1,0]
	v_fma_mix_f32 v210, v21, 1.0, v210 op_sel_hi:[1,0,0]
	v_fma_mix_f32 v211, v21, v21, v211 op_sel_hi:[1,1,0]
	v_fma_mix_f32 v210, v21, 1.0, v210 op_sel:[1,0,0] op_sel_hi:[1,0,0]
	v_fma_mix_f32 v211, v21, v21, v211 op_sel:[1,1,0] op_sel_hi:[1,1,0]
	v_fma_mix_f32 v210, v22, 1.0, v210 op_sel_hi:[1,0,0]
	v_fma_mix_f32 v211, v22, v22, v211 op_sel_hi:[1,1,0]
	v_fma_mix_f32 v210, v22, 1.0, v210 op_sel:[1,0,0] op_sel_hi:[1,0,0]
	v_fma_mix_f32 v211, v22, v22, v211 op_sel:[1,1,0] op_sel_hi:[1,1,0]
	v_fma_mix_f32 v210, v23, 1.0, v210 op_sel_hi:[1,0,0]
	v_fma_mix_f32 v211, v23, v23, v211 op_sel_hi:[1,1,0]
	v_fma_mix_f32 v210, v23, 1.0, v210 op_sel:[1,0,0] op_sel_hi:[1,0,0]
	v_fma_mix_f32 v211, v23, v23, v211 op_sel:[1,1,0] op_sel_hi:[1,1,0]
	ds_read_b128 v[240:243], v236
	ds_read_b128 v[96:99], v236 offset:1152
	s_waitcnt vmcnt(11)
	v_cvt_f32_f16_e32 v72, v132
	v_cvt_f32_f16_sdwa v73, v132 dst_sel:DWORD dst_unused:UNUSED_PAD src0_sel:WORD_1
	v_cvt_f32_f16_e32 v74, v133
	v_cvt_f32_f16_sdwa v75, v133 dst_sel:DWORD dst_unused:UNUSED_PAD src0_sel:WORD_1
	v_cvt_f32_f16_e32 v80, v134
	v_cvt_f32_f16_sdwa v81, v134 dst_sel:DWORD dst_unused:UNUSED_PAD src0_sel:WORD_1
	v_cvt_f32_f16_e32 v82, v135
	v_cvt_f32_f16_sdwa v83, v135 dst_sel:DWORD dst_unused:UNUSED_PAD src0_sel:WORD_1
	v_sub_f32_e32 v72, v72, v204
	v_sub_f32_e32 v73, v73, v204
	v_sub_f32_e32 v74, v74, v204
	v_sub_f32_e32 v75, v75, v204
	v_sub_f32_e32 v80, v80, v204
	v_sub_f32_e32 v81, v81, v204
	v_sub_f32_e32 v82, v82, v204
	v_sub_f32_e32 v83, v83, v204
	v_pk_mul_f32 v[72:73], v[204:205], v[72:73] op_sel:[1,0]
	v_pk_mul_f32 v[74:75], v[204:205], v[74:75] op_sel:[1,0]
	v_pk_mul_f32 v[80:81], v[204:205], v[80:81] op_sel:[1,0]
	v_pk_mul_f32 v[82:83], v[204:205], v[82:83] op_sel:[1,0]
	v_pk_fma_f32 v[12:13], v[72:73], v[160:161], v[12:13]
	v_pk_fma_f32 v[14:15], v[74:75], v[162:163], v[14:15]
	v_pk_fma_f32 v[8:9], v[80:81], v[164:165], v[8:9]
	v_pk_fma_f32 v[10:11], v[82:83], v[166:167], v[10:11]
	v_cvt_pk_f16_f32 v12, v12, v13
	v_cvt_pk_f16_f32 v13, v14, v15
	v_cvt_pk_f16_f32 v14, v8, v9
	v_cvt_pk_f16_f32 v15, v10, v11
	s_waitcnt lgkmcnt(0)
	v_add_u32_e32 v83, 0x3c000, v224
	buffer_store_dwordx4 v[240:243], v83, s[24:27], 0 offen sc1
	v_add_u32_e32 v82, 0x3f000, v224
	buffer_store_dwordx4 v[96:99], v82, s[24:27], 0 offen sc1
	ds_write_b128 v235, v[12:15]
	v_fma_mix_f32 v244, v12, 1.0, 0 op_sel_hi:[1,0,0]
	v_fma_mix_f32 v245, v12, v12, 0 op_sel_hi:[1,1,0]
	v_fma_mix_f32 v244, v12, 1.0, v244 op_sel:[1,0,0] op_sel_hi:[1,0,0]
	v_fma_mix_f32 v245, v12, v12, v245 op_sel:[1,1,0] op_sel_hi:[1,1,0]
	v_fma_mix_f32 v244, v13, 1.0, v244 op_sel_hi:[1,0,0]
	v_fma_mix_f32 v245, v13, v13, v245 op_sel_hi:[1,1,0]
	v_fma_mix_f32 v244, v13, 1.0, v244 op_sel:[1,0,0] op_sel_hi:[1,0,0]
	v_fma_mix_f32 v245, v13, v13, v245 op_sel:[1,1,0] op_sel_hi:[1,1,0]
	v_fma_mix_f32 v244, v14, 1.0, v244 op_sel_hi:[1,0,0]
	v_fma_mix_f32 v245, v14, v14, v245 op_sel_hi:[1,1,0]
	v_fma_mix_f32 v244, v14, 1.0, v244 op_sel:[1,0,0] op_sel_hi:[1,0,0]
	v_fma_mix_f32 v245, v14, v14, v245 op_sel:[1,1,0] op_sel_hi:[1,1,0]
	v_fma_mix_f32 v244, v15, 1.0, v244 op_sel_hi:[1,0,0]
	v_fma_mix_f32 v245, v15, v15, v245 op_sel_hi:[1,1,0]
	v_fma_mix_f32 v244, v15, 1.0, v244 op_sel:[1,0,0] op_sel_hi:[1,0,0]
	v_fma_mix_f32 v245, v15, v15, v245 op_sel:[1,1,0] op_sel_hi:[1,1,0]
	s_waitcnt vmcnt(12)
	v_cvt_f32_f16_e32 v72, v88
	v_cvt_f32_f16_sdwa v73, v88 dst_sel:DWORD dst_unused:UNUSED_PAD src0_sel:WORD_1
	v_cvt_f32_f16_e32 v74, v89
	v_cvt_f32_f16_sdwa v75, v89 dst_sel:DWORD dst_unused:UNUSED_PAD src0_sel:WORD_1
	v_cvt_f32_f16_e32 v80, v90
	v_cvt_f32_f16_sdwa v81, v90 dst_sel:DWORD dst_unused:UNUSED_PAD src0_sel:WORD_1
	v_cvt_f32_f16_e32 v82, v91
	v_cvt_f32_f16_sdwa v83, v91 dst_sel:DWORD dst_unused:UNUSED_PAD src0_sel:WORD_1
	v_sub_f32_e32 v72, v72, v204
	v_sub_f32_e32 v73, v73, v204
	v_sub_f32_e32 v74, v74, v204
	v_sub_f32_e32 v75, v75, v204
	v_sub_f32_e32 v80, v80, v204
	v_sub_f32_e32 v81, v81, v204
	v_sub_f32_e32 v82, v82, v204
	v_sub_f32_e32 v83, v83, v204
	v_pk_mul_f32 v[72:73], v[204:205], v[72:73] op_sel:[1,0]
	v_pk_mul_f32 v[74:75], v[204:205], v[74:75] op_sel:[1,0]
	v_pk_mul_f32 v[80:81], v[204:205], v[80:81] op_sel:[1,0]
	v_pk_mul_f32 v[82:83], v[204:205], v[82:83] op_sel:[1,0]
	v_pk_fma_f32 v[4:5], v[72:73], v[168:169], v[4:5]
	v_pk_fma_f32 v[6:7], v[74:75], v[170:171], v[6:7]
	v_pk_fma_f32 v[0:1], v[80:81], v[172:173], v[0:1]
	v_pk_fma_f32 v[2:3], v[82:83], v[174:175], v[2:3]
	v_cvt_pk_f16_f32 v4, v4, v5
	v_cvt_pk_f16_f32 v5, v6, v7
	v_cvt_pk_f16_f32 v6, v0, v1
	v_cvt_pk_f16_f32 v7, v2, v3
	ds_write_b128 v235, v[4:7] offset:64
	v_fma_mix_f32 v244, v4, 1.0, v244 op_sel_hi:[1,0,0]
	v_fma_mix_f32 v245, v4, v4, v245 op_sel_hi:[1,1,0]
	v_fma_mix_f32 v244, v4, 1.0, v244 op_sel:[1,0,0] op_sel_hi:[1,0,0]
	v_fma_mix_f32 v245, v4, v4, v245 op_sel:[1,1,0] op_sel_hi:[1,1,0]
	v_fma_mix_f32 v244, v5, 1.0, v244 op_sel_hi:[1,0,0]
	v_fma_mix_f32 v245, v5, v5, v245 op_sel_hi:[1,1,0]
	v_fma_mix_f32 v244, v5, 1.0, v244 op_sel:[1,0,0] op_sel_hi:[1,0,0]
	v_fma_mix_f32 v245, v5, v5, v245 op_sel:[1,1,0] op_sel_hi:[1,1,0]
	v_fma_mix_f32 v244, v6, 1.0, v244 op_sel_hi:[1,0,0]
	v_fma_mix_f32 v245, v6, v6, v245 op_sel_hi:[1,1,0]
	v_fma_mix_f32 v244, v6, 1.0, v244 op_sel:[1,0,0] op_sel_hi:[1,0,0]
	v_fma_mix_f32 v245, v6, v6, v245 op_sel:[1,1,0] op_sel_hi:[1,1,0]
	v_fma_mix_f32 v244, v7, 1.0, v244 op_sel_hi:[1,0,0]
	v_fma_mix_f32 v245, v7, v7, v245 op_sel_hi:[1,1,0]
	v_fma_mix_f32 v244, v7, 1.0, v244 op_sel:[1,0,0] op_sel_hi:[1,0,0]
	v_fma_mix_f32 v245, v7, v7, v245 op_sel:[1,1,0] op_sel_hi:[1,1,0]
	ds_read_b128 v[108:111], v236
	ds_read_b128 v[100:103], v236 offset:1152
	s_waitcnt lgkmcnt(0)
	v_add_u32_e32 v83, 0x42000, v224
	buffer_store_dwordx4 v[108:111], v83, s[24:27], 0 offen sc1
	v_add_u32_e32 v82, 0x45000, v224
	buffer_store_dwordx4 v[100:103], v82, s[24:27], 0 offen sc1
	v_xor_b32_e32 v225, 16, v234
	v_lshlrev_b32_e32 v225, 2, v225
	v_xor_b32_e32 v246, 32, v234
	v_lshlrev_b32_e32 v246, 2, v246
	ds_bpermute_b32 v92, v225, v206
	ds_bpermute_b32 v93, v225, v207
	ds_bpermute_b32 v94, v225, v140
	ds_bpermute_b32 v95, v225, v141
	ds_bpermute_b32 v120, v225, v142
	ds_bpermute_b32 v121, v225, v143
	ds_bpermute_b32 v122, v225, v216
	ds_bpermute_b32 v123, v225, v217
	s_waitcnt lgkmcnt(0)
	v_pk_add_f32 v[206:207], v[206:207], v[92:93]
	v_pk_add_f32 v[140:141], v[140:141], v[94:95]
	v_pk_add_f32 v[142:143], v[142:143], v[120:121]
	v_pk_add_f32 v[216:217], v[216:217], v[122:123]
	ds_bpermute_b32 v92, v225, v218
	ds_bpermute_b32 v93, v225, v219
	ds_bpermute_b32 v94, v225, v208
	ds_bpermute_b32 v95, v225, v209
	ds_bpermute_b32 v120, v225, v210
	ds_bpermute_b32 v121, v225, v211
	ds_bpermute_b32 v122, v225, v244
	ds_bpermute_b32 v123, v225, v245
	s_waitcnt lgkmcnt(0)
	v_pk_add_f32 v[218:219], v[218:219], v[92:93]
	v_pk_add_f32 v[208:209], v[208:209], v[94:95]
	v_pk_add_f32 v[210:211], v[210:211], v[120:121]
	v_pk_add_f32 v[244:245], v[244:245], v[122:123]
	ds_bpermute_b32 v92, v246, v206
	ds_bpermute_b32 v93, v246, v207
	ds_bpermute_b32 v94, v246, v140
	ds_bpermute_b32 v95, v246, v141
	ds_bpermute_b32 v120, v246, v142
	ds_bpermute_b32 v121, v246, v143
	ds_bpermute_b32 v122, v246, v216
	ds_bpermute_b32 v123, v246, v217
	s_waitcnt lgkmcnt(0)
	v_pk_add_f32 v[206:207], v[206:207], v[92:93]
	v_pk_add_f32 v[140:141], v[140:141], v[94:95]
	v_pk_add_f32 v[142:143], v[142:143], v[120:121]
	v_pk_add_f32 v[216:217], v[216:217], v[122:123]
	ds_bpermute_b32 v92, v246, v218
	ds_bpermute_b32 v93, v246, v219
	ds_bpermute_b32 v94, v246, v208
	ds_bpermute_b32 v95, v246, v209
	ds_bpermute_b32 v120, v246, v210
	ds_bpermute_b32 v121, v246, v211
	ds_bpermute_b32 v122, v246, v244
	ds_bpermute_b32 v123, v246, v245
	s_waitcnt lgkmcnt(0)
	v_pk_add_f32 v[218:219], v[218:219], v[92:93]
	v_pk_add_f32 v[208:209], v[208:209], v[94:95]
	v_pk_add_f32 v[210:211], v[210:211], v[120:121]
	v_pk_add_f32 v[244:245], v[244:245], v[122:123]
	s_mov_b64 exec, 0xffff
	global_store_dwordx2 v190, v[206:207], s[100:101] offset:0
	global_store_dwordx2 v190, v[140:141], s[100:101] offset:128
	global_store_dwordx2 v190, v[142:143], s[100:101] offset:256
	global_store_dwordx2 v190, v[216:217], s[100:101] offset:384
	global_store_dwordx2 v190, v[218:219], s[100:101] offset:1024
	global_store_dwordx2 v190, v[208:209], s[100:101] offset:1152
	global_store_dwordx2 v190, v[210:211], s[100:101] offset:1280
	global_store_dwordx2 v190, v[244:245], s[100:101] offset:1408
	s_mov_b64 exec, -1
	s_mov_b32 s83, s81
	s_mov_b32 s84, s82
	s_mov_b64 s[40:41], s[0:1]
	s_mov_b64 s[38:39], s[8:9]
	s_mov_b64 vcc, s[6:7]
	s_cbranch_vccz .LBB10_12
	s_waitcnt vmcnt(0)
	s_cmpk_gt_u32 s44, 0xff
	s_cbranch_scc1 .LBB10_31
	s_barrier
